# v18 plus the 181 inter-block s_nop 0 after LDS-DMA loads removed (they followed the deleted m0 restores)
# baseline (speedup 1.0000x reference)
.LBB0_249:
	v_bfe_i32 v3, v0, 27, 1
	v_lshlrev_b32_e32 v1, 4, v0
	v_lshrrev_b32_e32 v3, 22, v3
	v_add_u32_e32 v3, v1, v3
	v_and_b32_e32 v3, 0xfffffc00, v3
	v_sub_u32_e32 v3, v1, v3
	v_ashrrev_i32_e32 v2, 31, v0
	v_lshrrev_b32_e32 v4, 4, v3
	v_lshrrev_b32_e32 v2, 26, v2
	v_bitop3_b32 v3, v4, v3, 32 bitop3:0x6c
	v_add_u32_e32 v2, v0, v2
	v_ashrrev_i32_e32 v5, 31, v3
	v_ashrrev_i32_e32 v2, 6, v2
	v_lshrrev_b32_e32 v5, 26, v5
	v_lshlrev_b32_e32 v4, 3, v2
	v_add_u32_e32 v5, v3, v5
	v_and_b32_e32 v4, -16, v4
	v_ashrrev_i32_e32 v6, 6, v5
	v_and_b32_e32 v5, 0xc0, v5
	v_add_u32_e32 v4, v6, v4
	v_sub_u32_e32 v3, v3, v5
	v_mov_b32_e32 v5, 1
	v_lshlrev_b32_e32 v2, 5, v2
	v_ashrrev_i16_sdwa v3, v5, sext(v3) dst_sel:DWORD dst_unused:UNUSED_PAD src0_sel:DWORD src1_sel:BYTE_0
	v_lshlrev_b32_e32 v7, 1, v4
	s_waitcnt vmcnt(3)
	v_lshrrev_b32_e32 v8, 2, v4
	v_and_b32_e32 v6, 3, v6
	s_mov_b32 s5, 0x1fffe0
	v_and_b32_e32 v2, 32, v2
	v_bfe_i32 v3, v3, 0, 16
	v_and_b32_e32 v7, 24, v7
	v_and_b32_e32 v8, 4, v8
	v_and_or_b32 v6, v4, s5, v6
	v_or3_b32 v6, v6, v8, v7
	v_add_lshl_u32 v2, v2, v3, 1
	v_add_u32_e32 v1, 0x2000, v1
	v_lshl_add_u32 v215, v4, 11, v2
	v_lshl_add_u32 v216, v6, 11, v2
	v_ashrrev_i32_e32 v2, 31, v1
	v_lshrrev_b32_e32 v2, 22, v2
	v_add_u32_e32 v2, v1, v2
	v_ashrrev_i32_e32 v2, 10, v2
	v_mul_i32_i24_e32 v3, 0x400, v2
	v_sub_u32_e32 v1, v1, v3
	v_lshrrev_b32_e32 v3, 4, v1
	v_bitop3_b32 v1, v3, v1, 32 bitop3:0x6c
	v_ashrrev_i32_e32 v4, 31, v1
	v_lshrrev_b32_e32 v4, 26, v4
	s_add_u32 s54, s70, 0x42800000
	v_lshlrev_b32_e32 v3, 3, v2
	v_add_u32_e32 v4, v1, v4
	s_addc_u32 s55, s71, 0
	v_and_b32_e32 v3, -16, v3
	v_ashrrev_i32_e32 v6, 6, v4
	s_add_u32 s56, s70, 0x600000
	v_add_u32_e32 v3, v6, v3
	v_and_b32_e32 v6, 3, v6
	s_addc_u32 s57, s71, 0
	v_and_or_b32 v6, v3, s5, v6
	s_lshl_b32 s5, s29, 10
	s_ashr_i32 s11, s10, 31
	s_ashr_i32 s4, s28, 8
	s_add_i32 s59, s5, 0
	s_lshl_b64 s[8:9], s[10:11], 19
	v_and_b32_e32 v4, 0xc0, v4
	s_add_u32 s12, s54, s8
	v_sub_u32_e32 v1, v1, v4
	s_addc_u32 s13, s55, s9
	s_ashr_i32 s7, s6, 31
	v_lshlrev_b32_e32 v2, 5, v2
	v_ashrrev_i16_sdwa v1, v5, sext(v1) dst_sel:DWORD dst_unused:UNUSED_PAD src0_sel:DWORD src1_sel:BYTE_0
	v_lshlrev_b32_e32 v4, 1, v3
	v_lshrrev_b32_e32 v5, 2, v3
	s_lshl_b64 s[8:9], s[6:7], 19
	v_and_b32_e32 v2, 32, v2
	v_bfe_i32 v1, v1, 0, 16
	v_and_b32_e32 v4, 24, v4
	v_and_b32_e32 v5, 4, v5
	s_add_u32 s8, s56, s8
	v_or3_b32 v4, v6, v5, v4
	v_add_lshl_u32 v1, v2, v1, 1
	s_addc_u32 s9, s57, s9
	s_add_i32 m0, s59, 0x10000
	s_nop 0
	global_load_lds_dwordx4 v216, s[8:9]
	v_lshl_add_u32 v218, v4, 11, v1
	s_add_i32 m0, s59, 0x12000
	s_nop 0
	global_load_lds_dwordx4 v218, s[8:9]
	s_add_u32 s14, s8, 0x40000
	s_addc_u32 s15, s9, 0
	s_add_i32 m0, s59, 0x14000
	s_nop 0
	global_load_lds_dwordx4 v216, s[14:15]
	v_lshl_add_u32 v217, v3, 11, v1
	s_add_i32 m0, s59, 0x16000
	s_nop 0
	global_load_lds_dwordx4 v218, s[14:15]
	s_mov_b32 s58, 0
	s_add_i32 m0, s59, 0
	s_nop 0
	global_load_lds_dwordx4 v215, s[12:13]
	s_mov_b64 s[16:17], 0x40000
	s_add_i32 m0, s59, 0x2000
	s_nop 0
	global_load_lds_dwordx4 v217, s[12:13]
	s_add_u32 s14, s12, 0x40000
	s_addc_u32 s15, s13, 0
	s_add_i32 m0, s59, 0x4000
	s_nop 0
	global_load_lds_dwordx4 v215, s[14:15]
	s_add_i32 m0, s59, 0x6000
	s_nop 0
	global_load_lds_dwordx4 v217, s[14:15]
	s_cmp_eq_u32 s4, 1
	s_cselect_b64 s[14:15], -1, 0
	s_cmp_lg_u32 s4, 1
	s_cbranch_scc1 .LBB0_251
	s_barrier

.LBB0_260:
	s_ashr_i32 s41, s40, 31
	s_lshl_b64 s[42:43], s[40:41], 19
	s_add_u32 s42, s54, s42
	s_addc_u32 s43, s55, s43
	s_and_b64 s[44:45], s[4:5], exec
	ds_read_b128 v[0:3], v219
	ds_read_b128 v[4:7], v219 offset:1024
	ds_read_b128 v[8:11], v219 offset:2048
	s_waitcnt vmcnt(2)
	ds_read_b128 v[12:15], v219 offset:3072
	s_waitcnt vmcnt(1)
	ds_read_b128 v[16:19], v220
	s_waitcnt vmcnt(0)
	ds_read_b128 v[20:23], v220 offset:1024
	ds_read_b128 v[24:27], v220 offset:2048
	ds_read_b128 v[28:31], v220 offset:3072
	s_cselect_b32 s7, s43, s13
	s_cselect_b32 s11, s42, s12
	s_ashr_i32 s39, s38, 31
	s_lshl_b64 s[44:45], s[38:39], 19
	s_add_u32 s44, s56, s44
	s_addc_u32 s45, s57, s45
	s_and_b64 s[46:47], s[4:5], exec
	s_cselect_b32 s39, s45, s9
	s_cselect_b32 s41, s44, s8
	s_add_u32 s46, s12, 0x100
	s_addc_u32 s47, s13, 0
	s_add_u32 s52, s8, 0x100
	s_addc_u32 s53, s9, 0
	s_add_u32 s48, s12, 0x180
	s_addc_u32 s49, s13, 0
	ds_read_b128 v[32:35], v221
	ds_read_b128 v[36:39], v221 offset:1024
	ds_read_b128 v[40:43], v221 offset:2048
	ds_read_b128 v[44:47], v221 offset:3072
	ds_read_b128 v[48:51], v221 offset:4096
	ds_read_b128 v[52:55], v221 offset:5120
	ds_read_b128 v[56:59], v221 offset:6144
	ds_read_b128 v[60:63], v221 offset:7168
	s_add_u32 s50, s8, 0x180
	s_addc_u32 s51, s9, 0
	s_add_u32 s76, s12, 0x40080
	s_addc_u32 s77, s13, 0
	s_add_i32 m0, s59, 0xc000
	s_nop 0
	global_load_lds_dwordx4 v215, s[76:77]
	s_add_i32 m0, s59, 0xe000
	s_nop 0
	global_load_lds_dwordx4 v217, s[76:77]
	s_waitcnt vmcnt(8) lgkmcnt(0)
	s_barrier
	s_waitcnt lgkmcnt(7)
	v_mfma_i32_16x16x64_i8 v[64:67], v[0:3], v[32:35], 0
	s_mov_b32 s76, 0
	v_mfma_i32_16x16x64_i8 v[68:71], v[8:11], v[32:35], 0
	s_waitcnt lgkmcnt(5)
	v_mfma_i32_16x16x64_i8 v[72:75], v[0:3], v[40:43], 0
	v_mfma_i32_16x16x64_i8 v[76:79], v[8:11], v[40:43], 0
	s_waitcnt lgkmcnt(3)
	v_mfma_i32_16x16x64_i8 v[84:87], v[8:11], v[48:51], 0
	s_waitcnt lgkmcnt(1)
	v_mfma_i32_16x16x64_i8 v[88:91], v[0:3], v[56:59], 0
	v_mfma_i32_16x16x64_i8 v[140:143], v[4:7], v[36:39], v[64:67]
	v_mfma_i32_16x16x64_i8 v[144:147], v[12:15], v[36:39], v[68:71]
	v_mfma_i32_16x16x64_i8 v[152:155], v[4:7], v[44:47], v[72:75]
	v_mfma_i32_16x16x64_i8 v[156:159], v[12:15], v[44:47], v[76:79]
	v_mfma_i32_16x16x64_i8 v[80:83], v[0:3], v[48:51], 0
	v_mfma_i32_16x16x64_i8 v[84:87], v[12:15], v[52:55], v[84:87]
	s_waitcnt lgkmcnt(0)
	v_mfma_i32_16x16x64_i8 v[88:91], v[4:7], v[60:63], v[88:91]
	v_mfma_i32_16x16x64_i8 v[92:95], v[8:11], v[56:59], 0
	v_mfma_i32_16x16x64_i8 v[80:83], v[4:7], v[52:55], v[80:83]
	v_mfma_i32_16x16x64_i8 v[92:95], v[12:15], v[60:63], v[92:95]
	v_mfma_i32_16x16x64_i8 v[96:99], v[16:19], v[32:35], 0
	v_mfma_i32_16x16x64_i8 v[32:35], v[24:27], v[32:35], 0
	v_mfma_i32_16x16x64_i8 v[96:99], v[20:23], v[36:39], v[96:99]
	v_mfma_i32_16x16x64_i8 v[32:35], v[28:31], v[36:39], v[32:35]
	v_mfma_i32_16x16x64_i8 v[36:39], v[16:19], v[40:43], 0
	v_mfma_i32_16x16x64_i8 v[40:43], v[24:27], v[40:43], 0
	v_mfma_i32_16x16x64_i8 v[36:39], v[20:23], v[44:47], v[36:39]
	v_mfma_i32_16x16x64_i8 v[40:43], v[28:31], v[44:47], v[40:43]
	v_mfma_i32_16x16x64_i8 v[44:47], v[16:19], v[48:51], 0
	v_mfma_i32_16x16x64_i8 v[48:51], v[24:27], v[48:51], 0
	v_mfma_i32_16x16x64_i8 v[44:47], v[20:23], v[52:55], v[44:47]
	v_mfma_i32_16x16x64_i8 v[48:51], v[28:31], v[52:55], v[48:51]
	v_mfma_i32_16x16x64_i8 v[52:55], v[16:19], v[56:59], 0
	v_mfma_i32_16x16x64_i8 v[56:59], v[24:27], v[56:59], 0
	v_mfma_i32_16x16x64_i8 v[52:55], v[20:23], v[60:63], v[52:55]
	v_mfma_i32_16x16x64_i8 v[56:59], v[28:31], v[60:63], v[56:59]
	s_barrier
	ds_read_b128 v[60:63], v221 offset:16384
	ds_read_b128 v[100:103], v221 offset:17408
	ds_read_b128 v[104:107], v221 offset:18432
	ds_read_b128 v[108:111], v221 offset:19456
	ds_read_b128 v[112:115], v221 offset:20480
	ds_read_b128 v[116:119], v221 offset:21504
	ds_read_b128 v[120:123], v221 offset:22528
	ds_read_b128 v[124:127], v221 offset:23552
	s_add_i32 m0, s59, 0x10000
	s_nop 0
	global_load_lds_dwordx4 v216, s[52:53]
	s_add_i32 m0, s59, 0x12000
	s_nop 0
	global_load_lds_dwordx4 v218, s[52:53]
	s_add_u32 s52, s8, 0x40100
	s_addc_u32 s53, s9, 0
	s_add_i32 m0, s59, 0x14000
	s_nop 0
	global_load_lds_dwordx4 v216, s[52:53]
	s_add_i32 m0, s59, 0x16000
	s_nop 0
	global_load_lds_dwordx4 v218, s[52:53]
	s_add_i32 m0, s59, 0
	s_nop 0
	global_load_lds_dwordx4 v215, s[46:47]
	s_add_i32 m0, s59, 0x2000
	s_nop 0
	global_load_lds_dwordx4 v217, s[46:47]
	s_waitcnt vmcnt(8) lgkmcnt(0)
	s_barrier
	v_mfma_i32_16x16x64_i8 v[136:139], v[0:3], v[104:107], 0
	v_mfma_i32_16x16x64_i8 v[228:231], v[4:7], v[108:111], v[136:139]
	v_mfma_i32_16x16x64_i8 v[136:139], v[8:11], v[104:107], 0
	v_mfma_i32_16x16x64_i8 v[128:131], v[0:3], v[60:63], 0
	v_mfma_i32_16x16x64_i8 v[132:135], v[8:11], v[60:63], 0
	v_mfma_i32_16x16x64_i8 v[232:235], v[12:15], v[108:111], v[136:139]
	v_mfma_i32_16x16x64_i8 v[136:139], v[0:3], v[112:115], 0
	v_mfma_i32_16x16x64_i8 v[0:3], v[0:3], v[120:123], 0
	v_mfma_i32_16x16x64_i8 v[128:131], v[4:7], v[100:103], v[128:131]
	v_mfma_i32_16x16x64_i8 v[132:135], v[12:15], v[100:103], v[132:135]
	v_mfma_i32_16x16x64_i8 v[236:239], v[4:7], v[116:119], v[136:139]
	v_mfma_i32_16x16x64_i8 v[136:139], v[8:11], v[112:115], 0
	v_mfma_i32_16x16x64_i8 v[0:3], v[4:7], v[124:127], v[0:3]
	v_mfma_i32_16x16x64_i8 v[4:7], v[8:11], v[120:123], 0
	v_mfma_i32_16x16x64_i8 v[240:243], v[12:15], v[116:119], v[136:139]
	v_mfma_i32_16x16x64_i8 v[4:7], v[12:15], v[124:127], v[4:7]
	v_mfma_i32_16x16x64_i8 v[8:11], v[16:19], v[60:63], 0
	v_mfma_i32_16x16x64_i8 v[12:15], v[24:27], v[60:63], 0
	v_mfma_i32_16x16x64_i8 v[8:11], v[20:23], v[100:103], v[8:11]
	v_mfma_i32_16x16x64_i8 v[12:15], v[28:31], v[100:103], v[12:15]
	v_mfma_i32_16x16x64_i8 v[60:63], v[16:19], v[104:107], 0
	v_mfma_i32_16x16x64_i8 v[100:103], v[24:27], v[104:107], 0
	v_mfma_i32_16x16x64_i8 v[104:107], v[16:19], v[112:115], 0
	v_mfma_i32_16x16x64_i8 v[16:19], v[16:19], v[120:123], 0
	v_mfma_i32_16x16x64_i8 v[60:63], v[20:23], v[108:111], v[60:63]
	v_mfma_i32_16x16x64_i8 v[100:103], v[28:31], v[108:111], v[100:103]
	v_mfma_i32_16x16x64_i8 v[244:247], v[20:23], v[116:119], v[104:107]
	v_mfma_i32_16x16x64_i8 v[104:107], v[24:27], v[112:115], 0
	v_mfma_i32_16x16x64_i8 v[16:19], v[20:23], v[124:127], v[16:19]
	v_mfma_i32_16x16x64_i8 v[20:23], v[24:27], v[120:123], 0
	v_mfma_i32_16x16x64_i8 v[248:251], v[28:31], v[116:119], v[104:107]
	v_mfma_i32_16x16x64_i8 v[20:23], v[28:31], v[124:127], v[20:23]
	s_barrier
	ds_read_b128 v[24:27], v222
	ds_read_b128 v[28:31], v222 offset:1024
	ds_read_b128 v[112:115], v222 offset:2048
	ds_read_b128 v[116:119], v222 offset:3072
	ds_read_b128 v[208:211], v223
	ds_read_b128 v[224:227], v223 offset:1024
	ds_read_b128 v[64:67], v223 offset:2048
	ds_read_b128 v[68:71], v223 offset:3072
	ds_read_b128 v[104:107], v221 offset:32768
	ds_read_b128 v[108:111], v221 offset:33792
	ds_read_b128 v[120:123], v221 offset:34816
	ds_read_b128 v[124:127], v221 offset:35840
	ds_read_b128 v[136:139], v221 offset:36864
	ds_read_b128 v[148:151], v221 offset:37888
	ds_read_b128 v[72:75], v221 offset:38912
	ds_read_b128 v[76:79], v221 offset:39936
	s_add_u32 s12, s12, 0x40100
	s_addc_u32 s13, s13, 0
	s_add_i32 m0, s59, 0x4000
	s_nop 0
	global_load_lds_dwordx4 v215, s[12:13]
	s_add_i32 m0, s59, 0x6000
	s_nop 0
	global_load_lds_dwordx4 v217, s[12:13]
	s_waitcnt vmcnt(8) lgkmcnt(0)
	s_barrier
	v_mfma_i32_16x16x64_i8 v[140:143], v[24:27], v[104:107], v[140:143]
	v_mfma_i32_16x16x64_i8 v[80:83], v[24:27], v[136:139], v[80:83]
	v_mfma_i32_16x16x64_i8 v[204:207], v[28:31], v[108:111], v[140:143]
	v_mfma_i32_16x16x64_i8 v[140:143], v[112:115], v[104:107], v[144:147]
	v_mfma_i32_16x16x64_i8 v[172:175], v[28:31], v[148:151], v[80:83]
	v_mfma_i32_16x16x64_i8 v[80:83], v[112:115], v[136:139], v[84:87]
	v_mfma_i32_16x16x64_i8 v[200:203], v[116:119], v[108:111], v[140:143]
	v_mfma_i32_16x16x64_i8 v[140:143], v[24:27], v[120:123], v[152:155]
	v_mfma_i32_16x16x64_i8 v[168:171], v[116:119], v[148:151], v[80:83]
	v_mfma_i32_16x16x64_i8 v[80:83], v[24:27], v[72:75], v[88:91]
	v_mfma_i32_16x16x64_i8 v[188:191], v[28:31], v[124:127], v[140:143]
	v_mfma_i32_16x16x64_i8 v[140:143], v[112:115], v[120:123], v[156:159]
	v_mfma_i32_16x16x64_i8 v[156:159], v[28:31], v[76:79], v[80:83]
	v_mfma_i32_16x16x64_i8 v[80:83], v[112:115], v[72:75], v[92:95]
	v_mfma_i32_16x16x64_i8 v[184:187], v[116:119], v[124:127], v[140:143]
	v_mfma_i32_16x16x64_i8 v[152:155], v[116:119], v[76:79], v[80:83]
	v_mfma_i32_16x16x64_i8 v[32:35], v[64:67], v[104:107], v[32:35]
	v_mfma_i32_16x16x64_i8 v[192:195], v[68:71], v[108:111], v[32:35]
	v_mfma_i32_16x16x64_i8 v[32:35], v[208:211], v[120:123], v[36:39]
	v_mfma_i32_16x16x64_i8 v[180:183], v[224:227], v[124:127], v[32:35]
	v_mfma_i32_16x16x64_i8 v[32:35], v[64:67], v[120:123], v[40:43]
	v_mfma_i32_16x16x64_i8 v[176:179], v[68:71], v[124:127], v[32:35]
	v_mfma_i32_16x16x64_i8 v[32:35], v[208:211], v[136:139], v[44:47]
	v_mfma_i32_16x16x64_i8 v[164:167], v[224:227], v[148:151], v[32:35]
	v_mfma_i32_16x16x64_i8 v[32:35], v[64:67], v[136:139], v[48:51]
	v_mfma_i32_16x16x64_i8 v[160:163], v[68:71], v[148:151], v[32:35]
	v_mfma_i32_16x16x64_i8 v[32:35], v[208:211], v[72:75], v[52:55]
	v_mfma_i32_16x16x64_i8 v[80:83], v[208:211], v[104:107], v[96:99]
	v_mfma_i32_16x16x64_i8 v[148:151], v[224:227], v[76:79], v[32:35]
	v_mfma_i32_16x16x64_i8 v[32:35], v[64:67], v[72:75], v[56:59]
	v_mfma_i32_16x16x64_i8 v[196:199], v[224:227], v[108:111], v[80:83]
	v_mfma_i32_16x16x64_i8 v[144:147], v[68:71], v[76:79], v[32:35]
	s_barrier
	s_nop 3
	ds_read_b128 v[32:35], v221 offset:49152
	ds_read_b128 v[36:39], v221 offset:50176
	ds_read_b128 v[40:43], v221 offset:51200
	ds_read_b128 v[44:47], v221 offset:52224
	ds_read_b128 v[48:51], v221 offset:53248
	ds_read_b128 v[52:55], v221 offset:54272
	ds_read_b128 v[56:59], v221 offset:55296
	ds_read_b128 v[76:79], v221 offset:56320
	s_add_i32 m0, s59, 0x18000
	s_nop 0
	global_load_lds_dwordx4 v216, s[50:51]
	s_add_i32 m0, s59, 0x1a000
	s_nop 0
	global_load_lds_dwordx4 v218, s[50:51]
	s_add_u32 s12, s8, 0x40180
	s_addc_u32 s13, s9, 0
	s_add_i32 m0, s59, 0x1c000
	s_nop 0
	global_load_lds_dwordx4 v216, s[12:13]
	s_add_i32 m0, s59, 0x1e000
	s_nop 0
	global_load_lds_dwordx4 v218, s[12:13]
	s_add_i32 m0, s59, 0x8000
	s_nop 0
	global_load_lds_dwordx4 v215, s[48:49]
	s_add_i32 m0, s59, 0xa000
	s_nop 0
	global_load_lds_dwordx4 v217, s[48:49]
	s_waitcnt vmcnt(8) lgkmcnt(0)
	s_barrier
	v_mfma_i32_16x16x64_i8 v[72:75], v[24:27], v[32:35], v[128:131]
	v_mfma_i32_16x16x64_i8 v[140:143], v[28:31], v[36:39], v[72:75]
	v_mfma_i32_16x16x64_i8 v[72:75], v[112:115], v[32:35], v[132:135]
	v_mfma_i32_16x16x64_i8 v[136:139], v[116:119], v[36:39], v[72:75]
	v_mfma_i32_16x16x64_i8 v[72:75], v[24:27], v[40:43], v[228:231]
	v_mfma_i32_16x16x64_i8 v[124:127], v[28:31], v[44:47], v[72:75]
	v_mfma_i32_16x16x64_i8 v[72:75], v[112:115], v[40:43], v[232:235]
	v_mfma_i32_16x16x64_i8 v[120:123], v[116:119], v[44:47], v[72:75]
	v_mfma_i32_16x16x64_i8 v[72:75], v[24:27], v[48:51], v[236:239]
	v_mfma_i32_16x16x64_i8 v[0:3], v[24:27], v[56:59], v[0:3]
	v_mfma_i32_16x16x64_i8 v[108:111], v[28:31], v[52:55], v[72:75]
	v_mfma_i32_16x16x64_i8 v[72:75], v[112:115], v[48:51], v[240:243]
	v_mfma_i32_16x16x64_i8 v[88:91], v[28:31], v[76:79], v[0:3]
	v_mfma_i32_16x16x64_i8 v[0:3], v[112:115], v[56:59], v[4:7]
	v_mfma_i32_16x16x64_i8 v[104:107], v[116:119], v[52:55], v[72:75]
	v_mfma_i32_16x16x64_i8 v[84:87], v[116:119], v[76:79], v[0:3]
	v_mfma_i32_16x16x64_i8 v[0:3], v[208:211], v[32:35], v[8:11]
	v_mfma_i32_16x16x64_i8 v[132:135], v[224:227], v[36:39], v[0:3]
	v_mfma_i32_16x16x64_i8 v[0:3], v[64:67], v[32:35], v[12:15]
	v_mfma_i32_16x16x64_i8 v[128:131], v[68:71], v[36:39], v[0:3]
	v_mfma_i32_16x16x64_i8 v[0:3], v[208:211], v[40:43], v[60:63]
	v_mfma_i32_16x16x64_i8 v[116:119], v[224:227], v[44:47], v[0:3]
	v_mfma_i32_16x16x64_i8 v[0:3], v[64:67], v[40:43], v[100:103]
	v_mfma_i32_16x16x64_i8 v[112:115], v[68:71], v[44:47], v[0:3]
	v_mfma_i32_16x16x64_i8 v[0:3], v[208:211], v[48:51], v[244:247]
	v_mfma_i32_16x16x64_i8 v[100:103], v[224:227], v[52:55], v[0:3]
	v_mfma_i32_16x16x64_i8 v[0:3], v[64:67], v[48:51], v[248:251]
	v_mfma_i32_16x16x64_i8 v[96:99], v[68:71], v[52:55], v[0:3]
	v_mfma_i32_16x16x64_i8 v[0:3], v[208:211], v[56:59], v[16:19]
	v_mfma_i32_16x16x64_i8 v[72:75], v[224:227], v[76:79], v[0:3]
	v_mfma_i32_16x16x64_i8 v[0:3], v[64:67], v[56:59], v[20:23]
	v_mfma_i32_16x16x64_i8 v[68:71], v[68:71], v[76:79], v[0:3]
	s_barrier
	s_add_u32 s77, s8, 0x200
	s_addc_u32 s80, s9, 0
.LBB0_261:
	s_nop 2
	ds_read_b128 v[0:3], v219
	ds_read_b128 v[4:7], v219 offset:1024
	ds_read_b128 v[8:11], v219 offset:2048
	ds_read_b128 v[12:15], v219 offset:3072
	ds_read_b128 v[16:19], v220
	ds_read_b128 v[20:23], v220 offset:1024
	ds_read_b128 v[24:27], v220 offset:2048
	ds_read_b128 v[28:31], v220 offset:3072
	ds_read_b128 v[32:35], v221
	ds_read_b128 v[36:39], v221 offset:1024
	ds_read_b128 v[40:43], v221 offset:2048
	ds_read_b128 v[44:47], v221 offset:3072
	ds_read_b128 v[48:51], v221 offset:4096
	ds_read_b128 v[52:55], v221 offset:5120
	ds_read_b128 v[56:59], v221 offset:6144
	ds_read_b128 v[60:63], v221 offset:7168
	s_add_u32 s8, s46, 0x100
	s_addc_u32 s9, s47, 0
	s_cmp_eq_u32 s76, 12
	s_cselect_b32 s52, s11, s8
	s_cselect_b32 s53, s7, s9
	s_cselect_b32 s48, s41, s77
	s_cselect_b32 s49, s39, s80
	s_add_u32 s12, s52, 0x80
	s_addc_u32 s13, s53, 0
	s_add_u32 s50, s48, 0x80
	s_addc_u32 s51, s49, 0
	s_add_u32 s46, s46, 0x40080
	s_addc_u32 s47, s47, 0
	s_add_i32 m0, s59, 0xc000
	s_nop 0
	global_load_lds_dwordx4 v215, s[46:47]
	s_add_i32 m0, s59, 0xe000
	s_nop 0
	global_load_lds_dwordx4 v217, s[46:47]
	s_waitcnt vmcnt(8) lgkmcnt(0)
	s_barrier
	v_mfma_i32_16x16x64_i8 v[172:175], v[0:3], v[48:51], v[172:175]
	v_mfma_i32_16x16x64_i8 v[168:171], v[8:11], v[48:51], v[168:171]
	v_mfma_i32_16x16x64_i8 v[152:155], v[8:11], v[56:59], v[152:155]
	v_mfma_i32_16x16x64_i8 v[156:159], v[0:3], v[56:59], v[156:159]
	v_mfma_i32_16x16x64_i8 v[64:67], v[0:3], v[32:35], v[204:207]
	v_mfma_i32_16x16x64_i8 v[76:79], v[8:11], v[32:35], v[200:203]
	v_mfma_i32_16x16x64_i8 v[92:95], v[8:11], v[40:43], v[184:187]
	v_mfma_i32_16x16x64_i8 v[80:83], v[0:3], v[40:43], v[188:191]
	v_mfma_i32_16x16x64_i8 v[172:175], v[4:7], v[52:55], v[172:175]
	v_mfma_i32_16x16x64_i8 v[168:171], v[12:15], v[52:55], v[168:171]
	v_mfma_i32_16x16x64_i8 v[152:155], v[12:15], v[60:63], v[152:155]
	v_mfma_i32_16x16x64_i8 v[156:159], v[4:7], v[60:63], v[156:159]
	v_mfma_i32_16x16x64_i8 v[64:67], v[4:7], v[36:39], v[64:67]
	v_mfma_i32_16x16x64_i8 v[76:79], v[12:15], v[36:39], v[76:79]
	v_mfma_i32_16x16x64_i8 v[92:95], v[12:15], v[44:47], v[92:95]
	v_mfma_i32_16x16x64_i8 v[80:83], v[4:7], v[44:47], v[80:83]
	v_mfma_i32_16x16x64_i8 v[184:187], v[16:19], v[32:35], v[196:199]
	v_mfma_i32_16x16x64_i8 v[32:35], v[24:27], v[32:35], v[192:195]
	v_mfma_i32_16x16x64_i8 v[196:199], v[20:23], v[36:39], v[184:187]
	v_mfma_i32_16x16x64_i8 v[32:35], v[28:31], v[36:39], v[32:35]
	v_mfma_i32_16x16x64_i8 v[36:39], v[16:19], v[40:43], v[180:183]
	v_mfma_i32_16x16x64_i8 v[40:43], v[24:27], v[40:43], v[176:179]
	v_mfma_i32_16x16x64_i8 v[36:39], v[20:23], v[44:47], v[36:39]
	v_mfma_i32_16x16x64_i8 v[40:43], v[28:31], v[44:47], v[40:43]
	v_mfma_i32_16x16x64_i8 v[44:47], v[16:19], v[48:51], v[164:167]
	v_mfma_i32_16x16x64_i8 v[48:51], v[24:27], v[48:51], v[160:163]
	v_mfma_i32_16x16x64_i8 v[44:47], v[20:23], v[52:55], v[44:47]
	v_mfma_i32_16x16x64_i8 v[48:51], v[28:31], v[52:55], v[48:51]
	v_mfma_i32_16x16x64_i8 v[52:55], v[16:19], v[56:59], v[148:151]
	v_mfma_i32_16x16x64_i8 v[56:59], v[24:27], v[56:59], v[144:147]
	v_mfma_i32_16x16x64_i8 v[52:55], v[20:23], v[60:63], v[52:55]
	v_mfma_i32_16x16x64_i8 v[56:59], v[28:31], v[60:63], v[56:59]
	s_barrier
	ds_read_b128 v[60:63], v221 offset:16384
	ds_read_b128 v[144:147], v221 offset:17408
	ds_read_b128 v[148:151], v221 offset:18432
	ds_read_b128 v[160:163], v221 offset:19456
	ds_read_b128 v[164:167], v221 offset:20480
	ds_read_b128 v[176:179], v221 offset:21504
	ds_read_b128 v[180:183], v221 offset:22528
	ds_read_b128 v[184:187], v221 offset:23552
	s_add_i32 m0, s59, 0x10000
	s_nop 0
	global_load_lds_dwordx4 v216, s[48:49]
	s_add_i32 m0, s59, 0x12000
	s_nop 0
	global_load_lds_dwordx4 v218, s[48:49]
	s_add_u32 s46, s48, 0x40000
	s_addc_u32 s47, s49, 0
	s_add_i32 m0, s59, 0x14000
	s_nop 0
	global_load_lds_dwordx4 v216, s[46:47]
	s_add_i32 m0, s59, 0x16000
	s_nop 0
	global_load_lds_dwordx4 v218, s[46:47]
	s_add_i32 m0, s59, 0
	s_nop 0
	global_load_lds_dwordx4 v215, s[52:53]
	s_add_i32 m0, s59, 0x2000
	s_nop 0
	global_load_lds_dwordx4 v217, s[52:53]
	s_waitcnt vmcnt(8) lgkmcnt(0)
	s_barrier
	v_mfma_i32_16x16x64_i8 v[140:143], v[0:3], v[60:63], v[140:143]
	v_mfma_i32_16x16x64_i8 v[124:127], v[0:3], v[148:151], v[124:127]
	v_mfma_i32_16x16x64_i8 v[108:111], v[0:3], v[164:167], v[108:111]
	v_mfma_i32_16x16x64_i8 v[0:3], v[0:3], v[180:183], v[88:91]
	v_mfma_i32_16x16x64_i8 v[136:139], v[8:11], v[60:63], v[136:139]
	v_mfma_i32_16x16x64_i8 v[120:123], v[8:11], v[148:151], v[120:123]
	v_mfma_i32_16x16x64_i8 v[104:107], v[8:11], v[164:167], v[104:107]
	v_mfma_i32_16x16x64_i8 v[88:91], v[4:7], v[184:187], v[0:3]
	v_mfma_i32_16x16x64_i8 v[0:3], v[8:11], v[180:183], v[84:87]
	v_mfma_i32_16x16x64_i8 v[140:143], v[4:7], v[144:147], v[140:143]
	v_mfma_i32_16x16x64_i8 v[136:139], v[12:15], v[144:147], v[136:139]
	v_mfma_i32_16x16x64_i8 v[124:127], v[4:7], v[160:163], v[124:127]
	v_mfma_i32_16x16x64_i8 v[120:123], v[12:15], v[160:163], v[120:123]
	v_mfma_i32_16x16x64_i8 v[108:111], v[4:7], v[176:179], v[108:111]
	v_mfma_i32_16x16x64_i8 v[104:107], v[12:15], v[176:179], v[104:107]
	v_mfma_i32_16x16x64_i8 v[84:87], v[12:15], v[184:187], v[0:3]
	v_mfma_i32_16x16x64_i8 v[0:3], v[16:19], v[60:63], v[132:135]
	v_mfma_i32_16x16x64_i8 v[132:135], v[20:23], v[144:147], v[0:3]
	v_mfma_i32_16x16x64_i8 v[0:3], v[24:27], v[60:63], v[128:131]
	v_mfma_i32_16x16x64_i8 v[128:131], v[28:31], v[144:147], v[0:3]
	v_mfma_i32_16x16x64_i8 v[0:3], v[16:19], v[148:151], v[116:119]
	v_mfma_i32_16x16x64_i8 v[116:119], v[20:23], v[160:163], v[0:3]
	v_mfma_i32_16x16x64_i8 v[0:3], v[24:27], v[148:151], v[112:115]
	v_mfma_i32_16x16x64_i8 v[112:115], v[28:31], v[160:163], v[0:3]
	v_mfma_i32_16x16x64_i8 v[0:3], v[16:19], v[164:167], v[100:103]
	v_mfma_i32_16x16x64_i8 v[100:103], v[20:23], v[176:179], v[0:3]
	v_mfma_i32_16x16x64_i8 v[0:3], v[24:27], v[164:167], v[96:99]
	v_mfma_i32_16x16x64_i8 v[96:99], v[28:31], v[176:179], v[0:3]
	v_mfma_i32_16x16x64_i8 v[0:3], v[16:19], v[180:183], v[72:75]
	v_mfma_i32_16x16x64_i8 v[72:75], v[20:23], v[184:187], v[0:3]
	v_mfma_i32_16x16x64_i8 v[0:3], v[24:27], v[180:183], v[68:71]
	v_mfma_i32_16x16x64_i8 v[68:71], v[28:31], v[184:187], v[0:3]
	s_barrier
	ds_read_b128 v[16:19], v222
	ds_read_b128 v[8:11], v222 offset:1024
	ds_read_b128 v[4:7], v222 offset:2048
	s_nop 1
	ds_read_b128 v[0:3], v222 offset:3072
	ds_read_b128 v[28:31], v223
	ds_read_b128 v[24:27], v223 offset:1024
	ds_read_b128 v[20:23], v223 offset:2048
	ds_read_b128 v[12:15], v223 offset:3072
	ds_read_b128 v[60:63], v221 offset:32768
	ds_read_b128 v[144:147], v221 offset:33792
	ds_read_b128 v[148:151], v221 offset:34816
	ds_read_b128 v[160:163], v221 offset:35840
	ds_read_b128 v[208:211], v221 offset:36864
	ds_read_b128 v[224:227], v221 offset:37888
	ds_read_b128 v[228:231], v221 offset:38912
	ds_read_b128 v[232:235], v221 offset:39936
	s_add_u32 s46, s52, 0x40000
	s_addc_u32 s47, s53, 0
	s_add_i32 m0, s59, 0x4000
	s_nop 0
	global_load_lds_dwordx4 v215, s[46:47]
	s_add_i32 m0, s59, 0x6000
	s_nop 0
	global_load_lds_dwordx4 v217, s[46:47]
	s_waitcnt vmcnt(8) lgkmcnt(0)
	s_barrier
	v_mfma_i32_16x16x64_i8 v[64:67], v[16:19], v[60:63], v[64:67]
	v_mfma_i32_16x16x64_i8 v[204:207], v[8:11], v[144:147], v[64:67]
	v_mfma_i32_16x16x64_i8 v[64:67], v[4:7], v[60:63], v[76:79]
	v_mfma_i32_16x16x64_i8 v[200:203], v[0:3], v[144:147], v[64:67]
	v_mfma_i32_16x16x64_i8 v[64:67], v[16:19], v[148:151], v[80:83]
	v_mfma_i32_16x16x64_i8 v[188:191], v[8:11], v[160:163], v[64:67]
	v_mfma_i32_16x16x64_i8 v[64:67], v[4:7], v[148:151], v[92:95]
	v_mfma_i32_16x16x64_i8 v[184:187], v[0:3], v[160:163], v[64:67]
	v_mfma_i32_16x16x64_i8 v[64:67], v[16:19], v[208:211], v[172:175]
	v_mfma_i32_16x16x64_i8 v[172:175], v[8:11], v[224:227], v[64:67]
	v_mfma_i32_16x16x64_i8 v[64:67], v[4:7], v[208:211], v[168:171]
	v_mfma_i32_16x16x64_i8 v[168:171], v[0:3], v[224:227], v[64:67]
	v_mfma_i32_16x16x64_i8 v[64:67], v[16:19], v[228:231], v[156:159]
	v_mfma_i32_16x16x64_i8 v[156:159], v[8:11], v[232:235], v[64:67]
	v_mfma_i32_16x16x64_i8 v[64:67], v[4:7], v[228:231], v[152:155]
	v_mfma_i32_16x16x64_i8 v[152:155], v[0:3], v[232:235], v[64:67]
	v_mfma_i32_16x16x64_i8 v[32:35], v[20:23], v[60:63], v[32:35]
	v_mfma_i32_16x16x64_i8 v[192:195], v[12:15], v[144:147], v[32:35]
	v_mfma_i32_16x16x64_i8 v[32:35], v[28:31], v[148:151], v[36:39]
	v_mfma_i32_16x16x64_i8 v[180:183], v[24:27], v[160:163], v[32:35]
	v_mfma_i32_16x16x64_i8 v[32:35], v[20:23], v[148:151], v[40:43]
	v_mfma_i32_16x16x64_i8 v[176:179], v[12:15], v[160:163], v[32:35]
	v_mfma_i32_16x16x64_i8 v[32:35], v[28:31], v[208:211], v[44:47]
	v_mfma_i32_16x16x64_i8 v[164:167], v[24:27], v[224:227], v[32:35]
	v_mfma_i32_16x16x64_i8 v[32:35], v[20:23], v[208:211], v[48:51]
	v_mfma_i32_16x16x64_i8 v[160:163], v[12:15], v[224:227], v[32:35]
	v_mfma_i32_16x16x64_i8 v[32:35], v[28:31], v[228:231], v[52:55]
	v_mfma_i32_16x16x64_i8 v[64:67], v[28:31], v[60:63], v[196:199]
	v_mfma_i32_16x16x64_i8 v[148:151], v[24:27], v[232:235], v[32:35]
	v_mfma_i32_16x16x64_i8 v[32:35], v[20:23], v[228:231], v[56:59]
	v_mfma_i32_16x16x64_i8 v[196:199], v[24:27], v[144:147], v[64:67]
	v_mfma_i32_16x16x64_i8 v[144:147], v[12:15], v[232:235], v[32:35]
	s_barrier
	ds_read_b128 v[60:63], v221 offset:49152
	ds_read_b128 v[56:59], v221 offset:50176
	ds_read_b128 v[52:55], v221 offset:51200
	ds_read_b128 v[48:51], v221 offset:52224
	ds_read_b128 v[44:47], v221 offset:53248
	ds_read_b128 v[40:43], v221 offset:54272
	ds_read_b128 v[36:39], v221 offset:55296
	ds_read_b128 v[32:35], v221 offset:56320
	s_add_i32 m0, s59, 0x18000
	s_nop 0
	global_load_lds_dwordx4 v216, s[50:51]
	s_add_i32 m0, s59, 0x1a000
	s_nop 0
	global_load_lds_dwordx4 v218, s[50:51]
	s_add_u32 s46, s48, 0x40080
	s_addc_u32 s47, s49, 0
	s_add_i32 m0, s59, 0x1c000
	s_nop 0
	global_load_lds_dwordx4 v216, s[46:47]
	s_add_i32 m0, s59, 0x1e000
	s_nop 0
	global_load_lds_dwordx4 v218, s[46:47]
	s_add_i32 m0, s59, 0x8000
	s_nop 0
	global_load_lds_dwordx4 v215, s[12:13]
	s_add_i32 m0, s59, 0xa000
	s_nop 0
	global_load_lds_dwordx4 v217, s[12:13]
	s_waitcnt vmcnt(8) lgkmcnt(0)
	s_barrier
	v_mfma_i32_16x16x64_i8 v[64:67], v[16:19], v[60:63], v[140:143]
	v_mfma_i32_16x16x64_i8 v[140:143], v[8:11], v[56:59], v[64:67]
	v_mfma_i32_16x16x64_i8 v[64:67], v[4:7], v[60:63], v[136:139]
	v_mfma_i32_16x16x64_i8 v[136:139], v[0:3], v[56:59], v[64:67]
	v_mfma_i32_16x16x64_i8 v[64:67], v[16:19], v[52:55], v[124:127]
	v_mfma_i32_16x16x64_i8 v[124:127], v[8:11], v[48:51], v[64:67]
	v_mfma_i32_16x16x64_i8 v[64:67], v[4:7], v[52:55], v[120:123]
	v_mfma_i32_16x16x64_i8 v[120:123], v[0:3], v[48:51], v[64:67]
	v_mfma_i32_16x16x64_i8 v[64:67], v[16:19], v[44:47], v[108:111]
	v_mfma_i32_16x16x64_i8 v[108:111], v[8:11], v[40:43], v[64:67]
	v_mfma_i32_16x16x64_i8 v[64:67], v[4:7], v[44:47], v[104:107]
	v_mfma_i32_16x16x64_i8 v[104:107], v[0:3], v[40:43], v[64:67]
	v_mfma_i32_16x16x64_i8 v[64:67], v[16:19], v[36:39], v[88:91]
	v_mfma_i32_16x16x64_i8 v[88:91], v[8:11], v[32:35], v[64:67]
	v_mfma_i32_16x16x64_i8 v[64:67], v[4:7], v[36:39], v[84:87]
	v_mfma_i32_16x16x64_i8 v[84:87], v[0:3], v[32:35], v[64:67]
	v_mfma_i32_16x16x64_i8 v[64:67], v[28:31], v[60:63], v[132:135]
	v_mfma_i32_16x16x64_i8 v[132:135], v[24:27], v[56:59], v[64:67]
	v_mfma_i32_16x16x64_i8 v[64:67], v[20:23], v[60:63], v[128:131]
	v_mfma_i32_16x16x64_i8 v[128:131], v[12:15], v[56:59], v[64:67]
	v_mfma_i32_16x16x64_i8 v[64:67], v[28:31], v[52:55], v[116:119]
	v_mfma_i32_16x16x64_i8 v[116:119], v[24:27], v[48:51], v[64:67]
	v_mfma_i32_16x16x64_i8 v[64:67], v[20:23], v[52:55], v[112:115]
	v_mfma_i32_16x16x64_i8 v[112:115], v[12:15], v[48:51], v[64:67]
	v_mfma_i32_16x16x64_i8 v[64:67], v[28:31], v[44:47], v[100:103]
	v_mfma_i32_16x16x64_i8 v[100:103], v[24:27], v[40:43], v[64:67]
	v_mfma_i32_16x16x64_i8 v[64:67], v[20:23], v[44:47], v[96:99]
	v_mfma_i32_16x16x64_i8 v[96:99], v[12:15], v[40:43], v[64:67]
	v_mfma_i32_16x16x64_i8 v[64:67], v[28:31], v[36:39], v[72:75]
	v_mfma_i32_16x16x64_i8 v[72:75], v[24:27], v[32:35], v[64:67]
	v_mfma_i32_16x16x64_i8 v[64:67], v[20:23], v[36:39], v[68:71]
	v_mfma_i32_16x16x64_i8 v[68:71], v[12:15], v[32:35], v[64:67]
	s_barrier
	s_add_i32 s76, s76, 2
	s_add_u32 s77, s77, 0x100
	s_addc_u32 s80, s80, 0
	s_cmp_gt_u32 s76, 13
	s_mov_b64 s[46:47], s[8:9]
	s_cbranch_scc0 .LBB0_261
	s_and_b64 vcc, exec, s[28:29]
	s_cbranch_vccz .LBB0_264
	s_barrier

.LBB0_591:
	v_bfe_i32 v3, v0, 27, 1
	v_lshlrev_b32_e32 v1, 4, v0
	v_lshrrev_b32_e32 v3, 22, v3
	v_add_u32_e32 v3, v1, v3
	v_and_b32_e32 v3, 0xfffffc00, v3
	v_sub_u32_e32 v3, v1, v3
	v_lshrrev_b32_e32 v4, 4, v3
	v_bitop3_b32 v3, v4, v3, 32 bitop3:0x6c
	v_ashrrev_i32_e32 v2, 31, v0
	v_ashrrev_i32_e32 v5, 31, v3
	v_lshrrev_b32_e32 v2, 26, v2
	v_lshrrev_b32_e32 v5, 26, v5
	v_add_u32_e32 v2, v0, v2
	v_add_u32_e32 v5, v3, v5
	v_ashrrev_i32_e32 v2, 6, v2
	v_lshrrev_b32_e32 v6, 6, v5
	v_and_b32_e32 v5, 0xc0, v5
	v_lshlrev_b32_e32 v4, 3, v2
	v_lshlrev_b32_e32 v2, 5, v2
	v_sub_u32_e32 v3, v3, v5
	v_mov_b32_e32 v5, 1
	v_and_b32_e32 v4, 0xffff0, v4
	v_and_b32_e32 v2, 32, v2
	v_ashrrev_i16_sdwa v3, v5, sext(v3) dst_sel:DWORD dst_unused:UNUSED_PAD src0_sel:DWORD src1_sel:BYTE_0
	v_add_u32_sdwa v2, v2, sext(v3) dst_sel:DWORD dst_unused:UNUSED_PAD src0_sel:DWORD src1_sel:WORD_0
	v_add_lshl_u32 v3, v6, v4, 12
	v_add_u32_e32 v1, 0x2000, v1
	v_lshl_add_u32 v213, v2, 1, v3
	v_ashrrev_i32_e32 v2, 31, v1
	v_lshrrev_b32_e32 v2, 22, v2
	v_add_u32_e32 v2, v1, v2
	v_ashrrev_i32_e32 v2, 10, v2
	v_mul_i32_i24_e32 v3, 0x400, v2
	s_add_u32 s44, s70, 0x69400000
	v_sub_u32_e32 v1, v1, v3
	s_addc_u32 s45, s71, 0
	v_lshrrev_b32_e32 v3, 4, v1
	s_add_u32 s46, s70, 0x2600000
	v_bitop3_b32 v1, v3, v1, 32 bitop3:0x6c
	s_addc_u32 s47, s71, 0
	v_ashrrev_i32_e32 v4, 31, v1
	s_lshl_b32 s5, s21, 10
	s_ashr_i32 s9, s8, 31
	s_ashr_i32 s4, s20, 8
	v_lshrrev_b32_e32 v4, 26, v4
	s_add_i32 s48, s5, 0
	s_lshl_b64 s[10:11], s[8:9], 20
	v_add_u32_e32 v4, v1, v4
	s_add_u32 s34, s44, s10
	v_lshrrev_b32_e32 v6, 6, v4
	v_and_b32_e32 v4, 0xc0, v4
	s_addc_u32 s35, s45, s11
	s_ashr_i32 s7, s6, 31
	v_lshlrev_b32_e32 v3, 3, v2
	v_lshlrev_b32_e32 v2, 5, v2
	v_sub_u32_e32 v1, v1, v4
	s_lshl_b64 s[10:11], s[6:7], 20
	v_and_b32_e32 v3, 0xffff0, v3
	v_and_b32_e32 v2, 32, v2
	v_ashrrev_i16_sdwa v1, v5, sext(v1) dst_sel:DWORD dst_unused:UNUSED_PAD src0_sel:DWORD src1_sel:BYTE_0
	s_add_u32 s30, s46, s10
	v_add_u32_sdwa v1, v2, sext(v1) dst_sel:DWORD dst_unused:UNUSED_PAD src0_sel:DWORD src1_sel:WORD_0
	v_add_lshl_u32 v2, v6, v3, 12
	s_addc_u32 s31, s47, s11
	s_add_i32 m0, s48, 0x10000
	s_nop 0
	global_load_lds_dwordx4 v213, s[30:31]
	v_lshl_add_u32 v214, v1, 1, v2
	s_add_i32 m0, s48, 0x12000
	s_nop 0
	global_load_lds_dwordx4 v214, s[30:31]
	s_add_u32 s10, s30, 0x80000
	s_addc_u32 s11, s31, 0
	s_add_i32 m0, s48, 0x14000
	s_nop 0
	global_load_lds_dwordx4 v213, s[10:11]
	s_mov_b32 s49, 0
	s_add_i32 m0, s48, 0x16000
	s_nop 0
	global_load_lds_dwordx4 v214, s[10:11]
	s_add_i32 m0, s48, 0
	s_nop 0
	global_load_lds_dwordx4 v213, s[34:35]
	s_add_i32 m0, s48, 0x2000
	s_nop 0
	global_load_lds_dwordx4 v214, s[34:35]
	s_add_u32 s10, s34, 0x80000
	s_addc_u32 s11, s35, 0
	s_add_i32 m0, s48, 0x4000
	s_nop 0
	global_load_lds_dwordx4 v213, s[10:11]
	s_add_i32 m0, s48, 0x6000
	s_nop 0
	global_load_lds_dwordx4 v214, s[10:11]
	s_cmp_eq_u32 s4, 1
	s_cselect_b64 s[10:11], -1, 0
	s_cmp_lg_u32 s4, 1
	s_cbranch_scc1 .LBB0_593
	s_barrier

.LBB0_602:
	s_ashr_i32 s25, s24, 31
	s_lshl_b64 s[26:27], s[24:25], 20
	s_add_u32 s26, s44, s26
	s_addc_u32 s27, s45, s27
	s_and_b64 s[28:29], s[4:5], exec
	s_waitcnt lgkmcnt(0)
	ds_read_b128 v[0:3], v217
	ds_read_b128 v[4:7], v217 offset:1024
	ds_read_b128 v[8:11], v217 offset:2048
	ds_read_b128 v[12:15], v217 offset:3072
	ds_read_b128 v[16:19], v218
	ds_read_b128 v[20:23], v218 offset:1024
	ds_read_b128 v[24:27], v218 offset:2048
	ds_read_b128 v[28:31], v218 offset:3072
	ds_read_b128 v[32:35], v219
	ds_read_b128 v[36:39], v219 offset:1024
	ds_read_b128 v[40:43], v219 offset:2048
	ds_read_b128 v[44:47], v219 offset:3072
	ds_read_b128 v[48:51], v219 offset:4096
	ds_read_b128 v[52:55], v219 offset:5120
	ds_read_b128 v[56:59], v219 offset:6144
	ds_read_b128 v[60:63], v219 offset:7168
	s_cselect_b32 s7, s27, s35
	s_cselect_b32 s9, s26, s34
	s_ashr_i32 s23, s22, 31
	s_lshl_b64 s[28:29], s[22:23], 20
	s_add_u32 s28, s46, s28
	s_addc_u32 s29, s47, s29
	s_and_b64 s[36:37], s[4:5], exec
	s_cselect_b32 s23, s29, s31
	s_cselect_b32 s25, s28, s30
	s_add_u32 s36, s34, 0x100
	s_addc_u32 s37, s35, 0
	s_add_u32 s42, s30, 0x100
	s_addc_u32 s43, s31, 0
	s_add_u32 s38, s34, 0x180
	s_addc_u32 s39, s35, 0
	s_add_u32 s40, s30, 0x180
	s_addc_u32 s41, s31, 0
	s_add_u32 s60, s34, 0x80080
	s_addc_u32 s61, s35, 0
	s_add_i32 m0, s48, 0xc000
	s_nop 0
	global_load_lds_dwordx4 v213, s[60:61]
	s_add_i32 m0, s48, 0xe000
	s_nop 0
	global_load_lds_dwordx4 v214, s[60:61]
	s_waitcnt vmcnt(8) lgkmcnt(0)
	s_barrier
	v_mfma_f32_16x16x32_bf16 v[64:67], v[0:3], v[32:35], 0
	v_mfma_f32_16x16x32_bf16 v[68:71], v[8:11], v[32:35], 0
	v_mfma_f32_16x16x32_bf16 v[72:75], v[0:3], v[40:43], 0
	v_mfma_f32_16x16x32_bf16 v[76:79], v[8:11], v[40:43], 0
	v_mfma_f32_16x16x32_bf16 v[80:83], v[0:3], v[48:51], 0
	v_mfma_f32_16x16x32_bf16 v[84:87], v[8:11], v[48:51], 0
	v_mfma_f32_16x16x32_bf16 v[88:91], v[0:3], v[56:59], 0
	v_mfma_f32_16x16x32_bf16 v[64:67], v[4:7], v[36:39], v[64:67]
	v_mfma_f32_16x16x32_bf16 v[68:71], v[12:15], v[36:39], v[68:71]
	v_mfma_f32_16x16x32_bf16 v[72:75], v[4:7], v[44:47], v[72:75]
	v_mfma_f32_16x16x32_bf16 v[76:79], v[12:15], v[44:47], v[76:79]
	v_mfma_f32_16x16x32_bf16 v[80:83], v[4:7], v[52:55], v[80:83]
	v_mfma_f32_16x16x32_bf16 v[84:87], v[12:15], v[52:55], v[84:87]
	v_mfma_f32_16x16x32_bf16 v[96:99], v[4:7], v[60:63], v[88:91]
	v_mfma_f32_16x16x32_bf16 v[88:91], v[8:11], v[56:59], 0
	v_mfma_f32_16x16x32_bf16 v[100:103], v[12:15], v[60:63], v[88:91]
	v_mfma_f32_16x16x32_bf16 v[88:91], v[16:19], v[32:35], 0
	v_mfma_f32_16x16x32_bf16 v[32:35], v[24:27], v[32:35], 0
	v_mfma_f32_16x16x32_bf16 v[104:107], v[20:23], v[36:39], v[88:91]
	v_mfma_f32_16x16x32_bf16 v[32:35], v[28:31], v[36:39], v[32:35]
	v_mfma_f32_16x16x32_bf16 v[36:39], v[16:19], v[40:43], 0
	v_mfma_f32_16x16x32_bf16 v[40:43], v[24:27], v[40:43], 0
	v_mfma_f32_16x16x32_bf16 v[36:39], v[20:23], v[44:47], v[36:39]
	v_mfma_f32_16x16x32_bf16 v[40:43], v[28:31], v[44:47], v[40:43]
	v_mfma_f32_16x16x32_bf16 v[44:47], v[16:19], v[48:51], 0
	v_mfma_f32_16x16x32_bf16 v[48:51], v[24:27], v[48:51], 0
	v_mfma_f32_16x16x32_bf16 v[44:47], v[20:23], v[52:55], v[44:47]
	v_mfma_f32_16x16x32_bf16 v[48:51], v[28:31], v[52:55], v[48:51]
	v_mfma_f32_16x16x32_bf16 v[52:55], v[16:19], v[56:59], 0
	v_mfma_f32_16x16x32_bf16 v[56:59], v[24:27], v[56:59], 0
	v_mfma_f32_16x16x32_bf16 v[52:55], v[20:23], v[60:63], v[52:55]
	v_mfma_f32_16x16x32_bf16 v[56:59], v[28:31], v[60:63], v[56:59]
	s_barrier
	ds_read_b128 v[60:63], v219 offset:16384
	ds_read_b128 v[88:91], v219 offset:17408
	ds_read_b128 v[92:95], v219 offset:18432
	ds_read_b128 v[108:111], v219 offset:19456
	ds_read_b128 v[112:115], v219 offset:20480
	ds_read_b128 v[116:119], v219 offset:21504
	ds_read_b128 v[120:123], v219 offset:22528
	ds_read_b128 v[124:127], v219 offset:23552
	s_add_i32 m0, s48, 0x10000
	s_nop 0
	global_load_lds_dwordx4 v213, s[42:43]
	s_add_i32 m0, s48, 0x12000
	s_nop 0
	global_load_lds_dwordx4 v214, s[42:43]
	s_add_u32 s42, s30, 0x80100
	s_addc_u32 s43, s31, 0
	s_add_i32 m0, s48, 0x14000
	s_nop 0
	global_load_lds_dwordx4 v213, s[42:43]
	s_add_i32 m0, s48, 0x16000
	s_nop 0
	global_load_lds_dwordx4 v214, s[42:43]
	s_add_i32 m0, s48, 0
	s_nop 0
	global_load_lds_dwordx4 v213, s[36:37]
	s_add_i32 m0, s48, 0x2000
	s_nop 0
	global_load_lds_dwordx4 v214, s[36:37]
	s_waitcnt vmcnt(8) lgkmcnt(0)
	s_barrier
	v_mfma_f32_16x16x32_bf16 v[128:131], v[0:3], v[60:63], 0
	v_mfma_f32_16x16x32_bf16 v[132:135], v[4:7], v[88:91], v[128:131]
	v_mfma_f32_16x16x32_bf16 v[128:131], v[8:11], v[60:63], 0
	v_mfma_f32_16x16x32_bf16 v[140:143], v[12:15], v[88:91], v[128:131]
	v_mfma_f32_16x16x32_bf16 v[128:131], v[0:3], v[92:95], 0
	v_mfma_f32_16x16x32_bf16 v[148:151], v[4:7], v[108:111], v[128:131]
	v_mfma_f32_16x16x32_bf16 v[128:131], v[8:11], v[92:95], 0
	v_mfma_f32_16x16x32_bf16 v[156:159], v[12:15], v[108:111], v[128:131]
	v_mfma_f32_16x16x32_bf16 v[128:131], v[0:3], v[112:115], 0
	v_mfma_f32_16x16x32_bf16 v[0:3], v[0:3], v[120:123], 0
	v_mfma_f32_16x16x32_bf16 v[160:163], v[4:7], v[116:119], v[128:131]
	v_mfma_f32_16x16x32_bf16 v[0:3], v[4:7], v[124:127], v[0:3]
	v_mfma_f32_16x16x32_bf16 v[4:7], v[8:11], v[120:123], 0
	v_mfma_f32_16x16x32_bf16 v[128:131], v[8:11], v[112:115], 0
	v_mfma_f32_16x16x32_bf16 v[4:7], v[12:15], v[124:127], v[4:7]
	v_mfma_f32_16x16x32_bf16 v[164:167], v[12:15], v[116:119], v[128:131]
	v_mfma_f32_16x16x32_bf16 v[8:11], v[16:19], v[60:63], 0
	v_mfma_f32_16x16x32_bf16 v[168:171], v[20:23], v[88:91], v[8:11]
	v_mfma_f32_16x16x32_bf16 v[8:11], v[24:27], v[60:63], 0
	v_mfma_f32_16x16x32_bf16 v[172:175], v[28:31], v[88:91], v[8:11]
	v_mfma_f32_16x16x32_bf16 v[8:11], v[16:19], v[92:95], 0
	v_mfma_f32_16x16x32_bf16 v[176:179], v[20:23], v[108:111], v[8:11]
	v_mfma_f32_16x16x32_bf16 v[8:11], v[24:27], v[92:95], 0
	v_mfma_f32_16x16x32_bf16 v[108:111], v[28:31], v[108:111], v[8:11]
	v_mfma_f32_16x16x32_bf16 v[8:11], v[16:19], v[112:115], 0
	v_mfma_f32_16x16x32_bf16 v[180:183], v[20:23], v[116:119], v[8:11]
	v_mfma_f32_16x16x32_bf16 v[8:11], v[24:27], v[112:115], 0
	v_mfma_f32_16x16x32_bf16 v[116:119], v[28:31], v[116:119], v[8:11]
	v_mfma_f32_16x16x32_bf16 v[8:11], v[16:19], v[120:123], 0
	v_mfma_f32_16x16x32_bf16 v[184:187], v[20:23], v[124:127], v[8:11]
	v_mfma_f32_16x16x32_bf16 v[8:11], v[24:27], v[120:123], 0
	v_mfma_f32_16x16x32_bf16 v[124:127], v[28:31], v[124:127], v[8:11]
	s_barrier
	s_nop 4
	ds_read_b128 v[8:11], v220
	ds_read_b128 v[12:15], v220 offset:1024
	ds_read_b128 v[16:19], v220 offset:2048
	ds_read_b128 v[20:23], v220 offset:3072
	ds_read_b128 v[194:197], v221
	ds_read_b128 v[198:201], v221 offset:1024
	ds_read_b128 v[202:205], v221 offset:2048
	ds_read_b128 v[206:209], v221 offset:3072
	ds_read_b128 v[24:27], v219 offset:32768
	ds_read_b128 v[28:31], v219 offset:33792
	ds_read_b128 v[60:63], v219 offset:34816
	ds_read_b128 v[224:227], v219 offset:35840
	ds_read_b128 v[228:231], v219 offset:36864
	ds_read_b128 v[232:235], v219 offset:37888
	ds_read_b128 v[236:239], v219 offset:38912
	ds_read_b128 v[240:243], v219 offset:39936
	s_add_u32 s34, s34, 0x80100
	s_addc_u32 s35, s35, 0
	s_add_i32 m0, s48, 0x4000
	s_nop 0
	global_load_lds_dwordx4 v213, s[34:35]
	s_add_i32 m0, s48, 0x6000
	s_nop 0
	global_load_lds_dwordx4 v214, s[34:35]
	s_waitcnt vmcnt(8) lgkmcnt(0)
	s_barrier
	v_mfma_f32_16x16x32_bf16 v[64:67], v[8:11], v[24:27], v[64:67]
	v_mfma_f32_16x16x32_bf16 v[152:155], v[12:15], v[28:31], v[64:67]
	v_mfma_f32_16x16x32_bf16 v[64:67], v[16:19], v[24:27], v[68:71]
	v_mfma_f32_16x16x32_bf16 v[144:147], v[20:23], v[28:31], v[64:67]
	v_mfma_f32_16x16x32_bf16 v[64:67], v[8:11], v[60:63], v[72:75]
	v_mfma_f32_16x16x32_bf16 v[120:123], v[12:15], v[224:227], v[64:67]
	v_mfma_f32_16x16x32_bf16 v[64:67], v[16:19], v[60:63], v[76:79]
	v_mfma_f32_16x16x32_bf16 v[112:115], v[20:23], v[224:227], v[64:67]
	v_mfma_f32_16x16x32_bf16 v[64:67], v[8:11], v[228:231], v[80:83]
	v_mfma_f32_16x16x32_bf16 v[92:95], v[12:15], v[232:235], v[64:67]
	v_mfma_f32_16x16x32_bf16 v[64:67], v[16:19], v[228:231], v[84:87]
	v_mfma_f32_16x16x32_bf16 v[88:91], v[20:23], v[232:235], v[64:67]
	v_mfma_f32_16x16x32_bf16 v[64:67], v[8:11], v[236:239], v[96:99]
	v_mfma_f32_16x16x32_bf16 v[76:79], v[12:15], v[240:243], v[64:67]
	v_mfma_f32_16x16x32_bf16 v[64:67], v[16:19], v[236:239], v[100:103]
	v_mfma_f32_16x16x32_bf16 v[72:75], v[20:23], v[240:243], v[64:67]
	v_mfma_f32_16x16x32_bf16 v[64:67], v[194:197], v[24:27], v[104:107]
	v_mfma_f32_16x16x32_bf16 v[24:27], v[202:205], v[24:27], v[32:35]
	v_mfma_f32_16x16x32_bf16 v[128:131], v[206:209], v[28:31], v[24:27]
	v_mfma_f32_16x16x32_bf16 v[24:27], v[194:197], v[60:63], v[36:39]
	v_mfma_f32_16x16x32_bf16 v[104:107], v[198:201], v[224:227], v[24:27]
	v_mfma_f32_16x16x32_bf16 v[24:27], v[202:205], v[60:63], v[40:43]
	v_mfma_f32_16x16x32_bf16 v[96:99], v[206:209], v[224:227], v[24:27]
	v_mfma_f32_16x16x32_bf16 v[24:27], v[194:197], v[228:231], v[44:47]
	v_mfma_f32_16x16x32_bf16 v[84:87], v[198:201], v[232:235], v[24:27]
	v_mfma_f32_16x16x32_bf16 v[24:27], v[202:205], v[228:231], v[48:51]
	v_mfma_f32_16x16x32_bf16 v[80:83], v[206:209], v[232:235], v[24:27]
	v_mfma_f32_16x16x32_bf16 v[24:27], v[194:197], v[236:239], v[52:55]
	v_mfma_f32_16x16x32_bf16 v[68:71], v[198:201], v[240:243], v[24:27]
	v_mfma_f32_16x16x32_bf16 v[24:27], v[202:205], v[236:239], v[56:59]
	v_mfma_f32_16x16x32_bf16 v[136:139], v[198:201], v[28:31], v[64:67]
	v_mfma_f32_16x16x32_bf16 v[64:67], v[206:209], v[240:243], v[24:27]
	s_barrier
	ds_read_b128 v[32:35], v219 offset:49152
	ds_read_b128 v[36:39], v219 offset:50176
	ds_read_b128 v[100:103], v219 offset:51200
	ds_read_b128 v[224:227], v219 offset:52224
	ds_read_b128 v[228:231], v219 offset:53248
	ds_read_b128 v[232:235], v219 offset:54272
	ds_read_b128 v[236:239], v219 offset:55296
	ds_read_b128 v[240:243], v219 offset:56320
	s_add_i32 m0, s48, 0x18000
	s_nop 0
	global_load_lds_dwordx4 v213, s[40:41]
	s_add_i32 m0, s48, 0x1a000
	s_nop 0
	global_load_lds_dwordx4 v214, s[40:41]
	s_add_u32 s34, s30, 0x80180
	s_addc_u32 s35, s31, 0
	s_add_i32 m0, s48, 0x1c000
	s_nop 0
	global_load_lds_dwordx4 v213, s[34:35]
	s_add_i32 m0, s48, 0x1e000
	s_nop 0
	global_load_lds_dwordx4 v214, s[34:35]
	s_add_i32 m0, s48, 0x8000
	s_nop 0
	global_load_lds_dwordx4 v213, s[38:39]
	s_add_i32 m0, s48, 0xa000
	s_nop 0
	global_load_lds_dwordx4 v214, s[38:39]
	s_waitcnt vmcnt(8) lgkmcnt(0)
	s_barrier
	v_mfma_f32_16x16x32_bf16 v[24:27], v[8:11], v[32:35], v[132:135]
	v_mfma_f32_16x16x32_bf16 v[60:63], v[12:15], v[36:39], v[24:27]
	v_mfma_f32_16x16x32_bf16 v[24:27], v[16:19], v[32:35], v[140:143]
	v_mfma_f32_16x16x32_bf16 v[56:59], v[20:23], v[36:39], v[24:27]
	v_mfma_f32_16x16x32_bf16 v[24:27], v[8:11], v[100:103], v[148:151]
	v_mfma_f32_16x16x32_bf16 v[44:47], v[12:15], v[224:227], v[24:27]
	v_mfma_f32_16x16x32_bf16 v[24:27], v[16:19], v[100:103], v[156:159]
	v_mfma_f32_16x16x32_bf16 v[40:43], v[20:23], v[224:227], v[24:27]
	v_mfma_f32_16x16x32_bf16 v[24:27], v[8:11], v[228:231], v[160:163]
	v_mfma_f32_16x16x32_bf16 v[0:3], v[8:11], v[236:239], v[0:3]
	v_mfma_f32_16x16x32_bf16 v[28:31], v[12:15], v[232:235], v[24:27]
	v_mfma_f32_16x16x32_bf16 v[24:27], v[16:19], v[228:231], v[164:167]
	v_mfma_f32_16x16x32_bf16 v[12:15], v[12:15], v[240:243], v[0:3]
	v_mfma_f32_16x16x32_bf16 v[0:3], v[16:19], v[236:239], v[4:7]
	v_mfma_f32_16x16x32_bf16 v[24:27], v[20:23], v[232:235], v[24:27]
	v_mfma_f32_16x16x32_bf16 v[8:11], v[20:23], v[240:243], v[0:3]
	v_mfma_f32_16x16x32_bf16 v[0:3], v[194:197], v[32:35], v[168:171]
	v_mfma_f32_16x16x32_bf16 v[52:55], v[198:201], v[36:39], v[0:3]
	v_mfma_f32_16x16x32_bf16 v[0:3], v[202:205], v[32:35], v[172:175]
	v_mfma_f32_16x16x32_bf16 v[48:51], v[206:209], v[36:39], v[0:3]
	v_mfma_f32_16x16x32_bf16 v[0:3], v[194:197], v[100:103], v[176:179]
	v_mfma_f32_16x16x32_bf16 v[36:39], v[198:201], v[224:227], v[0:3]
	v_mfma_f32_16x16x32_bf16 v[0:3], v[202:205], v[100:103], v[108:111]
	v_mfma_f32_16x16x32_bf16 v[32:35], v[206:209], v[224:227], v[0:3]
	v_mfma_f32_16x16x32_bf16 v[0:3], v[194:197], v[228:231], v[180:183]
	v_mfma_f32_16x16x32_bf16 v[20:23], v[198:201], v[232:235], v[0:3]
	v_mfma_f32_16x16x32_bf16 v[0:3], v[202:205], v[228:231], v[116:119]
	v_mfma_f32_16x16x32_bf16 v[16:19], v[206:209], v[232:235], v[0:3]
	v_mfma_f32_16x16x32_bf16 v[0:3], v[194:197], v[236:239], v[184:187]
	v_mfma_f32_16x16x32_bf16 v[4:7], v[198:201], v[240:243], v[0:3]
	v_mfma_f32_16x16x32_bf16 v[0:3], v[202:205], v[236:239], v[124:127]
	v_mfma_f32_16x16x32_bf16 v[0:3], v[206:209], v[240:243], v[0:3]
	s_barrier
	s_add_u32 s59, s30, 0x200
	s_addc_u32 s60, s31, 0
	s_mov_b32 s61, 0
.LBB0_603:
	ds_read_b128 v[100:103], v217
	ds_read_b128 v[108:111], v217 offset:1024
	ds_read_b128 v[116:119], v217 offset:2048
	ds_read_b128 v[124:127], v217 offset:3072
	ds_read_b128 v[132:135], v218
	ds_read_b128 v[140:143], v218 offset:1024
	ds_read_b128 v[148:151], v218 offset:2048
	ds_read_b128 v[156:159], v218 offset:3072
	ds_read_b128 v[160:163], v219
	ds_read_b128 v[164:167], v219 offset:1024
	ds_read_b128 v[168:171], v219 offset:2048
	ds_read_b128 v[172:175], v219 offset:3072
	ds_read_b128 v[176:179], v219 offset:4096
	ds_read_b128 v[180:183], v219 offset:5120
	ds_read_b128 v[184:187], v219 offset:6144
	ds_read_b128 v[194:197], v219 offset:7168
	s_add_u32 s30, s36, 0x100
	s_addc_u32 s31, s37, 0
	s_cmp_eq_u32 s61, 28
	s_cselect_b32 s42, s9, s30
	s_cselect_b32 s43, s7, s31
	s_cselect_b32 s38, s25, s59
	s_cselect_b32 s39, s23, s60
	s_add_u32 s34, s42, 0x80
	s_addc_u32 s35, s43, 0
	s_add_u32 s40, s38, 0x80
	s_addc_u32 s41, s39, 0
	s_add_u32 s36, s36, 0x80080
	s_addc_u32 s37, s37, 0
	s_add_i32 m0, s48, 0xc000
	s_nop 0
	global_load_lds_dwordx4 v213, s[36:37]
	s_add_i32 m0, s48, 0xe000
	s_nop 0
	global_load_lds_dwordx4 v214, s[36:37]
	s_waitcnt vmcnt(8) lgkmcnt(0)
	s_barrier
	v_mfma_f32_16x16x32_bf16 v[152:155], v[100:103], v[160:163], v[152:155]
	v_mfma_f32_16x16x32_bf16 v[144:147], v[116:119], v[160:163], v[144:147]
	v_mfma_f32_16x16x32_bf16 v[112:115], v[116:119], v[168:171], v[112:115]
	v_mfma_f32_16x16x32_bf16 v[120:123], v[100:103], v[168:171], v[120:123]
	v_mfma_f32_16x16x32_bf16 v[92:95], v[100:103], v[176:179], v[92:95]
	v_mfma_f32_16x16x32_bf16 v[88:91], v[116:119], v[176:179], v[88:91]
	v_mfma_f32_16x16x32_bf16 v[72:75], v[116:119], v[184:187], v[72:75]
	v_mfma_f32_16x16x32_bf16 v[76:79], v[100:103], v[184:187], v[76:79]
	v_mfma_f32_16x16x32_bf16 v[152:155], v[108:111], v[164:167], v[152:155]
	v_mfma_f32_16x16x32_bf16 v[144:147], v[124:127], v[164:167], v[144:147]
	v_mfma_f32_16x16x32_bf16 v[112:115], v[124:127], v[172:175], v[112:115]
	v_mfma_f32_16x16x32_bf16 v[120:123], v[108:111], v[172:175], v[120:123]
	v_mfma_f32_16x16x32_bf16 v[92:95], v[108:111], v[180:183], v[92:95]
	v_mfma_f32_16x16x32_bf16 v[88:91], v[124:127], v[180:183], v[88:91]
	v_mfma_f32_16x16x32_bf16 v[72:75], v[124:127], v[194:197], v[72:75]
	v_mfma_f32_16x16x32_bf16 v[76:79], v[108:111], v[194:197], v[76:79]
	v_mfma_f32_16x16x32_bf16 v[136:139], v[132:135], v[160:163], v[136:139]
	v_mfma_f32_16x16x32_bf16 v[128:131], v[148:151], v[160:163], v[128:131]
	v_mfma_f32_16x16x32_bf16 v[96:99], v[148:151], v[168:171], v[96:99]
	v_mfma_f32_16x16x32_bf16 v[104:107], v[132:135], v[168:171], v[104:107]
	v_mfma_f32_16x16x32_bf16 v[84:87], v[132:135], v[176:179], v[84:87]
	v_mfma_f32_16x16x32_bf16 v[80:83], v[148:151], v[176:179], v[80:83]
	v_mfma_f32_16x16x32_bf16 v[64:67], v[148:151], v[184:187], v[64:67]
	v_mfma_f32_16x16x32_bf16 v[68:71], v[132:135], v[184:187], v[68:71]
	v_mfma_f32_16x16x32_bf16 v[136:139], v[140:143], v[164:167], v[136:139]
	v_mfma_f32_16x16x32_bf16 v[128:131], v[156:159], v[164:167], v[128:131]
	v_mfma_f32_16x16x32_bf16 v[96:99], v[156:159], v[172:175], v[96:99]
	v_mfma_f32_16x16x32_bf16 v[104:107], v[140:143], v[172:175], v[104:107]
	v_mfma_f32_16x16x32_bf16 v[84:87], v[140:143], v[180:183], v[84:87]
	v_mfma_f32_16x16x32_bf16 v[80:83], v[156:159], v[180:183], v[80:83]
	v_mfma_f32_16x16x32_bf16 v[64:67], v[156:159], v[194:197], v[64:67]
	v_mfma_f32_16x16x32_bf16 v[68:71], v[140:143], v[194:197], v[68:71]
	s_barrier
	ds_read_b128 v[160:163], v219 offset:16384
	ds_read_b128 v[164:167], v219 offset:17408
	ds_read_b128 v[168:171], v219 offset:18432
	ds_read_b128 v[172:175], v219 offset:19456
	ds_read_b128 v[176:179], v219 offset:20480
	ds_read_b128 v[180:183], v219 offset:21504
	ds_read_b128 v[184:187], v219 offset:22528
	ds_read_b128 v[194:197], v219 offset:23552
	s_add_i32 m0, s48, 0x10000
	s_nop 0
	global_load_lds_dwordx4 v213, s[38:39]
	s_add_i32 m0, s48, 0x12000
	s_nop 0
	global_load_lds_dwordx4 v214, s[38:39]
	s_add_u32 s36, s38, 0x80000
	s_addc_u32 s37, s39, 0
	s_add_i32 m0, s48, 0x14000
	s_nop 0
	global_load_lds_dwordx4 v213, s[36:37]
	s_add_i32 m0, s48, 0x16000
	s_nop 0
	global_load_lds_dwordx4 v214, s[36:37]
	s_add_i32 m0, s48, 0
	s_nop 0
	global_load_lds_dwordx4 v213, s[42:43]
	s_add_i32 m0, s48, 0x2000
	s_nop 0
	global_load_lds_dwordx4 v214, s[42:43]
	s_waitcnt vmcnt(8) lgkmcnt(0)
	s_barrier
	v_mfma_f32_16x16x32_bf16 v[60:63], v[100:103], v[160:163], v[60:63]
	v_mfma_f32_16x16x32_bf16 v[56:59], v[116:119], v[160:163], v[56:59]
	v_mfma_f32_16x16x32_bf16 v[40:43], v[116:119], v[168:171], v[40:43]
	v_mfma_f32_16x16x32_bf16 v[44:47], v[100:103], v[168:171], v[44:47]
	v_mfma_f32_16x16x32_bf16 v[28:31], v[100:103], v[176:179], v[28:31]
	v_mfma_f32_16x16x32_bf16 v[24:27], v[116:119], v[176:179], v[24:27]
	v_mfma_f32_16x16x32_bf16 v[8:11], v[116:119], v[184:187], v[8:11]
	v_mfma_f32_16x16x32_bf16 v[12:15], v[100:103], v[184:187], v[12:15]
	v_mfma_f32_16x16x32_bf16 v[60:63], v[108:111], v[164:167], v[60:63]
	v_mfma_f32_16x16x32_bf16 v[56:59], v[124:127], v[164:167], v[56:59]
	v_mfma_f32_16x16x32_bf16 v[40:43], v[124:127], v[172:175], v[40:43]
	v_mfma_f32_16x16x32_bf16 v[44:47], v[108:111], v[172:175], v[44:47]
	v_mfma_f32_16x16x32_bf16 v[28:31], v[108:111], v[180:183], v[28:31]
	v_mfma_f32_16x16x32_bf16 v[24:27], v[124:127], v[180:183], v[24:27]
	v_mfma_f32_16x16x32_bf16 v[8:11], v[124:127], v[194:197], v[8:11]
	v_mfma_f32_16x16x32_bf16 v[12:15], v[108:111], v[194:197], v[12:15]
	v_mfma_f32_16x16x32_bf16 v[52:55], v[132:135], v[160:163], v[52:55]
	v_mfma_f32_16x16x32_bf16 v[48:51], v[148:151], v[160:163], v[48:51]
	v_mfma_f32_16x16x32_bf16 v[32:35], v[148:151], v[168:171], v[32:35]
	v_mfma_f32_16x16x32_bf16 v[36:39], v[132:135], v[168:171], v[36:39]
	v_mfma_f32_16x16x32_bf16 v[20:23], v[132:135], v[176:179], v[20:23]
	v_mfma_f32_16x16x32_bf16 v[16:19], v[148:151], v[176:179], v[16:19]
	v_mfma_f32_16x16x32_bf16 v[0:3], v[148:151], v[184:187], v[0:3]
	v_mfma_f32_16x16x32_bf16 v[4:7], v[132:135], v[184:187], v[4:7]
	v_mfma_f32_16x16x32_bf16 v[52:55], v[140:143], v[164:167], v[52:55]
	v_mfma_f32_16x16x32_bf16 v[48:51], v[156:159], v[164:167], v[48:51]
	v_mfma_f32_16x16x32_bf16 v[32:35], v[156:159], v[172:175], v[32:35]
	v_mfma_f32_16x16x32_bf16 v[36:39], v[140:143], v[172:175], v[36:39]
	v_mfma_f32_16x16x32_bf16 v[20:23], v[140:143], v[180:183], v[20:23]
	v_mfma_f32_16x16x32_bf16 v[16:19], v[156:159], v[180:183], v[16:19]
	v_mfma_f32_16x16x32_bf16 v[0:3], v[156:159], v[194:197], v[0:3]
	v_mfma_f32_16x16x32_bf16 v[4:7], v[140:143], v[194:197], v[4:7]
	s_barrier
	ds_read_b128 v[100:103], v220
	ds_read_b128 v[108:111], v220 offset:1024
	ds_read_b128 v[116:119], v220 offset:2048
	ds_read_b128 v[124:127], v220 offset:3072
	ds_read_b128 v[132:135], v221
	ds_read_b128 v[140:143], v221 offset:1024
	ds_read_b128 v[148:151], v221 offset:2048
	ds_read_b128 v[156:159], v221 offset:3072
	ds_read_b128 v[160:163], v219 offset:32768
	ds_read_b128 v[164:167], v219 offset:33792
	ds_read_b128 v[168:171], v219 offset:34816
	ds_read_b128 v[172:175], v219 offset:35840
	ds_read_b128 v[176:179], v219 offset:36864
	ds_read_b128 v[180:183], v219 offset:37888
	ds_read_b128 v[184:187], v219 offset:38912
	ds_read_b128 v[194:197], v219 offset:39936
	s_add_u32 s36, s42, 0x80000
	s_addc_u32 s37, s43, 0
	s_add_i32 m0, s48, 0x4000
	s_nop 0
	global_load_lds_dwordx4 v213, s[36:37]
	s_add_i32 m0, s48, 0x6000
	s_nop 0
	global_load_lds_dwordx4 v214, s[36:37]
	s_waitcnt vmcnt(8) lgkmcnt(0)
	s_barrier
	v_mfma_f32_16x16x32_bf16 v[152:155], v[100:103], v[160:163], v[152:155]
	v_mfma_f32_16x16x32_bf16 v[144:147], v[116:119], v[160:163], v[144:147]
	v_mfma_f32_16x16x32_bf16 v[112:115], v[116:119], v[168:171], v[112:115]
	v_mfma_f32_16x16x32_bf16 v[120:123], v[100:103], v[168:171], v[120:123]
	v_mfma_f32_16x16x32_bf16 v[92:95], v[100:103], v[176:179], v[92:95]
	v_mfma_f32_16x16x32_bf16 v[88:91], v[116:119], v[176:179], v[88:91]
	v_mfma_f32_16x16x32_bf16 v[72:75], v[116:119], v[184:187], v[72:75]
	v_mfma_f32_16x16x32_bf16 v[76:79], v[100:103], v[184:187], v[76:79]
	v_mfma_f32_16x16x32_bf16 v[152:155], v[108:111], v[164:167], v[152:155]
	v_mfma_f32_16x16x32_bf16 v[144:147], v[124:127], v[164:167], v[144:147]
	v_mfma_f32_16x16x32_bf16 v[112:115], v[124:127], v[172:175], v[112:115]
	v_mfma_f32_16x16x32_bf16 v[120:123], v[108:111], v[172:175], v[120:123]
	v_mfma_f32_16x16x32_bf16 v[92:95], v[108:111], v[180:183], v[92:95]
	v_mfma_f32_16x16x32_bf16 v[88:91], v[124:127], v[180:183], v[88:91]
	v_mfma_f32_16x16x32_bf16 v[72:75], v[124:127], v[194:197], v[72:75]
	v_mfma_f32_16x16x32_bf16 v[76:79], v[108:111], v[194:197], v[76:79]
	v_mfma_f32_16x16x32_bf16 v[136:139], v[132:135], v[160:163], v[136:139]
	v_mfma_f32_16x16x32_bf16 v[128:131], v[148:151], v[160:163], v[128:131]
	v_mfma_f32_16x16x32_bf16 v[96:99], v[148:151], v[168:171], v[96:99]
	v_mfma_f32_16x16x32_bf16 v[104:107], v[132:135], v[168:171], v[104:107]
	v_mfma_f32_16x16x32_bf16 v[84:87], v[132:135], v[176:179], v[84:87]
	v_mfma_f32_16x16x32_bf16 v[80:83], v[148:151], v[176:179], v[80:83]
	v_mfma_f32_16x16x32_bf16 v[64:67], v[148:151], v[184:187], v[64:67]
	v_mfma_f32_16x16x32_bf16 v[68:71], v[132:135], v[184:187], v[68:71]
	v_mfma_f32_16x16x32_bf16 v[136:139], v[140:143], v[164:167], v[136:139]
	v_mfma_f32_16x16x32_bf16 v[128:131], v[156:159], v[164:167], v[128:131]
	v_mfma_f32_16x16x32_bf16 v[96:99], v[156:159], v[172:175], v[96:99]
	v_mfma_f32_16x16x32_bf16 v[104:107], v[140:143], v[172:175], v[104:107]
	v_mfma_f32_16x16x32_bf16 v[84:87], v[140:143], v[180:183], v[84:87]
	v_mfma_f32_16x16x32_bf16 v[80:83], v[156:159], v[180:183], v[80:83]
	v_mfma_f32_16x16x32_bf16 v[64:67], v[156:159], v[194:197], v[64:67]
	v_mfma_f32_16x16x32_bf16 v[68:71], v[140:143], v[194:197], v[68:71]
	s_barrier
	ds_read_b128 v[160:163], v219 offset:49152
	ds_read_b128 v[164:167], v219 offset:50176
	ds_read_b128 v[168:171], v219 offset:51200
	ds_read_b128 v[172:175], v219 offset:52224
	ds_read_b128 v[176:179], v219 offset:53248
	ds_read_b128 v[180:183], v219 offset:54272
	ds_read_b128 v[184:187], v219 offset:55296
	ds_read_b128 v[194:197], v219 offset:56320
	s_add_i32 m0, s48, 0x18000
	s_nop 0
	global_load_lds_dwordx4 v213, s[40:41]
	s_add_i32 m0, s48, 0x1a000
	s_nop 0
	global_load_lds_dwordx4 v214, s[40:41]
	s_add_u32 s36, s38, 0x80080
	s_addc_u32 s37, s39, 0
	s_add_i32 m0, s48, 0x1c000
	s_nop 0
	global_load_lds_dwordx4 v213, s[36:37]
	s_add_i32 m0, s48, 0x1e000
	s_nop 0
	global_load_lds_dwordx4 v214, s[36:37]
	s_add_i32 m0, s48, 0x8000
	s_nop 0
	global_load_lds_dwordx4 v213, s[34:35]
	s_add_i32 m0, s48, 0xa000
	s_nop 0
	global_load_lds_dwordx4 v214, s[34:35]
	s_waitcnt vmcnt(8) lgkmcnt(0)
	s_barrier
	v_mfma_f32_16x16x32_bf16 v[60:63], v[100:103], v[160:163], v[60:63]
	v_mfma_f32_16x16x32_bf16 v[56:59], v[116:119], v[160:163], v[56:59]
	v_mfma_f32_16x16x32_bf16 v[40:43], v[116:119], v[168:171], v[40:43]
	v_mfma_f32_16x16x32_bf16 v[44:47], v[100:103], v[168:171], v[44:47]
	v_mfma_f32_16x16x32_bf16 v[28:31], v[100:103], v[176:179], v[28:31]
	v_mfma_f32_16x16x32_bf16 v[24:27], v[116:119], v[176:179], v[24:27]
	v_mfma_f32_16x16x32_bf16 v[8:11], v[116:119], v[184:187], v[8:11]
	v_mfma_f32_16x16x32_bf16 v[12:15], v[100:103], v[184:187], v[12:15]
	v_mfma_f32_16x16x32_bf16 v[60:63], v[108:111], v[164:167], v[60:63]
	v_mfma_f32_16x16x32_bf16 v[56:59], v[124:127], v[164:167], v[56:59]
	v_mfma_f32_16x16x32_bf16 v[40:43], v[124:127], v[172:175], v[40:43]
	v_mfma_f32_16x16x32_bf16 v[44:47], v[108:111], v[172:175], v[44:47]
	v_mfma_f32_16x16x32_bf16 v[28:31], v[108:111], v[180:183], v[28:31]
	v_mfma_f32_16x16x32_bf16 v[24:27], v[124:127], v[180:183], v[24:27]
	v_mfma_f32_16x16x32_bf16 v[8:11], v[124:127], v[194:197], v[8:11]
	v_mfma_f32_16x16x32_bf16 v[12:15], v[108:111], v[194:197], v[12:15]
	v_mfma_f32_16x16x32_bf16 v[52:55], v[132:135], v[160:163], v[52:55]
	v_mfma_f32_16x16x32_bf16 v[48:51], v[148:151], v[160:163], v[48:51]
	v_mfma_f32_16x16x32_bf16 v[32:35], v[148:151], v[168:171], v[32:35]
	v_mfma_f32_16x16x32_bf16 v[36:39], v[132:135], v[168:171], v[36:39]
	v_mfma_f32_16x16x32_bf16 v[20:23], v[132:135], v[176:179], v[20:23]
	v_mfma_f32_16x16x32_bf16 v[16:19], v[148:151], v[176:179], v[16:19]
	v_mfma_f32_16x16x32_bf16 v[0:3], v[148:151], v[184:187], v[0:3]
	v_mfma_f32_16x16x32_bf16 v[4:7], v[132:135], v[184:187], v[4:7]
	v_mfma_f32_16x16x32_bf16 v[52:55], v[140:143], v[164:167], v[52:55]
	v_mfma_f32_16x16x32_bf16 v[48:51], v[156:159], v[164:167], v[48:51]
	v_mfma_f32_16x16x32_bf16 v[32:35], v[156:159], v[172:175], v[32:35]
	v_mfma_f32_16x16x32_bf16 v[36:39], v[140:143], v[172:175], v[36:39]
	v_mfma_f32_16x16x32_bf16 v[20:23], v[140:143], v[180:183], v[20:23]
	v_mfma_f32_16x16x32_bf16 v[16:19], v[156:159], v[180:183], v[16:19]
	v_mfma_f32_16x16x32_bf16 v[0:3], v[156:159], v[194:197], v[0:3]
	v_mfma_f32_16x16x32_bf16 v[4:7], v[140:143], v[194:197], v[4:7]
	s_barrier
	s_add_i32 s61, s61, 2
	s_add_u32 s59, s59, 0x100
	s_addc_u32 s60, s60, 0
	s_cmp_gt_u32 s61, 29
	s_mov_b64 s[36:37], s[30:31]
	s_cbranch_scc0 .LBB0_603
	s_and_b64 vcc, exec, s[20:21]
	s_cbranch_vccz .LBB0_606
	s_barrier

.LBB0_743:
	s_cmp_lt_i32 s92, 5
	s_cselect_b64 s[4:5], -1, 0
	s_cmp_gt_i32 s93, 4
	s_cselect_b64 s[6:7], -1, 0
	s_and_b64 s[4:5], s[4:5], s[6:7]
	s_andn2_b64 vcc, exec, s[4:5]
	s_cbranch_vccnz .LBB0_817
	v_mbcnt_lo_u32_b32 v0, -1, 0
	s_and_b32 s4, s3, 0xffffffc0
	s_waitcnt vmcnt(1)
	v_mbcnt_hi_u32_b32 v198, -1, v0
	v_add_u32_e32 v0, s4, v198
	s_nop 0
	v_readfirstlane_b32 s5, v0
	s_ashr_i32 s11, s5, 6
	s_cmpk_gt_i32 s87, 0x15ff
	s_cbranch_scc1 .LBB0_763
	v_bfe_i32 v3, v0, 27, 1
	s_waitcnt lgkmcnt(0)
	v_lshlrev_b32_e32 v1, 4, v0
	v_lshrrev_b32_e32 v3, 22, v3
	v_add_u32_e32 v3, v1, v3
	v_and_b32_e32 v3, 0xfffffc00, v3
	v_sub_u32_e32 v3, v1, v3
	v_ashrrev_i32_e32 v2, 31, v0
	v_lshrrev_b32_e32 v4, 4, v3
	v_lshrrev_b32_e32 v2, 26, v2
	v_bitop3_b32 v3, v4, v3, 32 bitop3:0x6c
	v_add_u32_e32 v2, v0, v2
	v_ashrrev_i32_e32 v5, 31, v3
	v_ashrrev_i32_e32 v2, 6, v2
	v_lshrrev_b32_e32 v5, 26, v5
	v_lshlrev_b32_e32 v4, 3, v2
	v_add_u32_e32 v5, v3, v5
	v_and_b32_e32 v4, -16, v4
	v_ashrrev_i32_e32 v6, 6, v5
	v_and_b32_e32 v5, 0xc0, v5
	v_add_u32_e32 v4, v6, v4
	v_sub_u32_e32 v3, v3, v5
	v_mov_b32_e32 v5, 1
	v_lshlrev_b32_e32 v2, 5, v2
	v_ashrrev_i16_sdwa v3, v5, sext(v3) dst_sel:DWORD dst_unused:UNUSED_PAD src0_sel:DWORD src1_sel:BYTE_0
	v_lshlrev_b32_e32 v7, 1, v4
	v_lshrrev_b32_e32 v8, 2, v4
	v_and_b32_e32 v6, 3, v6
	s_mov_b32 s4, 0x1fffe0
	v_and_b32_e32 v2, 32, v2
	v_bfe_i32 v3, v3, 0, 16
	v_and_b32_e32 v7, 24, v7
	v_and_b32_e32 v8, 4, v8
	v_and_or_b32 v6, v4, s4, v6
	v_or3_b32 v6, v6, v8, v7
	v_add_lshl_u32 v2, v2, v3, 1
	v_add_u32_e32 v1, 0x2000, v1
	s_waitcnt vmcnt(0)
	v_lshl_add_u32 v199, v4, 11, v2
	v_lshl_add_u32 v200, v6, 11, v2
	v_ashrrev_i32_e32 v2, 31, v1
	v_lshrrev_b32_e32 v2, 22, v2
	v_add_u32_e32 v2, v1, v2
	v_ashrrev_i32_e32 v2, 10, v2
	v_mul_i32_i24_e32 v3, 0x400, v2
	v_sub_u32_e32 v1, v1, v3
	v_lshrrev_b32_e32 v3, 4, v1
	s_add_u32 s40, s70, 0x62800000
	v_bitop3_b32 v1, v3, v1, 32 bitop3:0x6c
	s_addc_u32 s41, s71, 0
	v_ashrrev_i32_e32 v4, 31, v1
	s_add_u32 s42, s70, 0x2e00000
	v_lshrrev_b32_e32 v4, 26, v4
	s_addc_u32 s43, s71, 0
	v_lshlrev_b32_e32 v3, 3, v2
	v_add_u32_e32 v4, v1, v4
	s_add_u32 s44, s70, 0x100000
	v_and_b32_e32 v3, -16, v3
	v_ashrrev_i32_e32 v6, 6, v4
	s_addc_u32 s45, s71, 0
	v_add_u32_e32 v3, v6, v3
	v_and_b32_e32 v6, 3, v6
	s_ashr_i32 s47, s87, 31
	v_and_or_b32 v6, v3, s4, v6
	s_lshr_b32 s4, s47, 29
	s_add_i32 s4, s87, s4
	s_lshl_b32 s8, s11, 10
	s_ashr_i32 s6, s4, 3
	s_and_b32 s4, s4, -8
	s_ashr_i32 s10, s5, 8
	s_add_i32 s46, s8, 0
	s_sub_i32 s4, s87, s4
	s_cmp_lt_i32 s4, 0
	s_movk_i32 s48, 0x2c1
	s_cselect_b32 s7, s48, 0x2c0
	s_mul_i32 s4, s4, s7
	s_add_i32 s4, s4, s6
	s_mul_hi_i32 s6, s4, 0x2e8ba2e9
	s_lshr_b32 s7, s6, 31
	s_ashr_i32 s6, s6, 6
	s_add_i32 s6, s6, s7
	s_lshl_b32 s7, s6, 3
	s_mulk_i32 s6, 0x160
	s_sub_i32 s6, s4, s6
	s_sext_i32_i16 s4, s6
	s_bfe_u32 s4, s4, 0x3001c
	s_add_i32 s9, s6, s4
	s_sext_i32_i16 s4, s9
	s_and_b32 s9, s9, 0xfff8
	s_sub_i32 s6, s6, s9
	s_sext_i32_i16 s6, s6
	s_add_i32 s22, s7, s6
	s_ashr_i32 s23, s22, 31
	s_lshr_b32 s4, s4, 3
	s_lshl_b64 s[6:7], s[22:23], 19
	s_add_u32 s28, s40, s6
	s_addc_u32 s29, s41, s7
	s_bfe_i64 s[6:7], s[4:5], 0x100000
	s_lshl_b64 s[6:7], s[6:7], 19
	s_add_u32 s24, s42, s6
	s_addc_u32 s25, s43, s7
	s_and_b32 s49, s8, 0x400
	v_and_b32_e32 v4, 0xc0, v4
	s_add_i32 s6, s49, 0
	v_sub_u32_e32 v1, v1, v4
	s_add_i32 s8, s6, 0x20000
	s_lshl_b64 s[6:7], s[22:23], 11
	v_lshlrev_b32_e32 v2, 5, v2
	v_ashrrev_i16_sdwa v1, v5, sext(v1) dst_sel:DWORD dst_unused:UNUSED_PAD src0_sel:DWORD src1_sel:BYTE_0
	v_lshlrev_b32_e32 v4, 1, v3
	v_lshrrev_b32_e32 v5, 2, v3
	s_add_u32 s6, s44, s6
	v_and_b32_e32 v2, 32, v2
	v_bfe_i32 v1, v1, 0, 16
	v_and_b32_e32 v4, 24, v4
	v_and_b32_e32 v5, 4, v5
	s_addc_u32 s7, s45, s7
	v_lshl_add_u32 v203, v198, 4, s49
	s_add_i32 m0, s8, 0
	s_nop 0
	global_load_lds_dwordx4 v203, s[6:7]
	v_or3_b32 v4, v6, v5, v4
	v_add_lshl_u32 v1, v2, v1, 1
	s_add_i32 m0, s46, 0x10000
	s_nop 0
	global_load_lds_dwordx4 v200, s[24:25]
	v_lshl_add_u32 v202, v4, 11, v1
	s_add_i32 m0, s46, 0x12000
	s_nop 0
	global_load_lds_dwordx4 v202, s[24:25]
	s_add_u32 s6, s24, 0x40000
	s_addc_u32 s7, s25, 0
	s_add_i32 m0, s46, 0x14000
	s_nop 0
	global_load_lds_dwordx4 v200, s[6:7]
	v_lshl_add_u32 v201, v3, 11, v1
	s_add_i32 m0, s46, 0x16000
	s_nop 0
	global_load_lds_dwordx4 v202, s[6:7]
	s_add_i32 m0, s46, 0
	s_nop 0
	global_load_lds_dwordx4 v199, s[28:29]
	s_add_i32 m0, s46, 0x2000
	s_nop 0
	global_load_lds_dwordx4 v201, s[28:29]
	s_add_u32 s6, s28, 0x40000
	s_addc_u32 s7, s29, 0
	s_add_i32 m0, s46, 0x4000
	s_nop 0
	global_load_lds_dwordx4 v199, s[6:7]
	s_add_i32 m0, s46, 0x6000
	s_nop 0
	global_load_lds_dwordx4 v201, s[6:7]
	s_cmp_eq_u32 s10, 1
	s_cselect_b64 s[6:7], -1, 0
	s_cmp_lg_u32 s10, 1
	s_cbranch_scc1 .LBB0_747
	s_barrier

.LBB0_752:
	s_ashr_i32 s17, s16, 31
	s_lshl_b64 s[18:19], s[16:17], 19
	s_add_u32 s18, s40, s18
	s_addc_u32 s19, s41, s19
	s_and_b64 s[20:21], s[4:5], exec
	s_cselect_b32 s58, s19, s29
	s_cselect_b32 s59, s18, s28
	s_ashr_i32 s15, s14, 31
	s_lshl_b64 s[20:21], s[14:15], 19
	s_add_u32 s20, s42, s20
	s_addc_u32 s21, s43, s21
	s_and_b64 s[26:27], s[4:5], exec
	ds_read_b128 v[0:3], v204 offset:3072
	ds_read_b128 v[4:7], v204 offset:2048
	ds_read_b128 v[8:11], v204 offset:1024
	ds_read_b128 v[12:15], v204
	ds_read_b128 v[16:19], v205 offset:3072
	ds_read_b128 v[20:23], v205 offset:2048
	ds_read_b128 v[24:27], v205 offset:1024
	ds_read_b128 v[28:31], v205
	ds_read_b128 v[32:35], v206
	ds_read_b128 v[36:39], v206 offset:1024
	ds_read_b128 v[40:43], v206 offset:2048
	ds_read_b128 v[44:47], v206 offset:3072
	ds_read_b128 v[48:51], v206 offset:4096
	ds_read_b128 v[52:55], v206 offset:5120
	ds_read_b128 v[56:59], v206 offset:6144
	ds_read_b128 v[60:63], v206 offset:7168
	s_cselect_b32 s15, s21, s25
	s_cselect_b32 s60, s20, s24
	s_lshl_b32 s26, s55, 11
	s_and_b32 s26, s26, 0x800
	s_or_b32 s38, s26, s49
	s_lshl_b64 s[30:31], s[16:17], 11
	s_add_u32 s26, s28, 0x100
	s_addc_u32 s27, s29, 0
	s_add_u32 s62, s24, 0x100
	s_addc_u32 s63, s25, 0
	s_add_u32 s34, s28, 0x180
	s_addc_u32 s35, s29, 0
	s_add_u32 s36, s24, 0x180
	s_addc_u32 s37, s25, 0
	s_add_u32 s66, s28, 0x40080
	s_addc_u32 s67, s29, 0
	s_add_i32 m0, s46, 0xc000
	s_nop 0
	global_load_lds_dwordx4 v199, s[66:67]
	s_add_i32 m0, s46, 0xe000
	s_nop 0
	global_load_lds_dwordx4 v201, s[66:67]
	s_waitcnt vmcnt(8) lgkmcnt(0)
	s_barrier
	s_waitcnt lgkmcnt(7)
	v_mfma_i32_16x16x64_i8 v[64:67], v[28:31], v[32:35], 0
	s_mov_b32 s17, 0
	v_mfma_i32_16x16x64_i8 v[68:71], v[20:23], v[32:35], 0
	s_waitcnt lgkmcnt(5)
	v_mfma_i32_16x16x64_i8 v[72:75], v[28:31], v[40:43], 0
	v_mfma_i32_16x16x64_i8 v[132:135], v[24:27], v[36:39], v[64:67]
	v_mfma_i32_16x16x64_i8 v[136:139], v[16:19], v[36:39], v[68:71]
	s_waitcnt lgkmcnt(4)
	v_mfma_i32_16x16x64_i8 v[144:147], v[24:27], v[44:47], v[72:75]
	v_mfma_i32_16x16x64_i8 v[76:79], v[20:23], v[40:43], 0
	s_waitcnt lgkmcnt(3)
	v_mfma_i32_16x16x64_i8 v[80:83], v[28:31], v[48:51], 0
	v_mfma_i32_16x16x64_i8 v[84:87], v[20:23], v[48:51], 0
	s_waitcnt lgkmcnt(1)
	v_mfma_i32_16x16x64_i8 v[88:91], v[28:31], v[56:59], 0
	v_mfma_i32_16x16x64_i8 v[92:95], v[20:23], v[56:59], 0
	v_mfma_i32_16x16x64_i8 v[76:79], v[16:19], v[44:47], v[76:79]
	v_mfma_i32_16x16x64_i8 v[80:83], v[24:27], v[52:55], v[80:83]
	v_mfma_i32_16x16x64_i8 v[84:87], v[16:19], v[52:55], v[84:87]
	s_waitcnt lgkmcnt(0)
	v_mfma_i32_16x16x64_i8 v[88:91], v[24:27], v[60:63], v[88:91]
	v_mfma_i32_16x16x64_i8 v[92:95], v[16:19], v[60:63], v[92:95]
	v_mfma_i32_16x16x64_i8 v[96:99], v[12:15], v[32:35], 0
	v_mfma_i32_16x16x64_i8 v[32:35], v[4:7], v[32:35], 0
	v_mfma_i32_16x16x64_i8 v[96:99], v[8:11], v[36:39], v[96:99]
	v_mfma_i32_16x16x64_i8 v[32:35], v[0:3], v[36:39], v[32:35]
	v_mfma_i32_16x16x64_i8 v[36:39], v[12:15], v[40:43], 0
	v_mfma_i32_16x16x64_i8 v[40:43], v[4:7], v[40:43], 0
	v_mfma_i32_16x16x64_i8 v[36:39], v[8:11], v[44:47], v[36:39]
	v_mfma_i32_16x16x64_i8 v[40:43], v[0:3], v[44:47], v[40:43]
	v_mfma_i32_16x16x64_i8 v[44:47], v[12:15], v[48:51], 0
	v_mfma_i32_16x16x64_i8 v[48:51], v[4:7], v[48:51], 0
	v_mfma_i32_16x16x64_i8 v[44:47], v[8:11], v[52:55], v[44:47]
	v_mfma_i32_16x16x64_i8 v[48:51], v[0:3], v[52:55], v[48:51]
	v_mfma_i32_16x16x64_i8 v[52:55], v[12:15], v[56:59], 0
	v_mfma_i32_16x16x64_i8 v[56:59], v[4:7], v[56:59], 0
	v_mfma_i32_16x16x64_i8 v[52:55], v[8:11], v[60:63], v[52:55]
	v_mfma_i32_16x16x64_i8 v[56:59], v[0:3], v[60:63], v[56:59]
	s_barrier
	ds_read_b128 v[60:63], v206 offset:16384
	ds_read_b128 v[100:103], v206 offset:17408
	ds_read_b128 v[104:107], v206 offset:18432
	ds_read_b128 v[108:111], v206 offset:19456
	ds_read_b128 v[112:115], v206 offset:20480
	ds_read_b128 v[116:119], v206 offset:21504
	ds_read_b128 v[120:123], v206 offset:22528
	ds_read_b128 v[124:127], v206 offset:23552
	s_add_i32 m0, s46, 0x10000
	s_nop 0
	global_load_lds_dwordx4 v200, s[62:63]
	s_add_i32 m0, s46, 0x12000
	s_nop 0
	global_load_lds_dwordx4 v202, s[62:63]
	s_add_u32 s62, s24, 0x40100
	s_addc_u32 s63, s25, 0
	s_add_i32 m0, s46, 0x14000
	s_nop 0
	global_load_lds_dwordx4 v200, s[62:63]
	s_add_i32 m0, s46, 0x16000
	s_nop 0
	global_load_lds_dwordx4 v202, s[62:63]
	s_add_i32 m0, s46, 0
	s_nop 0
	global_load_lds_dwordx4 v199, s[26:27]
	s_add_i32 m0, s46, 0x2000
	s_nop 0
	global_load_lds_dwordx4 v201, s[26:27]
	s_waitcnt vmcnt(8) lgkmcnt(0)
	s_barrier
	v_mfma_i32_16x16x64_i8 v[128:131], v[28:31], v[60:63], 0
	v_mfma_i32_16x16x64_i8 v[210:213], v[24:27], v[100:103], v[128:131]
	v_mfma_i32_16x16x64_i8 v[128:131], v[20:23], v[60:63], 0
	v_mfma_i32_16x16x64_i8 v[214:217], v[16:19], v[100:103], v[128:131]
	v_mfma_i32_16x16x64_i8 v[128:131], v[28:31], v[104:107], 0
	v_mfma_i32_16x16x64_i8 v[218:221], v[24:27], v[108:111], v[128:131]
	v_mfma_i32_16x16x64_i8 v[128:131], v[20:23], v[104:107], 0
	v_mfma_i32_16x16x64_i8 v[222:225], v[16:19], v[108:111], v[128:131]
	v_mfma_i32_16x16x64_i8 v[128:131], v[28:31], v[112:115], 0
	v_mfma_i32_16x16x64_i8 v[226:229], v[24:27], v[116:119], v[128:131]
	v_mfma_i32_16x16x64_i8 v[128:131], v[20:23], v[112:115], 0
	v_mfma_i32_16x16x64_i8 v[28:31], v[28:31], v[120:123], 0
	v_mfma_i32_16x16x64_i8 v[20:23], v[20:23], v[120:123], 0
	v_mfma_i32_16x16x64_i8 v[230:233], v[16:19], v[116:119], v[128:131]
	v_mfma_i32_16x16x64_i8 v[24:27], v[24:27], v[124:127], v[28:31]
	v_mfma_i32_16x16x64_i8 v[20:23], v[16:19], v[124:127], v[20:23]
	v_mfma_i32_16x16x64_i8 v[16:19], v[12:15], v[60:63], 0
	v_mfma_i32_16x16x64_i8 v[28:31], v[8:11], v[100:103], v[16:19]
	v_mfma_i32_16x16x64_i8 v[16:19], v[4:7], v[60:63], 0
	v_mfma_i32_16x16x64_i8 v[60:63], v[0:3], v[100:103], v[16:19]
	v_mfma_i32_16x16x64_i8 v[16:19], v[12:15], v[104:107], 0
	v_mfma_i32_16x16x64_i8 v[100:103], v[8:11], v[108:111], v[16:19]
	v_mfma_i32_16x16x64_i8 v[16:19], v[4:7], v[104:107], 0
	v_mfma_i32_16x16x64_i8 v[234:237], v[0:3], v[108:111], v[16:19]
	v_mfma_i32_16x16x64_i8 v[16:19], v[12:15], v[112:115], 0
	v_mfma_i32_16x16x64_i8 v[238:241], v[8:11], v[116:119], v[16:19]
	v_mfma_i32_16x16x64_i8 v[16:19], v[4:7], v[112:115], 0
	v_mfma_i32_16x16x64_i8 v[12:15], v[12:15], v[120:123], 0
	v_mfma_i32_16x16x64_i8 v[4:7], v[4:7], v[120:123], 0
	v_mfma_i32_16x16x64_i8 v[12:15], v[8:11], v[124:127], v[12:15]
	v_mfma_i32_16x16x64_i8 v[4:7], v[0:3], v[124:127], v[4:7]
	v_mfma_i32_16x16x64_i8 v[242:245], v[0:3], v[116:119], v[16:19]
	s_barrier
	ds_read_b128 v[0:3], v207
	ds_read_b128 v[8:11], v207 offset:1024
	ds_read_b128 v[108:111], v207 offset:2048
	ds_read_b128 v[116:119], v207 offset:3072
	ds_read_b128 v[246:249], v208
	ds_read_b128 v[250:253], v208 offset:1024
	ds_read_b128 v[192:195], v208 offset:2048
	ds_read_b128 v[64:67], v208 offset:3072
	ds_read_b128 v[16:19], v206 offset:32768
	ds_read_b128 v[104:107], v206 offset:33792
	ds_read_b128 v[112:115], v206 offset:34816
	ds_read_b128 v[120:123], v206 offset:35840
	ds_read_b128 v[124:127], v206 offset:36864
	ds_read_b128 v[140:143], v206 offset:37888
	ds_read_b128 v[68:71], v206 offset:38912
	ds_read_b128 v[72:75], v206 offset:39936
	s_add_u32 s28, s28, 0x40100
	s_addc_u32 s29, s29, 0
	s_add_i32 m0, s46, 0x4000
	s_nop 0
	global_load_lds_dwordx4 v199, s[28:29]
	s_add_i32 m0, s46, 0x6000
	s_nop 0
	global_load_lds_dwordx4 v201, s[28:29]
	s_waitcnt vmcnt(8) lgkmcnt(0)
	s_barrier
	v_mfma_i32_16x16x64_i8 v[76:79], v[108:111], v[112:115], v[76:79]
	v_mfma_i32_16x16x64_i8 v[128:131], v[0:3], v[16:19], v[132:135]
	v_mfma_i32_16x16x64_i8 v[160:163], v[116:119], v[120:123], v[76:79]
	v_mfma_i32_16x16x64_i8 v[76:79], v[0:3], v[124:127], v[80:83]
	v_mfma_i32_16x16x64_i8 v[184:187], v[8:11], v[104:107], v[128:131]
	v_mfma_i32_16x16x64_i8 v[128:131], v[108:111], v[16:19], v[136:139]
	v_mfma_i32_16x16x64_i8 v[152:155], v[8:11], v[140:143], v[76:79]
	v_mfma_i32_16x16x64_i8 v[76:79], v[108:111], v[124:127], v[84:87]
	v_mfma_i32_16x16x64_i8 v[176:179], v[116:119], v[104:107], v[128:131]
	v_mfma_i32_16x16x64_i8 v[128:131], v[0:3], v[112:115], v[144:147]
	v_mfma_i32_16x16x64_i8 v[144:147], v[116:119], v[140:143], v[76:79]
	v_mfma_i32_16x16x64_i8 v[76:79], v[0:3], v[68:71], v[88:91]
	v_mfma_i32_16x16x64_i8 v[136:139], v[8:11], v[72:75], v[76:79]
	v_mfma_i32_16x16x64_i8 v[76:79], v[108:111], v[68:71], v[92:95]
	v_mfma_i32_16x16x64_i8 v[168:171], v[8:11], v[120:123], v[128:131]
	v_mfma_i32_16x16x64_i8 v[128:131], v[116:119], v[72:75], v[76:79]
	v_mfma_i32_16x16x64_i8 v[76:79], v[246:249], v[16:19], v[96:99]
	v_mfma_i32_16x16x64_i8 v[16:19], v[192:195], v[16:19], v[32:35]
	v_mfma_i32_16x16x64_i8 v[180:183], v[64:67], v[104:107], v[16:19]
	v_mfma_i32_16x16x64_i8 v[16:19], v[246:249], v[112:115], v[36:39]
	v_mfma_i32_16x16x64_i8 v[172:175], v[250:253], v[120:123], v[16:19]
	v_mfma_i32_16x16x64_i8 v[16:19], v[192:195], v[112:115], v[40:43]
	v_mfma_i32_16x16x64_i8 v[164:167], v[64:67], v[120:123], v[16:19]
	v_mfma_i32_16x16x64_i8 v[16:19], v[246:249], v[124:127], v[44:47]
	v_mfma_i32_16x16x64_i8 v[156:159], v[250:253], v[140:143], v[16:19]
	v_mfma_i32_16x16x64_i8 v[16:19], v[192:195], v[124:127], v[48:51]
	v_mfma_i32_16x16x64_i8 v[148:151], v[64:67], v[140:143], v[16:19]
	v_mfma_i32_16x16x64_i8 v[16:19], v[246:249], v[68:71], v[52:55]
	v_mfma_i32_16x16x64_i8 v[140:143], v[250:253], v[72:75], v[16:19]
	v_mfma_i32_16x16x64_i8 v[16:19], v[192:195], v[68:71], v[56:59]
	v_mfma_i32_16x16x64_i8 v[188:191], v[250:253], v[104:107], v[76:79]
	v_mfma_i32_16x16x64_i8 v[132:135], v[64:67], v[72:75], v[16:19]
	s_barrier
	ds_read_b128 v[32:35], v206 offset:49152
	ds_read_b128 v[36:39], v206 offset:50176
	ds_read_b128 v[40:43], v206 offset:51200
	ds_read_b128 v[44:47], v206 offset:52224
	ds_read_b128 v[52:55], v206 offset:53248
	ds_read_b128 v[56:59], v206 offset:54272
	ds_read_b128 v[68:71], v206 offset:55296
	ds_read_b128 v[72:75], v206 offset:56320
	s_add_i32 m0, s46, 0x18000
	s_nop 0
	global_load_lds_dwordx4 v200, s[36:37]
	s_add_i32 m0, s46, 0x1a000
	s_nop 0
	global_load_lds_dwordx4 v202, s[36:37]
	s_add_u32 s28, s24, 0x40180
	s_addc_u32 s29, s25, 0
	s_add_i32 m0, s46, 0x1c000
	s_nop 0
	global_load_lds_dwordx4 v200, s[28:29]
	s_add_i32 m0, s46, 0x1e000
	s_nop 0
	global_load_lds_dwordx4 v202, s[28:29]
	s_add_i32 m0, s46, 0x8000
	s_nop 0
	global_load_lds_dwordx4 v199, s[34:35]
	s_add_i32 m0, s46, 0xa000
	s_nop 0
	global_load_lds_dwordx4 v201, s[34:35]
	s_waitcnt vmcnt(8) lgkmcnt(0)
	s_barrier
	v_mfma_i32_16x16x64_i8 v[16:19], v[0:3], v[32:35], v[210:213]
	v_mfma_i32_16x16x64_i8 v[120:123], v[8:11], v[36:39], v[16:19]
	v_mfma_i32_16x16x64_i8 v[16:19], v[108:111], v[32:35], v[214:217]
	v_mfma_i32_16x16x64_i8 v[112:115], v[116:119], v[36:39], v[16:19]
	v_mfma_i32_16x16x64_i8 v[16:19], v[0:3], v[40:43], v[218:221]
	v_mfma_i32_16x16x64_i8 v[104:107], v[8:11], v[44:47], v[16:19]
	v_mfma_i32_16x16x64_i8 v[16:19], v[108:111], v[40:43], v[222:225]
	v_mfma_i32_16x16x64_i8 v[96:99], v[116:119], v[44:47], v[16:19]
	v_mfma_i32_16x16x64_i8 v[16:19], v[0:3], v[52:55], v[226:229]
	v_mfma_i32_16x16x64_i8 v[0:3], v[0:3], v[68:71], v[24:27]
	v_mfma_i32_16x16x64_i8 v[48:51], v[8:11], v[56:59], v[16:19]
	v_mfma_i32_16x16x64_i8 v[16:19], v[108:111], v[52:55], v[230:233]
	v_mfma_i32_16x16x64_i8 v[8:11], v[8:11], v[72:75], v[0:3]
	v_mfma_i32_16x16x64_i8 v[0:3], v[108:111], v[68:71], v[20:23]
	v_mfma_i32_16x16x64_i8 v[16:19], v[116:119], v[56:59], v[16:19]
	v_mfma_i32_16x16x64_i8 v[0:3], v[116:119], v[72:75], v[0:3]
	v_mfma_i32_16x16x64_i8 v[20:23], v[246:249], v[32:35], v[28:31]
	v_mfma_i32_16x16x64_i8 v[124:127], v[250:253], v[36:39], v[20:23]
	v_mfma_i32_16x16x64_i8 v[20:23], v[192:195], v[32:35], v[60:63]
	v_mfma_i32_16x16x64_i8 v[116:119], v[64:67], v[36:39], v[20:23]
	v_mfma_i32_16x16x64_i8 v[20:23], v[246:249], v[40:43], v[100:103]
	v_mfma_i32_16x16x64_i8 v[108:111], v[250:253], v[44:47], v[20:23]
	v_mfma_i32_16x16x64_i8 v[20:23], v[192:195], v[40:43], v[234:237]
	v_mfma_i32_16x16x64_i8 v[100:103], v[64:67], v[44:47], v[20:23]
	v_mfma_i32_16x16x64_i8 v[20:23], v[246:249], v[52:55], v[238:241]
	v_mfma_i32_16x16x64_i8 v[60:63], v[250:253], v[56:59], v[20:23]
	v_mfma_i32_16x16x64_i8 v[20:23], v[192:195], v[52:55], v[242:245]
	v_mfma_i32_16x16x64_i8 v[12:15], v[246:249], v[68:71], v[12:15]
	v_mfma_i32_16x16x64_i8 v[4:7], v[192:195], v[68:71], v[4:7]
	v_mfma_i32_16x16x64_i8 v[44:47], v[64:67], v[56:59], v[20:23]
	v_mfma_i32_16x16x64_i8 v[12:15], v[250:253], v[72:75], v[12:15]
	v_mfma_i32_16x16x64_i8 v[4:7], v[64:67], v[72:75], v[4:7]
	s_barrier
	s_add_u32 s28, s44, s30
	s_addc_u32 s29, s45, s31
	s_add_u32 s61, s24, 0x200
	s_addc_u32 s62, s25, 0
	s_add_i32 s63, s38, 0
	s_add_i32 s63, s63, 0x20000

.LBB0_755:
	ds_read_b128 v[20:23], v205
	ds_read_b128 v[24:27], v205 offset:1024
	ds_read_b128 v[28:31], v205 offset:2048
	ds_read_b128 v[32:35], v205 offset:3072
	ds_read_b128 v[36:39], v204
	ds_read_b128 v[40:43], v204 offset:1024
	ds_read_b128 v[52:55], v204 offset:2048
	ds_read_b128 v[56:59], v204 offset:3072
	ds_read_b128 v[64:67], v206
	ds_read_b128 v[68:71], v206 offset:1024
	ds_read_b128 v[72:75], v206 offset:2048
	ds_read_b128 v[76:79], v206 offset:3072
	ds_read_b128 v[80:83], v206 offset:4096
	ds_read_b128 v[84:87], v206 offset:5120
	ds_read_b128 v[88:91], v206 offset:6144
	ds_read_b128 v[92:95], v206 offset:7168
	s_add_u32 s24, s26, 0x100
	s_addc_u32 s25, s27, 0
	s_and_b64 s[30:31], s[30:31], exec
	s_cselect_b32 s38, s59, s24
	s_cselect_b32 s39, s58, s25
	s_cselect_b32 s35, s15, s62
	s_cselect_b32 s34, s60, s61
	s_add_u32 s30, s38, 0x80
	s_addc_u32 s31, s39, 0
	s_add_u32 s36, s34, 0x80
	s_addc_u32 s37, s35, 0
	s_add_u32 s26, s26, 0x40080
	s_addc_u32 s27, s27, 0
	s_add_i32 m0, s46, 0xc000
	s_nop 0
	global_load_lds_dwordx4 v199, s[26:27]
	s_add_i32 m0, s46, 0xe000
	s_nop 0
	global_load_lds_dwordx4 v201, s[26:27]
	s_waitcnt vmcnt(8) lgkmcnt(0)
	s_barrier
	v_mfma_i32_16x16x64_i8 v[184:187], v[20:23], v[64:67], v[184:187]
	v_mfma_i32_16x16x64_i8 v[176:179], v[28:31], v[64:67], v[176:179]
	v_mfma_i32_16x16x64_i8 v[160:163], v[28:31], v[72:75], v[160:163]
	v_mfma_i32_16x16x64_i8 v[168:171], v[20:23], v[72:75], v[168:171]
	v_mfma_i32_16x16x64_i8 v[152:155], v[20:23], v[80:83], v[152:155]
	v_mfma_i32_16x16x64_i8 v[144:147], v[28:31], v[80:83], v[144:147]
	v_mfma_i32_16x16x64_i8 v[128:131], v[28:31], v[88:91], v[128:131]
	v_mfma_i32_16x16x64_i8 v[136:139], v[20:23], v[88:91], v[136:139]
	v_mfma_i32_16x16x64_i8 v[184:187], v[24:27], v[68:71], v[184:187]
	v_mfma_i32_16x16x64_i8 v[176:179], v[32:35], v[68:71], v[176:179]
	v_mfma_i32_16x16x64_i8 v[160:163], v[32:35], v[76:79], v[160:163]
	v_mfma_i32_16x16x64_i8 v[168:171], v[24:27], v[76:79], v[168:171]
	v_mfma_i32_16x16x64_i8 v[152:155], v[24:27], v[84:87], v[152:155]
	v_mfma_i32_16x16x64_i8 v[144:147], v[32:35], v[84:87], v[144:147]
	v_mfma_i32_16x16x64_i8 v[128:131], v[32:35], v[92:95], v[128:131]
	v_mfma_i32_16x16x64_i8 v[136:139], v[24:27], v[92:95], v[136:139]
	v_mfma_i32_16x16x64_i8 v[188:191], v[36:39], v[64:67], v[188:191]
	v_mfma_i32_16x16x64_i8 v[64:67], v[52:55], v[64:67], v[180:183]
	v_mfma_i32_16x16x64_i8 v[188:191], v[40:43], v[68:71], v[188:191]
	v_mfma_i32_16x16x64_i8 v[64:67], v[56:59], v[68:71], v[64:67]
	v_mfma_i32_16x16x64_i8 v[68:71], v[36:39], v[72:75], v[172:175]
	v_mfma_i32_16x16x64_i8 v[72:75], v[52:55], v[72:75], v[164:167]
	v_mfma_i32_16x16x64_i8 v[68:71], v[40:43], v[76:79], v[68:71]
	v_mfma_i32_16x16x64_i8 v[72:75], v[56:59], v[76:79], v[72:75]
	v_mfma_i32_16x16x64_i8 v[76:79], v[36:39], v[80:83], v[156:159]
	v_mfma_i32_16x16x64_i8 v[80:83], v[52:55], v[80:83], v[148:151]
	v_mfma_i32_16x16x64_i8 v[76:79], v[40:43], v[84:87], v[76:79]
	v_mfma_i32_16x16x64_i8 v[80:83], v[56:59], v[84:87], v[80:83]
	v_mfma_i32_16x16x64_i8 v[84:87], v[36:39], v[88:91], v[140:143]
	v_mfma_i32_16x16x64_i8 v[88:91], v[52:55], v[88:91], v[132:135]
	v_mfma_i32_16x16x64_i8 v[84:87], v[40:43], v[92:95], v[84:87]
	v_mfma_i32_16x16x64_i8 v[88:91], v[56:59], v[92:95], v[88:91]
	s_barrier
	ds_read_b128 v[92:95], v206 offset:16384
	ds_read_b128 v[132:135], v206 offset:17408
	ds_read_b128 v[140:143], v206 offset:18432
	ds_read_b128 v[148:151], v206 offset:19456
	ds_read_b128 v[156:159], v206 offset:20480
	ds_read_b128 v[164:167], v206 offset:21504
	ds_read_b128 v[172:175], v206 offset:22528
	ds_read_b128 v[180:183], v206 offset:23552
	s_add_i32 m0, s46, 0x10000
	s_nop 0
	global_load_lds_dwordx4 v200, s[34:35]
	s_add_i32 m0, s46, 0x12000
	s_nop 0
	global_load_lds_dwordx4 v202, s[34:35]
	s_add_u32 s26, s34, 0x40000
	s_addc_u32 s27, s35, 0
	s_add_i32 m0, s46, 0x14000
	s_nop 0
	global_load_lds_dwordx4 v200, s[26:27]
	s_add_i32 m0, s46, 0x16000
	s_nop 0
	global_load_lds_dwordx4 v202, s[26:27]
	s_add_i32 m0, s46, 0
	s_nop 0
	global_load_lds_dwordx4 v199, s[38:39]
	s_add_i32 m0, s46, 0x2000
	s_nop 0
	global_load_lds_dwordx4 v201, s[38:39]
	s_waitcnt vmcnt(8) lgkmcnt(0)
	s_barrier
	v_mfma_i32_16x16x64_i8 v[120:123], v[20:23], v[92:95], v[120:123]
	v_mfma_i32_16x16x64_i8 v[112:115], v[28:31], v[92:95], v[112:115]
	v_mfma_i32_16x16x64_i8 v[96:99], v[28:31], v[140:143], v[96:99]
	v_mfma_i32_16x16x64_i8 v[104:107], v[20:23], v[140:143], v[104:107]
	v_mfma_i32_16x16x64_i8 v[48:51], v[20:23], v[156:159], v[48:51]
	v_mfma_i32_16x16x64_i8 v[16:19], v[28:31], v[156:159], v[16:19]
	v_mfma_i32_16x16x64_i8 v[0:3], v[28:31], v[172:175], v[0:3]
	v_mfma_i32_16x16x64_i8 v[8:11], v[20:23], v[172:175], v[8:11]
	v_mfma_i32_16x16x64_i8 v[120:123], v[24:27], v[132:135], v[120:123]
	v_mfma_i32_16x16x64_i8 v[112:115], v[32:35], v[132:135], v[112:115]
	v_mfma_i32_16x16x64_i8 v[96:99], v[32:35], v[148:151], v[96:99]
	v_mfma_i32_16x16x64_i8 v[104:107], v[24:27], v[148:151], v[104:107]
	v_mfma_i32_16x16x64_i8 v[48:51], v[24:27], v[164:167], v[48:51]
	v_mfma_i32_16x16x64_i8 v[16:19], v[32:35], v[164:167], v[16:19]
	v_mfma_i32_16x16x64_i8 v[0:3], v[32:35], v[180:183], v[0:3]
	v_mfma_i32_16x16x64_i8 v[8:11], v[24:27], v[180:183], v[8:11]
	v_mfma_i32_16x16x64_i8 v[20:23], v[36:39], v[92:95], v[124:127]
	v_mfma_i32_16x16x64_i8 v[124:127], v[40:43], v[132:135], v[20:23]
	v_mfma_i32_16x16x64_i8 v[20:23], v[52:55], v[92:95], v[116:119]
	v_mfma_i32_16x16x64_i8 v[116:119], v[56:59], v[132:135], v[20:23]
	v_mfma_i32_16x16x64_i8 v[20:23], v[36:39], v[140:143], v[108:111]
	v_mfma_i32_16x16x64_i8 v[108:111], v[40:43], v[148:151], v[20:23]
	v_mfma_i32_16x16x64_i8 v[20:23], v[52:55], v[140:143], v[100:103]
	v_mfma_i32_16x16x64_i8 v[100:103], v[56:59], v[148:151], v[20:23]
	v_mfma_i32_16x16x64_i8 v[20:23], v[36:39], v[156:159], v[60:63]
	v_mfma_i32_16x16x64_i8 v[60:63], v[40:43], v[164:167], v[20:23]
	v_mfma_i32_16x16x64_i8 v[20:23], v[52:55], v[156:159], v[44:47]
	v_mfma_i32_16x16x64_i8 v[12:15], v[36:39], v[172:175], v[12:15]
	v_mfma_i32_16x16x64_i8 v[4:7], v[52:55], v[172:175], v[4:7]
	v_mfma_i32_16x16x64_i8 v[44:47], v[56:59], v[164:167], v[20:23]
	v_mfma_i32_16x16x64_i8 v[12:15], v[40:43], v[180:183], v[12:15]
	v_mfma_i32_16x16x64_i8 v[4:7], v[56:59], v[180:183], v[4:7]
	s_barrier
	ds_read_b128 v[36:39], v207
	ds_read_b128 v[28:31], v207 offset:1024
	ds_read_b128 v[24:27], v207 offset:2048
	ds_read_b128 v[20:23], v207 offset:3072
	ds_read_b128 v[56:59], v208
	ds_read_b128 v[52:55], v208 offset:1024
	ds_read_b128 v[40:43], v208 offset:2048
	ds_read_b128 v[32:35], v208 offset:3072
	ds_read_b128 v[92:95], v206 offset:32768
	ds_read_b128 v[132:135], v206 offset:33792
	ds_read_b128 v[140:143], v206 offset:34816
	ds_read_b128 v[148:151], v206 offset:35840
	ds_read_b128 v[192:195], v206 offset:36864
	ds_read_b128 v[210:213], v206 offset:37888
	ds_read_b128 v[214:217], v206 offset:38912
	ds_read_b128 v[218:221], v206 offset:39936
	s_add_u32 s26, s38, 0x40000
	s_addc_u32 s27, s39, 0
	s_add_i32 m0, s46, 0x4000
	s_nop 0
	global_load_lds_dwordx4 v199, s[26:27]
	s_add_i32 m0, s46, 0x6000
	s_nop 0
	global_load_lds_dwordx4 v201, s[26:27]
	s_waitcnt vmcnt(8) lgkmcnt(0)
	s_barrier
	v_mfma_i32_16x16x64_i8 v[156:159], v[36:39], v[92:95], v[184:187]
	v_mfma_i32_16x16x64_i8 v[184:187], v[28:31], v[132:135], v[156:159]
	v_mfma_i32_16x16x64_i8 v[156:159], v[24:27], v[92:95], v[176:179]
	v_mfma_i32_16x16x64_i8 v[176:179], v[20:23], v[132:135], v[156:159]
	v_mfma_i32_16x16x64_i8 v[156:159], v[36:39], v[140:143], v[168:171]
	v_mfma_i32_16x16x64_i8 v[168:171], v[28:31], v[148:151], v[156:159]
	v_mfma_i32_16x16x64_i8 v[156:159], v[24:27], v[140:143], v[160:163]
	v_mfma_i32_16x16x64_i8 v[152:155], v[36:39], v[192:195], v[152:155]
	v_mfma_i32_16x16x64_i8 v[144:147], v[24:27], v[192:195], v[144:147]
	v_mfma_i32_16x16x64_i8 v[136:139], v[36:39], v[214:217], v[136:139]
	v_mfma_i32_16x16x64_i8 v[128:131], v[24:27], v[214:217], v[128:131]
	v_mfma_i32_16x16x64_i8 v[160:163], v[20:23], v[148:151], v[156:159]
	v_mfma_i32_16x16x64_i8 v[152:155], v[28:31], v[210:213], v[152:155]
	v_mfma_i32_16x16x64_i8 v[144:147], v[20:23], v[210:213], v[144:147]
	v_mfma_i32_16x16x64_i8 v[136:139], v[28:31], v[218:221], v[136:139]
	v_mfma_i32_16x16x64_i8 v[128:131], v[20:23], v[218:221], v[128:131]
	v_mfma_i32_16x16x64_i8 v[64:67], v[40:43], v[92:95], v[64:67]
	v_mfma_i32_16x16x64_i8 v[180:183], v[32:35], v[132:135], v[64:67]
	v_mfma_i32_16x16x64_i8 v[64:67], v[56:59], v[140:143], v[68:71]
	v_mfma_i32_16x16x64_i8 v[172:175], v[52:55], v[148:151], v[64:67]
	v_mfma_i32_16x16x64_i8 v[64:67], v[40:43], v[140:143], v[72:75]
	v_mfma_i32_16x16x64_i8 v[156:159], v[56:59], v[92:95], v[188:191]
	v_mfma_i32_16x16x64_i8 v[164:167], v[32:35], v[148:151], v[64:67]
	v_mfma_i32_16x16x64_i8 v[64:67], v[56:59], v[192:195], v[76:79]
	v_mfma_i32_16x16x64_i8 v[188:191], v[52:55], v[132:135], v[156:159]
	v_mfma_i32_16x16x64_i8 v[156:159], v[52:55], v[210:213], v[64:67]
	v_mfma_i32_16x16x64_i8 v[64:67], v[40:43], v[192:195], v[80:83]
	v_mfma_i32_16x16x64_i8 v[148:151], v[32:35], v[210:213], v[64:67]
	v_mfma_i32_16x16x64_i8 v[64:67], v[56:59], v[214:217], v[84:87]
	v_mfma_i32_16x16x64_i8 v[140:143], v[52:55], v[218:221], v[64:67]
	v_mfma_i32_16x16x64_i8 v[64:67], v[40:43], v[214:217], v[88:91]
	v_mfma_i32_16x16x64_i8 v[132:135], v[32:35], v[218:221], v[64:67]
	s_barrier
	ds_read_b128 v[92:95], v206 offset:49152
	ds_read_b128 v[88:91], v206 offset:50176
	ds_read_b128 v[84:87], v206 offset:51200
	ds_read_b128 v[80:83], v206 offset:52224
	ds_read_b128 v[76:79], v206 offset:53248
	ds_read_b128 v[72:75], v206 offset:54272
	ds_read_b128 v[68:71], v206 offset:55296
	ds_read_b128 v[64:67], v206 offset:56320
	s_add_i32 m0, s46, 0x18000
	s_nop 0
	global_load_lds_dwordx4 v200, s[36:37]
	s_add_i32 m0, s46, 0x1a000
	s_nop 0
	global_load_lds_dwordx4 v202, s[36:37]
	s_add_u32 s26, s34, 0x40080
	s_addc_u32 s27, s35, 0
	s_add_i32 m0, s46, 0x1c000
	s_nop 0
	global_load_lds_dwordx4 v200, s[26:27]
	s_add_i32 m0, s46, 0x1e000
	s_nop 0
	global_load_lds_dwordx4 v202, s[26:27]
	s_add_i32 m0, s46, 0x8000
	s_nop 0
	global_load_lds_dwordx4 v199, s[30:31]
	s_add_i32 m0, s46, 0xa000
	s_nop 0
	global_load_lds_dwordx4 v201, s[30:31]
	s_waitcnt vmcnt(8) lgkmcnt(0)
	s_barrier
	v_mfma_i32_16x16x64_i8 v[120:123], v[36:39], v[92:95], v[120:123]
	v_mfma_i32_16x16x64_i8 v[112:115], v[24:27], v[92:95], v[112:115]
	v_mfma_i32_16x16x64_i8 v[96:99], v[24:27], v[84:87], v[96:99]
	v_mfma_i32_16x16x64_i8 v[104:107], v[36:39], v[84:87], v[104:107]
	v_mfma_i32_16x16x64_i8 v[48:51], v[36:39], v[76:79], v[48:51]
	v_mfma_i32_16x16x64_i8 v[16:19], v[24:27], v[76:79], v[16:19]
	v_mfma_i32_16x16x64_i8 v[0:3], v[24:27], v[68:71], v[0:3]
	v_mfma_i32_16x16x64_i8 v[8:11], v[36:39], v[68:71], v[8:11]
	v_mfma_i32_16x16x64_i8 v[120:123], v[28:31], v[88:91], v[120:123]
	v_mfma_i32_16x16x64_i8 v[112:115], v[20:23], v[88:91], v[112:115]
	v_mfma_i32_16x16x64_i8 v[96:99], v[20:23], v[80:83], v[96:99]
	v_mfma_i32_16x16x64_i8 v[104:107], v[28:31], v[80:83], v[104:107]
	v_mfma_i32_16x16x64_i8 v[48:51], v[28:31], v[72:75], v[48:51]
	v_mfma_i32_16x16x64_i8 v[16:19], v[20:23], v[72:75], v[16:19]
	v_mfma_i32_16x16x64_i8 v[0:3], v[20:23], v[64:67], v[0:3]
	v_mfma_i32_16x16x64_i8 v[8:11], v[28:31], v[64:67], v[8:11]
	v_mfma_i32_16x16x64_i8 v[124:127], v[56:59], v[92:95], v[124:127]
	v_mfma_i32_16x16x64_i8 v[116:119], v[40:43], v[92:95], v[116:119]
	v_mfma_i32_16x16x64_i8 v[100:103], v[40:43], v[84:87], v[100:103]
	v_mfma_i32_16x16x64_i8 v[108:111], v[56:59], v[84:87], v[108:111]
	v_mfma_i32_16x16x64_i8 v[60:63], v[56:59], v[76:79], v[60:63]
	v_mfma_i32_16x16x64_i8 v[44:47], v[40:43], v[76:79], v[44:47]
	v_mfma_i32_16x16x64_i8 v[4:7], v[40:43], v[68:71], v[4:7]
	v_mfma_i32_16x16x64_i8 v[12:15], v[56:59], v[68:71], v[12:15]
	v_mfma_i32_16x16x64_i8 v[124:127], v[52:55], v[88:91], v[124:127]
	v_mfma_i32_16x16x64_i8 v[116:119], v[32:35], v[88:91], v[116:119]
	v_mfma_i32_16x16x64_i8 v[100:103], v[32:35], v[80:83], v[100:103]
	v_mfma_i32_16x16x64_i8 v[108:111], v[52:55], v[80:83], v[108:111]
	v_mfma_i32_16x16x64_i8 v[60:63], v[52:55], v[72:75], v[60:63]
	v_mfma_i32_16x16x64_i8 v[44:47], v[32:35], v[72:75], v[44:47]
	v_mfma_i32_16x16x64_i8 v[4:7], v[32:35], v[64:67], v[4:7]
	v_mfma_i32_16x16x64_i8 v[12:15], v[52:55], v[64:67], v[12:15]
	s_barrier
	s_add_i32 s17, s17, 2
	s_add_u32 s61, s61, 0x100
	s_addc_u32 s62, s62, 0
	s_cmp_gt_u32 s17, 13
	s_cbranch_scc1 .LBB0_757
	s_mov_b64 s[26:27], s[24:25]
	s_branch .LBB0_753

.LBB0_822:
	v_bfe_i32 v3, v0, 27, 1
	s_waitcnt lgkmcnt(0)
	v_lshlrev_b32_e32 v1, 4, v0
	v_lshrrev_b32_e32 v3, 22, v3
	v_add_u32_e32 v3, v1, v3
	v_and_b32_e32 v3, 0xfffffc00, v3
	v_sub_u32_e32 v3, v1, v3
	v_lshrrev_b32_e32 v4, 4, v3
	v_ashrrev_i32_e32 v2, 31, v0
	v_bitop3_b32 v3, v4, v3, 32 bitop3:0x6c
	v_lshrrev_b32_e32 v2, 26, v2
	v_ashrrev_i32_e32 v5, 31, v3
	v_add_u32_e32 v2, v0, v2
	v_lshrrev_b32_e32 v5, 26, v5
	v_ashrrev_i32_e32 v2, 6, v2
	v_add_u32_e32 v5, v3, v5
	v_lshlrev_b32_e32 v4, 3, v2
	v_ashrrev_i32_e32 v6, 6, v5
	v_and_b32_e32 v5, 0xc0, v5
	v_and_b32_e32 v4, -16, v4
	v_lshlrev_b32_e32 v2, 5, v2
	v_sub_u32_e32 v3, v3, v5
	v_mov_b32_e32 v5, 1
	v_add_u32_e32 v4, v6, v4
	v_and_b32_e32 v2, 32, v2
	v_ashrrev_i16_sdwa v3, v5, sext(v3) dst_sel:DWORD dst_unused:UNUSED_PAD src0_sel:DWORD src1_sel:BYTE_0
	v_add_u32_sdwa v2, v2, sext(v3) dst_sel:DWORD dst_unused:UNUSED_PAD src0_sel:DWORD src1_sel:WORD_0
	v_lshlrev_b32_e32 v3, 1, v4
	v_lshrrev_b32_e32 v7, 2, v4
	v_and_b32_e32 v6, 3, v6
	s_mov_b32 s4, 0x7fffe0
	v_and_b32_e32 v3, 24, v3
	v_and_b32_e32 v7, 4, v7
	v_and_or_b32 v6, v4, s4, v6
	v_or3_b32 v3, v6, v7, v3
	s_movk_i32 s5, 0x1600
	v_mul_lo_u32 v4, v4, s5
	v_mul_u32_u24_e32 v3, 0x1600, v3
	v_add_u32_e32 v1, 0x2000, v1
	v_add_lshl_u32 v175, v2, v4, 1
	v_add_lshl_u32 v176, v3, v2, 1
	v_ashrrev_i32_e32 v2, 31, v1
	v_lshrrev_b32_e32 v2, 22, v2
	v_add_u32_e32 v2, v1, v2
	v_ashrrev_i32_e32 v2, 10, v2
	v_mul_i32_i24_e32 v3, 0x400, v2
	v_sub_u32_e32 v1, v1, v3
	v_lshrrev_b32_e32 v3, 4, v1
	v_bitop3_b32 v1, v3, v1, 32 bitop3:0x6c
	v_ashrrev_i32_e32 v4, 31, v1
	v_lshrrev_b32_e32 v4, 26, v4
	v_add_u32_e32 v4, v1, v4
	s_add_u32 s30, s70, 0x3a800000
	v_lshlrev_b32_e32 v3, 3, v2
	v_ashrrev_i32_e32 v6, 6, v4
	v_and_b32_e32 v4, 0xc0, v4
	s_addc_u32 s31, s71, 0
	v_and_b32_e32 v3, -16, v3
	v_sub_u32_e32 v1, v1, v4
	s_add_u32 s34, s70, 0x5a00000
	v_add_u32_e32 v3, v6, v3
	v_lshlrev_b32_e32 v2, 5, v2
	v_ashrrev_i16_sdwa v1, v5, sext(v1) dst_sel:DWORD dst_unused:UNUSED_PAD src0_sel:DWORD src1_sel:BYTE_0
	v_and_b32_e32 v5, 3, v6
	s_addc_u32 s35, s71, 0
	v_and_b32_e32 v2, 32, v2
	v_and_or_b32 v5, v3, s4, v5
	s_lshl_b32 s4, s7, 10
	v_add_u32_sdwa v1, v2, sext(v1) dst_sel:DWORD dst_unused:UNUSED_PAD src0_sel:DWORD src1_sel:WORD_0
	v_lshlrev_b32_e32 v2, 1, v3
	v_lshrrev_b32_e32 v4, 2, v3
	v_mul_lo_u32 v3, v3, s5
	s_ashr_i32 s16, s6, 8
	s_add_i32 s36, s4, 0
	s_mul_i32 s5, s50, 0x2c0000
	s_mul_hi_i32 s4, s50, 0x2c0000
	s_add_u32 s22, s30, s5
	v_and_b32_e32 v2, 24, v2
	v_and_b32_e32 v4, 4, v4
	s_addc_u32 s23, s31, s4
	s_mul_i32 s5, s49, 0x2c0000
	v_or3_b32 v2, v5, v4, v2
	s_mul_hi_i32 s4, s49, 0x2c0000
	s_add_u32 s24, s34, s5
	v_mul_u32_u24_e32 v2, 0x1600, v2
	s_addc_u32 s25, s35, s4
	s_add_i32 m0, s36, 0x10000
	s_nop 0
	global_load_lds_dwordx4 v176, s[24:25]
	v_add_lshl_u32 v178, v2, v1, 1
	s_add_i32 m0, s36, 0x12000
	s_nop 0
	global_load_lds_dwordx4 v178, s[24:25]
	s_add_u32 s4, s24, 0x160000
	s_addc_u32 s5, s25, 0
	s_add_i32 m0, s36, 0x14000
	s_nop 0
	global_load_lds_dwordx4 v176, s[4:5]
	v_add_lshl_u32 v177, v1, v3, 1
	s_add_i32 m0, s36, 0x16000
	s_nop 0
	global_load_lds_dwordx4 v178, s[4:5]
	s_mov_b32 s37, 0
	s_add_i32 m0, s36, 0
	s_nop 0
	global_load_lds_dwordx4 v175, s[22:23]
	s_add_i32 m0, s36, 0x2000
	s_nop 0
	global_load_lds_dwordx4 v177, s[22:23]
	s_add_u32 s8, s22, 0x160000
	s_addc_u32 s9, s23, 0
	s_add_i32 m0, s36, 0x4000
	s_nop 0
	global_load_lds_dwordx4 v175, s[8:9]
	s_add_i32 m0, s36, 0x6000
	s_nop 0
	global_load_lds_dwordx4 v177, s[8:9]
	s_cmp_eq_u32 s16, 1
	s_cselect_b64 s[8:9], -1, 0
	s_cmp_lg_u32 s16, 1
	s_cbranch_scc1 .LBB0_824
	s_barrier

.LBB0_837:
	s_waitcnt lgkmcnt(0)
	ds_read_b128 v[0:3], v181
	ds_read_b128 v[4:7], v181 offset:1024
	ds_read_b128 v[8:11], v181 offset:2048
	ds_read_b128 v[12:15], v181 offset:3072
	ds_read_b128 v[16:19], v182
	ds_read_b128 v[20:23], v182 offset:1024
	ds_read_b128 v[24:27], v182 offset:2048
	ds_read_b128 v[28:31], v182 offset:3072
	ds_read_b128 v[32:35], v183
	ds_read_b128 v[36:39], v183 offset:1024
	ds_read_b128 v[40:43], v183 offset:2048
	ds_read_b128 v[44:47], v183 offset:3072
	ds_read_b128 v[48:51], v183 offset:4096
	ds_read_b128 v[52:55], v183 offset:5120
	ds_read_b128 v[56:59], v183 offset:6144
	ds_read_b128 v[60:63], v183 offset:7168
	s_add_u32 s28, s22, 0x100
	s_addc_u32 s29, s23, 0
	s_add_u32 s52, s24, 0x100
	s_addc_u32 s53, s25, 0
	s_add_u32 s6, s22, 0x180
	s_addc_u32 s7, s23, 0
	s_add_u32 s26, s24, 0x180
	s_addc_u32 s27, s25, 0
	s_add_u32 s54, s22, 0x160080
	s_addc_u32 s55, s23, 0
	s_add_i32 m0, s36, 0xc000
	s_nop 0
	global_load_lds_dwordx4 v175, s[54:55]
	s_add_i32 m0, s36, 0xe000
	s_nop 0
	global_load_lds_dwordx4 v177, s[54:55]
	s_waitcnt vmcnt(8) lgkmcnt(0)
	s_barrier
	v_mfma_f32_16x16x32_bf16 v[88:91], v[0:3], v[56:59], 0
	v_mfma_f32_16x16x32_bf16 v[64:67], v[0:3], v[32:35], 0
	v_mfma_f32_16x16x32_bf16 v[68:71], v[8:11], v[32:35], 0
	v_mfma_f32_16x16x32_bf16 v[72:75], v[0:3], v[40:43], 0
	v_mfma_f32_16x16x32_bf16 v[76:79], v[8:11], v[40:43], 0
	v_mfma_f32_16x16x32_bf16 v[80:83], v[0:3], v[48:51], 0
	v_mfma_f32_16x16x32_bf16 v[84:87], v[8:11], v[48:51], 0
	v_mfma_f32_16x16x32_bf16 v[96:99], v[4:7], v[60:63], v[88:91]
	v_mfma_f32_16x16x32_bf16 v[88:91], v[8:11], v[56:59], 0
	v_mfma_f32_16x16x32_bf16 v[64:67], v[4:7], v[36:39], v[64:67]
	v_mfma_f32_16x16x32_bf16 v[68:71], v[12:15], v[36:39], v[68:71]
	v_mfma_f32_16x16x32_bf16 v[72:75], v[4:7], v[44:47], v[72:75]
	v_mfma_f32_16x16x32_bf16 v[76:79], v[12:15], v[44:47], v[76:79]
	v_mfma_f32_16x16x32_bf16 v[80:83], v[4:7], v[52:55], v[80:83]
	v_mfma_f32_16x16x32_bf16 v[84:87], v[12:15], v[52:55], v[84:87]
	v_mfma_f32_16x16x32_bf16 v[100:103], v[12:15], v[60:63], v[88:91]
	v_mfma_f32_16x16x32_bf16 v[88:91], v[16:19], v[32:35], 0
	v_mfma_f32_16x16x32_bf16 v[32:35], v[24:27], v[32:35], 0
	v_mfma_f32_16x16x32_bf16 v[112:115], v[20:23], v[36:39], v[88:91]
	v_mfma_f32_16x16x32_bf16 v[32:35], v[28:31], v[36:39], v[32:35]
	v_mfma_f32_16x16x32_bf16 v[36:39], v[16:19], v[40:43], 0
	v_mfma_f32_16x16x32_bf16 v[40:43], v[24:27], v[40:43], 0
	v_mfma_f32_16x16x32_bf16 v[36:39], v[20:23], v[44:47], v[36:39]
	v_mfma_f32_16x16x32_bf16 v[40:43], v[28:31], v[44:47], v[40:43]
	v_mfma_f32_16x16x32_bf16 v[44:47], v[16:19], v[48:51], 0
	v_mfma_f32_16x16x32_bf16 v[48:51], v[24:27], v[48:51], 0
	v_mfma_f32_16x16x32_bf16 v[44:47], v[20:23], v[52:55], v[44:47]
	v_mfma_f32_16x16x32_bf16 v[48:51], v[28:31], v[52:55], v[48:51]
	v_mfma_f32_16x16x32_bf16 v[52:55], v[16:19], v[56:59], 0
	v_mfma_f32_16x16x32_bf16 v[56:59], v[24:27], v[56:59], 0
	v_mfma_f32_16x16x32_bf16 v[52:55], v[20:23], v[60:63], v[52:55]
	v_mfma_f32_16x16x32_bf16 v[56:59], v[28:31], v[60:63], v[56:59]
	s_barrier
	ds_read_b128 v[60:63], v183 offset:16384
	ds_read_b128 v[88:91], v183 offset:17408
	ds_read_b128 v[92:95], v183 offset:18432
	ds_read_b128 v[104:107], v183 offset:19456
	ds_read_b128 v[108:111], v183 offset:20480
	ds_read_b128 v[116:119], v183 offset:21504
	ds_read_b128 v[120:123], v183 offset:22528
	ds_read_b128 v[124:127], v183 offset:23552
	s_add_i32 m0, s36, 0x10000
	s_nop 0
	global_load_lds_dwordx4 v176, s[52:53]
	s_add_i32 m0, s36, 0x12000
	s_nop 0
	global_load_lds_dwordx4 v178, s[52:53]
	s_add_u32 s52, s24, 0x160100
	s_addc_u32 s53, s25, 0
	s_add_i32 m0, s36, 0x14000
	s_nop 0
	global_load_lds_dwordx4 v176, s[52:53]
	s_add_i32 m0, s36, 0x16000
	s_nop 0
	global_load_lds_dwordx4 v178, s[52:53]
	s_add_i32 m0, s36, 0
	s_nop 0
	global_load_lds_dwordx4 v175, s[28:29]
	s_add_i32 m0, s36, 0x2000
	s_nop 0
	global_load_lds_dwordx4 v177, s[28:29]
	s_waitcnt vmcnt(8) lgkmcnt(0)
	s_barrier
	v_mfma_f32_16x16x32_bf16 v[128:131], v[0:3], v[60:63], 0
	v_mfma_f32_16x16x32_bf16 v[136:139], v[4:7], v[88:91], v[128:131]
	v_mfma_f32_16x16x32_bf16 v[128:131], v[8:11], v[60:63], 0
	v_mfma_f32_16x16x32_bf16 v[140:143], v[12:15], v[88:91], v[128:131]
	v_mfma_f32_16x16x32_bf16 v[128:131], v[0:3], v[92:95], 0
	v_mfma_f32_16x16x32_bf16 v[144:147], v[4:7], v[104:107], v[128:131]
	v_mfma_f32_16x16x32_bf16 v[128:131], v[8:11], v[92:95], 0
	v_mfma_f32_16x16x32_bf16 v[148:151], v[12:15], v[104:107], v[128:131]
	v_mfma_f32_16x16x32_bf16 v[128:131], v[0:3], v[108:111], 0
	v_mfma_f32_16x16x32_bf16 v[0:3], v[0:3], v[120:123], 0
	v_mfma_f32_16x16x32_bf16 v[156:159], v[4:7], v[116:119], v[128:131]
	v_mfma_f32_16x16x32_bf16 v[0:3], v[4:7], v[124:127], v[0:3]
	v_mfma_f32_16x16x32_bf16 v[4:7], v[8:11], v[120:123], 0
	v_mfma_f32_16x16x32_bf16 v[128:131], v[8:11], v[108:111], 0
	v_mfma_f32_16x16x32_bf16 v[4:7], v[12:15], v[124:127], v[4:7]
	v_mfma_f32_16x16x32_bf16 v[160:163], v[12:15], v[116:119], v[128:131]
	v_mfma_f32_16x16x32_bf16 v[8:11], v[16:19], v[60:63], 0
	v_mfma_f32_16x16x32_bf16 v[164:167], v[20:23], v[88:91], v[8:11]
	v_mfma_f32_16x16x32_bf16 v[8:11], v[24:27], v[60:63], 0
	v_mfma_f32_16x16x32_bf16 v[168:171], v[28:31], v[88:91], v[8:11]
	v_mfma_f32_16x16x32_bf16 v[8:11], v[16:19], v[92:95], 0
	v_mfma_f32_16x16x32_bf16 v[188:191], v[20:23], v[104:107], v[8:11]
	v_mfma_f32_16x16x32_bf16 v[8:11], v[24:27], v[92:95], 0
	v_mfma_f32_16x16x32_bf16 v[192:195], v[28:31], v[104:107], v[8:11]
	v_mfma_f32_16x16x32_bf16 v[8:11], v[16:19], v[108:111], 0
	v_mfma_f32_16x16x32_bf16 v[196:199], v[20:23], v[116:119], v[8:11]
	v_mfma_f32_16x16x32_bf16 v[8:11], v[24:27], v[108:111], 0
	v_mfma_f32_16x16x32_bf16 v[116:119], v[28:31], v[116:119], v[8:11]
	v_mfma_f32_16x16x32_bf16 v[8:11], v[16:19], v[120:123], 0
	v_mfma_f32_16x16x32_bf16 v[200:203], v[20:23], v[124:127], v[8:11]
	v_mfma_f32_16x16x32_bf16 v[8:11], v[24:27], v[120:123], 0
	v_mfma_f32_16x16x32_bf16 v[204:207], v[28:31], v[124:127], v[8:11]
	s_barrier
	s_nop 4
	ds_read_b128 v[8:11], v184
	ds_read_b128 v[12:15], v184 offset:1024
	ds_read_b128 v[16:19], v184 offset:2048
	ds_read_b128 v[20:23], v184 offset:3072
	ds_read_b128 v[208:211], v185
	ds_read_b128 v[212:215], v185 offset:1024
	ds_read_b128 v[216:219], v185 offset:2048
	ds_read_b128 v[220:223], v185 offset:3072
	ds_read_b128 v[24:27], v183 offset:32768
	ds_read_b128 v[28:31], v183 offset:33792
	ds_read_b128 v[60:63], v183 offset:34816
	ds_read_b128 v[224:227], v183 offset:35840
	ds_read_b128 v[228:231], v183 offset:36864
	ds_read_b128 v[232:235], v183 offset:37888
	ds_read_b128 v[236:239], v183 offset:38912
	ds_read_b128 v[240:243], v183 offset:39936
	s_add_u32 s28, s22, 0x160100
	s_addc_u32 s29, s23, 0
	s_add_i32 m0, s36, 0x4000
	s_nop 0
	global_load_lds_dwordx4 v175, s[28:29]
	s_add_i32 m0, s36, 0x6000
	s_nop 0
	global_load_lds_dwordx4 v177, s[28:29]
	s_waitcnt vmcnt(8) lgkmcnt(0)
	s_barrier
	v_mfma_f32_16x16x32_bf16 v[64:67], v[8:11], v[24:27], v[64:67]
	v_mfma_f32_16x16x32_bf16 v[132:135], v[12:15], v[28:31], v[64:67]
	v_mfma_f32_16x16x32_bf16 v[64:67], v[16:19], v[24:27], v[68:71]
	v_mfma_f32_16x16x32_bf16 v[128:131], v[20:23], v[28:31], v[64:67]
	v_mfma_f32_16x16x32_bf16 v[64:67], v[8:11], v[60:63], v[72:75]
	v_mfma_f32_16x16x32_bf16 v[108:111], v[12:15], v[224:227], v[64:67]
	v_mfma_f32_16x16x32_bf16 v[64:67], v[16:19], v[60:63], v[76:79]
	v_mfma_f32_16x16x32_bf16 v[104:107], v[20:23], v[224:227], v[64:67]
	v_mfma_f32_16x16x32_bf16 v[64:67], v[8:11], v[228:231], v[80:83]
	v_mfma_f32_16x16x32_bf16 v[92:95], v[12:15], v[232:235], v[64:67]
	v_mfma_f32_16x16x32_bf16 v[64:67], v[16:19], v[228:231], v[84:87]
	v_mfma_f32_16x16x32_bf16 v[88:91], v[20:23], v[232:235], v[64:67]
	v_mfma_f32_16x16x32_bf16 v[64:67], v[8:11], v[236:239], v[96:99]
	v_mfma_f32_16x16x32_bf16 v[76:79], v[12:15], v[240:243], v[64:67]
	v_mfma_f32_16x16x32_bf16 v[64:67], v[16:19], v[236:239], v[100:103]
	v_mfma_f32_16x16x32_bf16 v[72:75], v[20:23], v[240:243], v[64:67]
	v_mfma_f32_16x16x32_bf16 v[64:67], v[208:211], v[24:27], v[112:115]
	v_mfma_f32_16x16x32_bf16 v[24:27], v[216:219], v[24:27], v[32:35]
	v_mfma_f32_16x16x32_bf16 v[120:123], v[220:223], v[28:31], v[24:27]
	v_mfma_f32_16x16x32_bf16 v[24:27], v[208:211], v[60:63], v[36:39]
	v_mfma_f32_16x16x32_bf16 v[100:103], v[212:215], v[224:227], v[24:27]
	v_mfma_f32_16x16x32_bf16 v[24:27], v[216:219], v[60:63], v[40:43]
	v_mfma_f32_16x16x32_bf16 v[96:99], v[220:223], v[224:227], v[24:27]
	v_mfma_f32_16x16x32_bf16 v[24:27], v[208:211], v[228:231], v[44:47]
	v_mfma_f32_16x16x32_bf16 v[84:87], v[212:215], v[232:235], v[24:27]
	v_mfma_f32_16x16x32_bf16 v[24:27], v[216:219], v[228:231], v[48:51]
	v_mfma_f32_16x16x32_bf16 v[80:83], v[220:223], v[232:235], v[24:27]
	v_mfma_f32_16x16x32_bf16 v[24:27], v[208:211], v[236:239], v[52:55]
	v_mfma_f32_16x16x32_bf16 v[68:71], v[212:215], v[240:243], v[24:27]
	v_mfma_f32_16x16x32_bf16 v[24:27], v[216:219], v[236:239], v[56:59]
	v_mfma_f32_16x16x32_bf16 v[124:127], v[212:215], v[28:31], v[64:67]
	v_mfma_f32_16x16x32_bf16 v[64:67], v[220:223], v[240:243], v[24:27]
	s_barrier
	ds_read_b128 v[32:35], v183 offset:49152
	ds_read_b128 v[36:39], v183 offset:50176
	ds_read_b128 v[112:115], v183 offset:51200
	ds_read_b128 v[224:227], v183 offset:52224
	ds_read_b128 v[228:231], v183 offset:53248
	ds_read_b128 v[232:235], v183 offset:54272
	ds_read_b128 v[236:239], v183 offset:55296
	ds_read_b128 v[240:243], v183 offset:56320
	s_add_i32 m0, s36, 0x18000
	s_nop 0
	global_load_lds_dwordx4 v176, s[26:27]
	s_add_i32 m0, s36, 0x1a000
	s_nop 0
	global_load_lds_dwordx4 v178, s[26:27]
	s_add_u32 s26, s24, 0x160180
	s_addc_u32 s27, s25, 0
	s_add_i32 m0, s36, 0x1c000
	s_nop 0
	global_load_lds_dwordx4 v176, s[26:27]
	s_add_i32 m0, s36, 0x1e000
	s_nop 0
	global_load_lds_dwordx4 v178, s[26:27]
	s_add_i32 m0, s36, 0x8000
	s_nop 0
	global_load_lds_dwordx4 v175, s[6:7]
	s_add_i32 m0, s36, 0xa000
	s_nop 0
	global_load_lds_dwordx4 v177, s[6:7]
	s_waitcnt vmcnt(8) lgkmcnt(0)
	s_barrier
	v_mfma_f32_16x16x32_bf16 v[24:27], v[8:11], v[32:35], v[136:139]
	v_mfma_f32_16x16x32_bf16 v[60:63], v[12:15], v[36:39], v[24:27]
	v_mfma_f32_16x16x32_bf16 v[24:27], v[16:19], v[32:35], v[140:143]
	v_mfma_f32_16x16x32_bf16 v[56:59], v[20:23], v[36:39], v[24:27]
	v_mfma_f32_16x16x32_bf16 v[24:27], v[8:11], v[112:115], v[144:147]
	v_mfma_f32_16x16x32_bf16 v[44:47], v[12:15], v[224:227], v[24:27]
	v_mfma_f32_16x16x32_bf16 v[24:27], v[16:19], v[112:115], v[148:151]
	v_mfma_f32_16x16x32_bf16 v[40:43], v[20:23], v[224:227], v[24:27]
	v_mfma_f32_16x16x32_bf16 v[24:27], v[8:11], v[228:231], v[156:159]
	v_mfma_f32_16x16x32_bf16 v[0:3], v[8:11], v[236:239], v[0:3]
	v_mfma_f32_16x16x32_bf16 v[28:31], v[12:15], v[232:235], v[24:27]
	v_mfma_f32_16x16x32_bf16 v[24:27], v[16:19], v[228:231], v[160:163]
	v_mfma_f32_16x16x32_bf16 v[12:15], v[12:15], v[240:243], v[0:3]
	v_mfma_f32_16x16x32_bf16 v[0:3], v[16:19], v[236:239], v[4:7]
	v_mfma_f32_16x16x32_bf16 v[24:27], v[20:23], v[232:235], v[24:27]
	v_mfma_f32_16x16x32_bf16 v[8:11], v[20:23], v[240:243], v[0:3]
	v_mfma_f32_16x16x32_bf16 v[0:3], v[208:211], v[32:35], v[164:167]
	v_mfma_f32_16x16x32_bf16 v[52:55], v[212:215], v[36:39], v[0:3]
	v_mfma_f32_16x16x32_bf16 v[0:3], v[216:219], v[32:35], v[168:171]
	v_mfma_f32_16x16x32_bf16 v[48:51], v[220:223], v[36:39], v[0:3]
	v_mfma_f32_16x16x32_bf16 v[0:3], v[208:211], v[112:115], v[188:191]
	v_mfma_f32_16x16x32_bf16 v[36:39], v[212:215], v[224:227], v[0:3]
	v_mfma_f32_16x16x32_bf16 v[0:3], v[216:219], v[112:115], v[192:195]
	v_mfma_f32_16x16x32_bf16 v[32:35], v[220:223], v[224:227], v[0:3]
	v_mfma_f32_16x16x32_bf16 v[0:3], v[208:211], v[228:231], v[196:199]
	v_mfma_f32_16x16x32_bf16 v[20:23], v[212:215], v[232:235], v[0:3]
	v_mfma_f32_16x16x32_bf16 v[0:3], v[216:219], v[228:231], v[116:119]
	v_mfma_f32_16x16x32_bf16 v[16:19], v[220:223], v[232:235], v[0:3]
	v_mfma_f32_16x16x32_bf16 v[0:3], v[208:211], v[236:239], v[200:203]
	v_mfma_f32_16x16x32_bf16 v[4:7], v[212:215], v[240:243], v[0:3]
	v_mfma_f32_16x16x32_bf16 v[0:3], v[216:219], v[236:239], v[204:207]
	v_mfma_f32_16x16x32_bf16 v[0:3], v[220:223], v[240:243], v[0:3]
	s_barrier
	s_add_u32 s51, s22, 0x200
	s_addc_u32 s52, s23, 0
	s_add_u32 s53, s24, 0x200
	s_addc_u32 s54, s25, 0
	s_add_u32 s6, s22, 0x160180
	s_addc_u32 s7, s23, 0
	s_mov_b32 s55, 0
.LBB0_838:
	ds_read_b128 v[112:115], v181
	ds_read_b128 v[116:119], v181 offset:1024
	ds_read_b128 v[136:139], v181 offset:2048
	ds_read_b128 v[140:143], v181 offset:3072
	ds_read_b128 v[144:147], v182
	ds_read_b128 v[148:151], v182 offset:1024
	ds_read_b128 v[156:159], v182 offset:2048
	ds_read_b128 v[160:163], v182 offset:3072
	ds_read_b128 v[164:167], v183
	ds_read_b128 v[168:171], v183 offset:1024
	ds_read_b128 v[188:191], v183 offset:2048
	ds_read_b128 v[192:195], v183 offset:3072
	ds_read_b128 v[196:199], v183 offset:4096
	ds_read_b128 v[200:203], v183 offset:5120
	ds_read_b128 v[204:207], v183 offset:6144
	ds_read_b128 v[208:211], v183 offset:7168
	s_cmpk_eq_i32 s55, 0x54
	s_cselect_b32 s28, s18, s51
	s_cselect_b32 s29, s19, s52
	s_cselect_b32 s24, s20, s53
	s_cselect_b32 s25, s21, s54
	s_add_u32 s22, s28, 0x80
	s_addc_u32 s23, s29, 0
	s_add_u32 s26, s24, 0x80
	s_addc_u32 s27, s25, 0
	s_add_i32 m0, s36, 0xc000
	s_nop 0
	global_load_lds_dwordx4 v175, s[6:7]
	s_add_i32 m0, s36, 0xe000
	s_nop 0
	global_load_lds_dwordx4 v177, s[6:7]
	s_waitcnt vmcnt(8) lgkmcnt(0)
	s_barrier
	v_mfma_f32_16x16x32_bf16 v[132:135], v[112:115], v[164:167], v[132:135]
	v_mfma_f32_16x16x32_bf16 v[128:131], v[136:139], v[164:167], v[128:131]
	v_mfma_f32_16x16x32_bf16 v[104:107], v[136:139], v[188:191], v[104:107]
	v_mfma_f32_16x16x32_bf16 v[108:111], v[112:115], v[188:191], v[108:111]
	v_mfma_f32_16x16x32_bf16 v[92:95], v[112:115], v[196:199], v[92:95]
	v_mfma_f32_16x16x32_bf16 v[88:91], v[136:139], v[196:199], v[88:91]
	v_mfma_f32_16x16x32_bf16 v[72:75], v[136:139], v[204:207], v[72:75]
	v_mfma_f32_16x16x32_bf16 v[76:79], v[112:115], v[204:207], v[76:79]
	v_mfma_f32_16x16x32_bf16 v[132:135], v[116:119], v[168:171], v[132:135]
	v_mfma_f32_16x16x32_bf16 v[128:131], v[140:143], v[168:171], v[128:131]
	v_mfma_f32_16x16x32_bf16 v[104:107], v[140:143], v[192:195], v[104:107]
	v_mfma_f32_16x16x32_bf16 v[108:111], v[116:119], v[192:195], v[108:111]
	v_mfma_f32_16x16x32_bf16 v[92:95], v[116:119], v[200:203], v[92:95]
	v_mfma_f32_16x16x32_bf16 v[88:91], v[140:143], v[200:203], v[88:91]
	v_mfma_f32_16x16x32_bf16 v[72:75], v[140:143], v[208:211], v[72:75]
	v_mfma_f32_16x16x32_bf16 v[76:79], v[116:119], v[208:211], v[76:79]
	v_mfma_f32_16x16x32_bf16 v[124:127], v[144:147], v[164:167], v[124:127]
	v_mfma_f32_16x16x32_bf16 v[120:123], v[156:159], v[164:167], v[120:123]
	v_mfma_f32_16x16x32_bf16 v[96:99], v[156:159], v[188:191], v[96:99]
	v_mfma_f32_16x16x32_bf16 v[100:103], v[144:147], v[188:191], v[100:103]
	v_mfma_f32_16x16x32_bf16 v[84:87], v[144:147], v[196:199], v[84:87]
	v_mfma_f32_16x16x32_bf16 v[80:83], v[156:159], v[196:199], v[80:83]
	v_mfma_f32_16x16x32_bf16 v[64:67], v[156:159], v[204:207], v[64:67]
	v_mfma_f32_16x16x32_bf16 v[68:71], v[144:147], v[204:207], v[68:71]
	v_mfma_f32_16x16x32_bf16 v[124:127], v[148:151], v[168:171], v[124:127]
	v_mfma_f32_16x16x32_bf16 v[120:123], v[160:163], v[168:171], v[120:123]
	v_mfma_f32_16x16x32_bf16 v[96:99], v[160:163], v[192:195], v[96:99]
	v_mfma_f32_16x16x32_bf16 v[100:103], v[148:151], v[192:195], v[100:103]
	v_mfma_f32_16x16x32_bf16 v[84:87], v[148:151], v[200:203], v[84:87]
	v_mfma_f32_16x16x32_bf16 v[80:83], v[160:163], v[200:203], v[80:83]
	v_mfma_f32_16x16x32_bf16 v[64:67], v[160:163], v[208:211], v[64:67]
	v_mfma_f32_16x16x32_bf16 v[68:71], v[148:151], v[208:211], v[68:71]
	s_barrier
	ds_read_b128 v[164:167], v183 offset:16384
	ds_read_b128 v[168:171], v183 offset:17408
	ds_read_b128 v[188:191], v183 offset:18432
	ds_read_b128 v[192:195], v183 offset:19456
	ds_read_b128 v[196:199], v183 offset:20480
	ds_read_b128 v[200:203], v183 offset:21504
	ds_read_b128 v[204:207], v183 offset:22528
	ds_read_b128 v[208:211], v183 offset:23552
	s_add_i32 m0, s36, 0x10000
	s_nop 0
	global_load_lds_dwordx4 v176, s[24:25]
	s_add_i32 m0, s36, 0x12000
	s_nop 0
	global_load_lds_dwordx4 v178, s[24:25]
	s_add_u32 s56, s24, 0x160000
	s_addc_u32 s57, s25, 0
	s_add_i32 m0, s36, 0x14000
	s_nop 0
	global_load_lds_dwordx4 v176, s[56:57]
	s_add_i32 m0, s36, 0x16000
	s_nop 0
	global_load_lds_dwordx4 v178, s[56:57]
	s_add_i32 m0, s36, 0
	s_nop 0
	global_load_lds_dwordx4 v175, s[28:29]
	s_add_i32 m0, s36, 0x2000
	s_nop 0
	global_load_lds_dwordx4 v177, s[28:29]
	s_waitcnt vmcnt(8) lgkmcnt(0)
	s_barrier
	v_mfma_f32_16x16x32_bf16 v[60:63], v[112:115], v[164:167], v[60:63]
	v_mfma_f32_16x16x32_bf16 v[56:59], v[136:139], v[164:167], v[56:59]
	v_mfma_f32_16x16x32_bf16 v[40:43], v[136:139], v[188:191], v[40:43]
	v_mfma_f32_16x16x32_bf16 v[44:47], v[112:115], v[188:191], v[44:47]
	v_mfma_f32_16x16x32_bf16 v[28:31], v[112:115], v[196:199], v[28:31]
	v_mfma_f32_16x16x32_bf16 v[24:27], v[136:139], v[196:199], v[24:27]
	v_mfma_f32_16x16x32_bf16 v[8:11], v[136:139], v[204:207], v[8:11]
	v_mfma_f32_16x16x32_bf16 v[12:15], v[112:115], v[204:207], v[12:15]
	v_mfma_f32_16x16x32_bf16 v[60:63], v[116:119], v[168:171], v[60:63]
	v_mfma_f32_16x16x32_bf16 v[56:59], v[140:143], v[168:171], v[56:59]
	v_mfma_f32_16x16x32_bf16 v[40:43], v[140:143], v[192:195], v[40:43]
	v_mfma_f32_16x16x32_bf16 v[44:47], v[116:119], v[192:195], v[44:47]
	v_mfma_f32_16x16x32_bf16 v[28:31], v[116:119], v[200:203], v[28:31]
	v_mfma_f32_16x16x32_bf16 v[24:27], v[140:143], v[200:203], v[24:27]
	v_mfma_f32_16x16x32_bf16 v[8:11], v[140:143], v[208:211], v[8:11]
	v_mfma_f32_16x16x32_bf16 v[12:15], v[116:119], v[208:211], v[12:15]
	v_mfma_f32_16x16x32_bf16 v[52:55], v[144:147], v[164:167], v[52:55]
	v_mfma_f32_16x16x32_bf16 v[48:51], v[156:159], v[164:167], v[48:51]
	v_mfma_f32_16x16x32_bf16 v[32:35], v[156:159], v[188:191], v[32:35]
	v_mfma_f32_16x16x32_bf16 v[36:39], v[144:147], v[188:191], v[36:39]
	v_mfma_f32_16x16x32_bf16 v[20:23], v[144:147], v[196:199], v[20:23]
	v_mfma_f32_16x16x32_bf16 v[16:19], v[156:159], v[196:199], v[16:19]
	v_mfma_f32_16x16x32_bf16 v[0:3], v[156:159], v[204:207], v[0:3]
	v_mfma_f32_16x16x32_bf16 v[4:7], v[144:147], v[204:207], v[4:7]
	v_mfma_f32_16x16x32_bf16 v[52:55], v[148:151], v[168:171], v[52:55]
	v_mfma_f32_16x16x32_bf16 v[48:51], v[160:163], v[168:171], v[48:51]
	v_mfma_f32_16x16x32_bf16 v[32:35], v[160:163], v[192:195], v[32:35]
	v_mfma_f32_16x16x32_bf16 v[36:39], v[148:151], v[192:195], v[36:39]
	v_mfma_f32_16x16x32_bf16 v[20:23], v[148:151], v[200:203], v[20:23]
	v_mfma_f32_16x16x32_bf16 v[16:19], v[160:163], v[200:203], v[16:19]
	v_mfma_f32_16x16x32_bf16 v[0:3], v[160:163], v[208:211], v[0:3]
	v_mfma_f32_16x16x32_bf16 v[4:7], v[148:151], v[208:211], v[4:7]
	s_barrier
	ds_read_b128 v[112:115], v184
	ds_read_b128 v[116:119], v184 offset:1024
	ds_read_b128 v[136:139], v184 offset:2048
	ds_read_b128 v[140:143], v184 offset:3072
	ds_read_b128 v[144:147], v185
	ds_read_b128 v[148:151], v185 offset:1024
	ds_read_b128 v[156:159], v185 offset:2048
	ds_read_b128 v[160:163], v185 offset:3072
	ds_read_b128 v[164:167], v183 offset:32768
	ds_read_b128 v[168:171], v183 offset:33792
	ds_read_b128 v[188:191], v183 offset:34816
	ds_read_b128 v[192:195], v183 offset:35840
	ds_read_b128 v[196:199], v183 offset:36864
	ds_read_b128 v[200:203], v183 offset:37888
	ds_read_b128 v[204:207], v183 offset:38912
	ds_read_b128 v[208:211], v183 offset:39936
	s_add_u32 s28, s28, 0x160000
	s_addc_u32 s29, s29, 0
	s_add_i32 m0, s36, 0x4000
	s_nop 0
	global_load_lds_dwordx4 v175, s[28:29]
	s_add_i32 m0, s36, 0x6000
	s_nop 0
	global_load_lds_dwordx4 v177, s[28:29]
	s_waitcnt vmcnt(8) lgkmcnt(0)
	s_barrier
	v_mfma_f32_16x16x32_bf16 v[132:135], v[112:115], v[164:167], v[132:135]
	v_mfma_f32_16x16x32_bf16 v[128:131], v[136:139], v[164:167], v[128:131]
	v_mfma_f32_16x16x32_bf16 v[104:107], v[136:139], v[188:191], v[104:107]
	v_mfma_f32_16x16x32_bf16 v[108:111], v[112:115], v[188:191], v[108:111]
	v_mfma_f32_16x16x32_bf16 v[92:95], v[112:115], v[196:199], v[92:95]
	v_mfma_f32_16x16x32_bf16 v[88:91], v[136:139], v[196:199], v[88:91]
	v_mfma_f32_16x16x32_bf16 v[72:75], v[136:139], v[204:207], v[72:75]
	v_mfma_f32_16x16x32_bf16 v[76:79], v[112:115], v[204:207], v[76:79]
	v_mfma_f32_16x16x32_bf16 v[132:135], v[116:119], v[168:171], v[132:135]
	v_mfma_f32_16x16x32_bf16 v[128:131], v[140:143], v[168:171], v[128:131]
	v_mfma_f32_16x16x32_bf16 v[104:107], v[140:143], v[192:195], v[104:107]
	v_mfma_f32_16x16x32_bf16 v[108:111], v[116:119], v[192:195], v[108:111]
	v_mfma_f32_16x16x32_bf16 v[92:95], v[116:119], v[200:203], v[92:95]
	v_mfma_f32_16x16x32_bf16 v[88:91], v[140:143], v[200:203], v[88:91]
	v_mfma_f32_16x16x32_bf16 v[72:75], v[140:143], v[208:211], v[72:75]
	v_mfma_f32_16x16x32_bf16 v[76:79], v[116:119], v[208:211], v[76:79]
	v_mfma_f32_16x16x32_bf16 v[124:127], v[144:147], v[164:167], v[124:127]
	v_mfma_f32_16x16x32_bf16 v[120:123], v[156:159], v[164:167], v[120:123]
	v_mfma_f32_16x16x32_bf16 v[96:99], v[156:159], v[188:191], v[96:99]
	v_mfma_f32_16x16x32_bf16 v[100:103], v[144:147], v[188:191], v[100:103]
	v_mfma_f32_16x16x32_bf16 v[84:87], v[144:147], v[196:199], v[84:87]
	v_mfma_f32_16x16x32_bf16 v[80:83], v[156:159], v[196:199], v[80:83]
	v_mfma_f32_16x16x32_bf16 v[64:67], v[156:159], v[204:207], v[64:67]
	v_mfma_f32_16x16x32_bf16 v[68:71], v[144:147], v[204:207], v[68:71]
	v_mfma_f32_16x16x32_bf16 v[124:127], v[148:151], v[168:171], v[124:127]
	v_mfma_f32_16x16x32_bf16 v[120:123], v[160:163], v[168:171], v[120:123]
	v_mfma_f32_16x16x32_bf16 v[96:99], v[160:163], v[192:195], v[96:99]
	v_mfma_f32_16x16x32_bf16 v[100:103], v[148:151], v[192:195], v[100:103]
	v_mfma_f32_16x16x32_bf16 v[84:87], v[148:151], v[200:203], v[84:87]
	v_mfma_f32_16x16x32_bf16 v[80:83], v[160:163], v[200:203], v[80:83]
	v_mfma_f32_16x16x32_bf16 v[64:67], v[160:163], v[208:211], v[64:67]
	v_mfma_f32_16x16x32_bf16 v[68:71], v[148:151], v[208:211], v[68:71]
	s_barrier
	ds_read_b128 v[164:167], v183 offset:49152
	ds_read_b128 v[168:171], v183 offset:50176
	ds_read_b128 v[188:191], v183 offset:51200
	ds_read_b128 v[192:195], v183 offset:52224
	ds_read_b128 v[196:199], v183 offset:53248
	ds_read_b128 v[200:203], v183 offset:54272
	ds_read_b128 v[204:207], v183 offset:55296
	ds_read_b128 v[208:211], v183 offset:56320
	s_add_i32 m0, s36, 0x18000
	s_nop 0
	global_load_lds_dwordx4 v176, s[26:27]
	s_add_i32 m0, s36, 0x1a000
	s_nop 0
	global_load_lds_dwordx4 v178, s[26:27]
	s_add_u32 s24, s24, 0x160080
	s_addc_u32 s25, s25, 0
	s_add_i32 m0, s36, 0x1c000
	s_nop 0
	global_load_lds_dwordx4 v176, s[24:25]
	s_add_i32 m0, s36, 0x1e000
	s_nop 0
	global_load_lds_dwordx4 v178, s[24:25]
	s_add_i32 m0, s36, 0x8000
	s_nop 0
	global_load_lds_dwordx4 v175, s[22:23]
	s_add_i32 m0, s36, 0xa000
	s_nop 0
	global_load_lds_dwordx4 v177, s[22:23]
	s_waitcnt vmcnt(8) lgkmcnt(0)
	s_barrier
	v_mfma_f32_16x16x32_bf16 v[60:63], v[112:115], v[164:167], v[60:63]
	v_mfma_f32_16x16x32_bf16 v[56:59], v[136:139], v[164:167], v[56:59]
	v_mfma_f32_16x16x32_bf16 v[40:43], v[136:139], v[188:191], v[40:43]
	v_mfma_f32_16x16x32_bf16 v[44:47], v[112:115], v[188:191], v[44:47]
	v_mfma_f32_16x16x32_bf16 v[28:31], v[112:115], v[196:199], v[28:31]
	v_mfma_f32_16x16x32_bf16 v[24:27], v[136:139], v[196:199], v[24:27]
	v_mfma_f32_16x16x32_bf16 v[8:11], v[136:139], v[204:207], v[8:11]
	v_mfma_f32_16x16x32_bf16 v[12:15], v[112:115], v[204:207], v[12:15]
	v_mfma_f32_16x16x32_bf16 v[60:63], v[116:119], v[168:171], v[60:63]
	v_mfma_f32_16x16x32_bf16 v[56:59], v[140:143], v[168:171], v[56:59]
	v_mfma_f32_16x16x32_bf16 v[40:43], v[140:143], v[192:195], v[40:43]
	v_mfma_f32_16x16x32_bf16 v[44:47], v[116:119], v[192:195], v[44:47]
	v_mfma_f32_16x16x32_bf16 v[28:31], v[116:119], v[200:203], v[28:31]
	v_mfma_f32_16x16x32_bf16 v[24:27], v[140:143], v[200:203], v[24:27]
	v_mfma_f32_16x16x32_bf16 v[8:11], v[140:143], v[208:211], v[8:11]
	v_mfma_f32_16x16x32_bf16 v[12:15], v[116:119], v[208:211], v[12:15]
	v_mfma_f32_16x16x32_bf16 v[52:55], v[144:147], v[164:167], v[52:55]
	v_mfma_f32_16x16x32_bf16 v[48:51], v[156:159], v[164:167], v[48:51]
	v_mfma_f32_16x16x32_bf16 v[32:35], v[156:159], v[188:191], v[32:35]
	v_mfma_f32_16x16x32_bf16 v[36:39], v[144:147], v[188:191], v[36:39]
	v_mfma_f32_16x16x32_bf16 v[20:23], v[144:147], v[196:199], v[20:23]
	v_mfma_f32_16x16x32_bf16 v[16:19], v[156:159], v[196:199], v[16:19]
	v_mfma_f32_16x16x32_bf16 v[0:3], v[156:159], v[204:207], v[0:3]
	v_mfma_f32_16x16x32_bf16 v[4:7], v[144:147], v[204:207], v[4:7]
	v_mfma_f32_16x16x32_bf16 v[52:55], v[148:151], v[168:171], v[52:55]
	v_mfma_f32_16x16x32_bf16 v[48:51], v[160:163], v[168:171], v[48:51]
	v_mfma_f32_16x16x32_bf16 v[32:35], v[160:163], v[192:195], v[32:35]
	v_mfma_f32_16x16x32_bf16 v[36:39], v[148:151], v[192:195], v[36:39]
	v_mfma_f32_16x16x32_bf16 v[20:23], v[148:151], v[200:203], v[20:23]
	v_mfma_f32_16x16x32_bf16 v[16:19], v[160:163], v[200:203], v[16:19]
	v_mfma_f32_16x16x32_bf16 v[0:3], v[160:163], v[208:211], v[0:3]
	v_mfma_f32_16x16x32_bf16 v[4:7], v[148:151], v[208:211], v[4:7]
	s_barrier
	s_add_i32 s55, s55, 2
	s_add_u32 s51, s51, 0x100
	s_addc_u32 s52, s52, 0
	s_add_u32 s53, s53, 0x100
	s_addc_u32 s54, s54, 0
	s_add_u32 s6, s6, 0x100
	s_addc_u32 s7, s7, 0
	s_cmpk_gt_u32 s55, 0x55
	s_cbranch_scc0 .LBB0_838
	s_and_b64 vcc, exec, s[16:17]
	s_cbranch_vccz .LBB0_841
	s_barrier

.LBB0_919:
	v_bfe_i32 v3, v0, 27, 1
	s_waitcnt lgkmcnt(0)
	v_lshlrev_b32_e32 v1, 4, v0
	v_lshrrev_b32_e32 v3, 22, v3
	v_add_u32_e32 v3, v1, v3
	v_and_b32_e32 v3, 0xfffffc00, v3
	v_sub_u32_e32 v3, v1, v3
	v_ashrrev_i32_e32 v2, 31, v0
	v_lshrrev_b32_e32 v4, 4, v3
	v_lshrrev_b32_e32 v2, 26, v2
	v_bitop3_b32 v3, v4, v3, 32 bitop3:0x6c
	v_add_u32_e32 v2, v0, v2
	v_ashrrev_i32_e32 v5, 31, v3
	v_ashrrev_i32_e32 v2, 6, v2
	v_lshrrev_b32_e32 v5, 26, v5
	v_lshlrev_b32_e32 v4, 3, v2
	v_add_u32_e32 v5, v3, v5
	v_and_b32_e32 v4, -16, v4
	v_ashrrev_i32_e32 v6, 6, v5
	v_and_b32_e32 v5, 0xc0, v5
	v_add_u32_e32 v4, v6, v4
	v_sub_u32_e32 v3, v3, v5
	v_mov_b32_e32 v5, 1
	v_lshlrev_b32_e32 v2, 5, v2
	v_ashrrev_i16_sdwa v3, v5, sext(v3) dst_sel:DWORD dst_unused:UNUSED_PAD src0_sel:DWORD src1_sel:BYTE_0
	v_lshlrev_b32_e32 v7, 1, v4
	s_waitcnt vmcnt(3)
	v_lshrrev_b32_e32 v8, 2, v4
	v_and_b32_e32 v6, 3, v6
	s_mov_b32 s5, 0x1fffe0
	v_and_b32_e32 v2, 32, v2
	v_bfe_i32 v3, v3, 0, 16
	v_and_b32_e32 v7, 24, v7
	v_and_b32_e32 v8, 4, v8
	v_and_or_b32 v6, v4, s5, v6
	v_or3_b32 v6, v6, v8, v7
	v_add_lshl_u32 v2, v2, v3, 1
	v_add_u32_e32 v1, 0x2000, v1
	v_lshl_add_u32 v219, v4, 11, v2
	v_lshl_add_u32 v220, v6, 11, v2
	v_ashrrev_i32_e32 v2, 31, v1
	v_lshrrev_b32_e32 v2, 22, v2
	v_add_u32_e32 v2, v1, v2
	v_ashrrev_i32_e32 v2, 10, v2
	v_mul_i32_i24_e32 v3, 0x400, v2
	v_sub_u32_e32 v1, v1, v3
	v_lshrrev_b32_e32 v3, 4, v1
	v_bitop3_b32 v1, v3, v1, 32 bitop3:0x6c
	s_add_u32 s19, s70, 0x62800000
	v_ashrrev_i32_e32 v4, 31, v1
	s_addc_u32 s21, s71, 0
	v_lshrrev_b32_e32 v4, 26, v4
	s_add_u32 s23, s70, 0x7000000
	v_lshlrev_b32_e32 v3, 3, v2
	v_add_u32_e32 v4, v1, v4
	s_addc_u32 s25, s71, 0
	v_and_b32_e32 v3, -16, v3
	v_ashrrev_i32_e32 v6, 6, v4
	s_add_u32 s27, s70, 0x140000
	v_add_u32_e32 v3, v6, v3
	v_and_b32_e32 v6, 3, v6
	s_addc_u32 s29, s71, 0
	v_and_or_b32 v6, v3, s5, v6
	s_lshl_b32 s5, s17, 10
	s_ashr_i32 s9, s8, 31
	s_ashr_i32 s4, s16, 8
	s_add_i32 s31, s5, 0
	s_lshl_b64 s[10:11], s[8:9], 19
	s_add_u32 s44, s19, s10
	s_addc_u32 s45, s21, s11
	s_ashr_i32 s7, s6, 31
	s_lshl_b64 s[10:11], s[6:7], 19
	s_add_u32 s42, s23, s10
	s_addc_u32 s43, s25, s11
	s_and_b32 s56, s5, 0x400
	v_and_b32_e32 v4, 0xc0, v4
	s_add_i32 s5, s56, 0
	v_sub_u32_e32 v1, v1, v4
	s_add_i32 s5, s5, 0x20000
	s_lshl_b64 s[10:11], s[8:9], 11
	v_lshlrev_b32_e32 v2, 5, v2
	v_ashrrev_i16_sdwa v1, v5, sext(v1) dst_sel:DWORD dst_unused:UNUSED_PAD src0_sel:DWORD src1_sel:BYTE_0
	v_lshlrev_b32_e32 v4, 1, v3
	v_lshrrev_b32_e32 v5, 2, v3
	s_add_u32 s10, s27, s10
	v_and_b32_e32 v2, 32, v2
	v_bfe_i32 v1, v1, 0, 16
	v_and_b32_e32 v4, 24, v4
	v_and_b32_e32 v5, 4, v5
	s_addc_u32 s11, s29, s11
	v_lshl_add_u32 v223, v218, 4, s56
	s_add_i32 m0, s5, 0
	s_nop 0
	global_load_lds_dwordx4 v223, s[10:11]
	v_or3_b32 v4, v6, v5, v4
	v_add_lshl_u32 v1, v2, v1, 1
	s_add_i32 m0, s31, 0x10000
	s_nop 0
	global_load_lds_dwordx4 v220, s[42:43]
	v_lshl_add_u32 v222, v4, 11, v1
	s_add_i32 m0, s31, 0x12000
	s_nop 0
	global_load_lds_dwordx4 v222, s[42:43]
	s_add_u32 s10, s42, 0x40000
	s_addc_u32 s11, s43, 0
	s_add_i32 m0, s31, 0x14000
	s_nop 0
	global_load_lds_dwordx4 v220, s[10:11]
	v_lshl_add_u32 v221, v3, 11, v1
	s_add_i32 m0, s31, 0x16000
	s_nop 0
	global_load_lds_dwordx4 v222, s[10:11]
	s_mov_b32 s7, 0
	s_add_i32 m0, s31, 0
	s_nop 0
	global_load_lds_dwordx4 v219, s[44:45]
	s_add_i32 m0, s31, 0x2000
	s_nop 0
	global_load_lds_dwordx4 v221, s[44:45]
	s_add_u32 s10, s44, 0x40000
	s_addc_u32 s11, s45, 0
	s_add_i32 m0, s31, 0x4000
	s_nop 0
	global_load_lds_dwordx4 v219, s[10:11]
	s_add_i32 m0, s31, 0x6000
	s_nop 0
	global_load_lds_dwordx4 v221, s[10:11]
	s_cmp_eq_u32 s4, 1
	s_cselect_b64 s[10:11], -1, 0
	s_cmp_lg_u32 s4, 1
	s_cbranch_scc1 .LBB0_921
	s_barrier

.LBB0_930:
	s_ashr_i32 s37, s36, 31
	s_lshl_b64 s[38:39], s[36:37], 19
	s_add_u32 s38, s19, s38
	s_addc_u32 s39, s21, s39
	s_and_b64 s[40:41], s[4:5], exec
	s_cselect_b32 s9, s39, s45
	s_cselect_b32 s76, s38, s44
	s_ashr_i32 s35, s34, 31
	s_lshl_b64 s[40:41], s[34:35], 19
	s_add_u32 s40, s23, s40
	s_addc_u32 s41, s25, s41
	s_and_b64 s[46:47], s[4:5], exec
	ds_read_b128 v[0:3], v226 offset:3072
	ds_read_b128 v[4:7], v226 offset:2048
	ds_read_b128 v[8:11], v226 offset:1024
	ds_read_b128 v[12:15], v226
	ds_read_b128 v[16:19], v227 offset:3072
	ds_read_b128 v[20:23], v227 offset:2048
	ds_read_b128 v[24:27], v227 offset:1024
	ds_read_b128 v[28:31], v227
	ds_read_b128 v[32:35], v228
	ds_read_b128 v[36:39], v228 offset:1024
	ds_read_b128 v[40:43], v228 offset:2048
	ds_read_b128 v[44:47], v228 offset:3072
	ds_read_b128 v[48:51], v228 offset:4096
	ds_read_b128 v[52:55], v228 offset:5120
	ds_read_b128 v[56:59], v228 offset:6144
	ds_read_b128 v[60:63], v228 offset:7168
	s_cselect_b32 s35, s41, s43
	s_cselect_b32 s77, s40, s42
	s_lshl_b32 s46, s78, 11
	s_and_b32 s46, s46, 0x800
	s_or_b32 s54, s46, s56
	s_lshl_b64 s[48:49], s[36:37], 11
	s_add_u32 s46, s44, 0x100
	s_addc_u32 s47, s45, 0
	s_add_u32 s80, s42, 0x100
	s_addc_u32 s81, s43, 0
	s_add_u32 s50, s44, 0x180
	s_addc_u32 s51, s45, 0
	s_add_u32 s52, s42, 0x180
	s_addc_u32 s53, s43, 0
	s_add_u32 s82, s44, 0x40080
	s_addc_u32 s83, s45, 0
	s_add_i32 m0, s31, 0xc000
	s_nop 0
	global_load_lds_dwordx4 v219, s[82:83]
	s_add_i32 m0, s31, 0xe000
	s_nop 0
	global_load_lds_dwordx4 v221, s[82:83]
	s_waitcnt vmcnt(8) lgkmcnt(0)
	s_barrier
	s_waitcnt lgkmcnt(7)
	v_mfma_i32_16x16x64_i8 v[64:67], v[28:31], v[32:35], 0
	s_mov_b32 s37, 0
	v_mfma_i32_16x16x64_i8 v[68:71], v[20:23], v[32:35], 0
	s_waitcnt lgkmcnt(5)
	v_mfma_i32_16x16x64_i8 v[72:75], v[28:31], v[40:43], 0
	v_mfma_i32_16x16x64_i8 v[76:79], v[20:23], v[40:43], 0
	s_waitcnt lgkmcnt(3)
	v_mfma_i32_16x16x64_i8 v[80:83], v[28:31], v[48:51], 0
	v_mfma_i32_16x16x64_i8 v[84:87], v[20:23], v[48:51], 0
	s_waitcnt lgkmcnt(1)
	v_mfma_i32_16x16x64_i8 v[92:95], v[20:23], v[56:59], 0
	v_mfma_i32_16x16x64_i8 v[136:139], v[24:27], v[36:39], v[64:67]
	v_mfma_i32_16x16x64_i8 v[148:151], v[24:27], v[44:47], v[72:75]
	v_mfma_i32_16x16x64_i8 v[144:147], v[16:19], v[36:39], v[68:71]
	v_mfma_i32_16x16x64_i8 v[76:79], v[16:19], v[44:47], v[76:79]
	v_mfma_i32_16x16x64_i8 v[80:83], v[24:27], v[52:55], v[80:83]
	v_mfma_i32_16x16x64_i8 v[88:91], v[28:31], v[56:59], 0
	v_mfma_i32_16x16x64_i8 v[84:87], v[16:19], v[52:55], v[84:87]
	s_waitcnt lgkmcnt(0)
	v_mfma_i32_16x16x64_i8 v[92:95], v[16:19], v[60:63], v[92:95]
	v_mfma_i32_16x16x64_i8 v[88:91], v[24:27], v[60:63], v[88:91]
	v_mfma_i32_16x16x64_i8 v[96:99], v[12:15], v[32:35], 0
	v_mfma_i32_16x16x64_i8 v[32:35], v[4:7], v[32:35], 0
	v_mfma_i32_16x16x64_i8 v[96:99], v[8:11], v[36:39], v[96:99]
	v_mfma_i32_16x16x64_i8 v[32:35], v[0:3], v[36:39], v[32:35]
	v_mfma_i32_16x16x64_i8 v[36:39], v[12:15], v[40:43], 0
	v_mfma_i32_16x16x64_i8 v[40:43], v[4:7], v[40:43], 0
	v_mfma_i32_16x16x64_i8 v[36:39], v[8:11], v[44:47], v[36:39]
	v_mfma_i32_16x16x64_i8 v[40:43], v[0:3], v[44:47], v[40:43]
	v_mfma_i32_16x16x64_i8 v[44:47], v[12:15], v[48:51], 0
	v_mfma_i32_16x16x64_i8 v[48:51], v[4:7], v[48:51], 0
	v_mfma_i32_16x16x64_i8 v[44:47], v[8:11], v[52:55], v[44:47]
	v_mfma_i32_16x16x64_i8 v[48:51], v[0:3], v[52:55], v[48:51]
	v_mfma_i32_16x16x64_i8 v[52:55], v[12:15], v[56:59], 0
	v_mfma_i32_16x16x64_i8 v[56:59], v[4:7], v[56:59], 0
	v_mfma_i32_16x16x64_i8 v[52:55], v[8:11], v[60:63], v[52:55]
	v_mfma_i32_16x16x64_i8 v[56:59], v[0:3], v[60:63], v[56:59]
	s_barrier
	ds_read_b128 v[60:63], v228 offset:16384
	ds_read_b128 v[100:103], v228 offset:17408
	ds_read_b128 v[104:107], v228 offset:18432
	ds_read_b128 v[108:111], v228 offset:19456
	ds_read_b128 v[112:115], v228 offset:20480
	ds_read_b128 v[116:119], v228 offset:21504
	ds_read_b128 v[120:123], v228 offset:22528
	ds_read_b128 v[124:127], v228 offset:23552
	s_add_i32 m0, s31, 0x10000
	s_nop 0
	global_load_lds_dwordx4 v220, s[80:81]
	s_add_i32 m0, s31, 0x12000
	s_nop 0
	global_load_lds_dwordx4 v222, s[80:81]
	s_add_u32 s80, s42, 0x40100
	s_addc_u32 s81, s43, 0
	s_add_i32 m0, s31, 0x14000
	s_nop 0
	global_load_lds_dwordx4 v220, s[80:81]
	s_add_i32 m0, s31, 0x16000
	s_nop 0
	global_load_lds_dwordx4 v222, s[80:81]
	s_add_i32 m0, s31, 0
	s_nop 0
	global_load_lds_dwordx4 v219, s[46:47]
	s_add_i32 m0, s31, 0x2000
	s_nop 0
	global_load_lds_dwordx4 v221, s[46:47]
	s_waitcnt vmcnt(8) lgkmcnt(0)
	s_barrier
	v_mfma_i32_16x16x64_i8 v[132:135], v[20:23], v[60:63], 0
	v_mfma_i32_16x16x64_i8 v[168:171], v[16:19], v[100:103], v[132:135]
	v_mfma_i32_16x16x64_i8 v[132:135], v[28:31], v[104:107], 0
	v_mfma_i32_16x16x64_i8 v[204:207], v[24:27], v[108:111], v[132:135]
	v_mfma_i32_16x16x64_i8 v[132:135], v[20:23], v[104:107], 0
	v_mfma_i32_16x16x64_i8 v[128:131], v[28:31], v[60:63], 0
	v_mfma_i32_16x16x64_i8 v[214:217], v[16:19], v[108:111], v[132:135]
	v_mfma_i32_16x16x64_i8 v[132:135], v[28:31], v[112:115], 0
	v_mfma_i32_16x16x64_i8 v[128:131], v[24:27], v[100:103], v[128:131]
	v_mfma_i32_16x16x64_i8 v[232:235], v[24:27], v[116:119], v[132:135]
	v_mfma_i32_16x16x64_i8 v[132:135], v[20:23], v[112:115], 0
	v_mfma_i32_16x16x64_i8 v[28:31], v[28:31], v[120:123], 0
	v_mfma_i32_16x16x64_i8 v[20:23], v[20:23], v[120:123], 0
	v_mfma_i32_16x16x64_i8 v[236:239], v[16:19], v[116:119], v[132:135]
	v_mfma_i32_16x16x64_i8 v[24:27], v[24:27], v[124:127], v[28:31]
	v_mfma_i32_16x16x64_i8 v[16:19], v[16:19], v[124:127], v[20:23]
	v_mfma_i32_16x16x64_i8 v[20:23], v[12:15], v[60:63], 0
	v_mfma_i32_16x16x64_i8 v[28:31], v[4:7], v[60:63], 0
	v_mfma_i32_16x16x64_i8 v[20:23], v[8:11], v[100:103], v[20:23]
	v_mfma_i32_16x16x64_i8 v[28:31], v[0:3], v[100:103], v[28:31]
	v_mfma_i32_16x16x64_i8 v[60:63], v[12:15], v[104:107], 0
	v_mfma_i32_16x16x64_i8 v[100:103], v[4:7], v[104:107], 0
	v_mfma_i32_16x16x64_i8 v[104:107], v[12:15], v[112:115], 0
	v_mfma_i32_16x16x64_i8 v[100:103], v[0:3], v[108:111], v[100:103]
	v_mfma_i32_16x16x64_i8 v[240:243], v[8:11], v[116:119], v[104:107]
	v_mfma_i32_16x16x64_i8 v[104:107], v[4:7], v[112:115], 0
	v_mfma_i32_16x16x64_i8 v[12:15], v[12:15], v[120:123], 0
	v_mfma_i32_16x16x64_i8 v[4:7], v[4:7], v[120:123], 0
	v_mfma_i32_16x16x64_i8 v[60:63], v[8:11], v[108:111], v[60:63]
	v_mfma_i32_16x16x64_i8 v[244:247], v[0:3], v[116:119], v[104:107]
	v_mfma_i32_16x16x64_i8 v[8:11], v[8:11], v[124:127], v[12:15]
	v_mfma_i32_16x16x64_i8 v[0:3], v[0:3], v[124:127], v[4:7]
	s_barrier
	s_nop 1
	ds_read_b128 v[4:7], v229
	ds_read_b128 v[12:15], v229 offset:1024
	ds_read_b128 v[104:107], v229 offset:2048
	ds_read_b128 v[116:119], v229 offset:3072
	ds_read_b128 v[124:127], v230
	ds_read_b128 v[248:251], v230 offset:1024
	ds_read_b128 v[208:211], v230 offset:2048
	ds_read_b128 v[64:67], v230 offset:3072
	ds_read_b128 v[108:111], v228 offset:32768
	ds_read_b128 v[112:115], v228 offset:33792
	ds_read_b128 v[120:123], v228 offset:34816
	ds_read_b128 v[132:135], v228 offset:35840
	ds_read_b128 v[140:143], v228 offset:36864
	ds_read_b128 v[152:155], v228 offset:37888
	ds_read_b128 v[68:71], v228 offset:38912
	ds_read_b128 v[72:75], v228 offset:39936
	s_add_u32 s44, s44, 0x40100
	s_addc_u32 s45, s45, 0
	s_add_i32 m0, s31, 0x4000
	s_nop 0
	global_load_lds_dwordx4 v219, s[44:45]
	s_add_i32 m0, s31, 0x6000
	s_nop 0
	global_load_lds_dwordx4 v221, s[44:45]
	s_waitcnt vmcnt(8) lgkmcnt(0)
	s_barrier
	v_mfma_i32_16x16x64_i8 v[76:79], v[104:107], v[120:123], v[76:79]
	v_mfma_i32_16x16x64_i8 v[180:183], v[116:119], v[132:135], v[76:79]
	v_mfma_i32_16x16x64_i8 v[76:79], v[4:7], v[140:143], v[80:83]
	v_mfma_i32_16x16x64_i8 v[136:139], v[4:7], v[108:111], v[136:139]
	v_mfma_i32_16x16x64_i8 v[164:167], v[12:15], v[152:155], v[76:79]
	v_mfma_i32_16x16x64_i8 v[76:79], v[104:107], v[140:143], v[84:87]
	v_mfma_i32_16x16x64_i8 v[200:203], v[12:15], v[112:115], v[136:139]
	v_mfma_i32_16x16x64_i8 v[136:139], v[104:107], v[108:111], v[144:147]
	v_mfma_i32_16x16x64_i8 v[160:163], v[116:119], v[152:155], v[76:79]
	v_mfma_i32_16x16x64_i8 v[76:79], v[4:7], v[68:71], v[88:91]
	v_mfma_i32_16x16x64_i8 v[196:199], v[116:119], v[112:115], v[136:139]
	v_mfma_i32_16x16x64_i8 v[136:139], v[4:7], v[120:123], v[148:151]
	v_mfma_i32_16x16x64_i8 v[148:151], v[12:15], v[72:75], v[76:79]
	v_mfma_i32_16x16x64_i8 v[76:79], v[104:107], v[68:71], v[92:95]
	v_mfma_i32_16x16x64_i8 v[184:187], v[12:15], v[132:135], v[136:139]
	v_mfma_i32_16x16x64_i8 v[144:147], v[116:119], v[72:75], v[76:79]
	v_mfma_i32_16x16x64_i8 v[32:35], v[208:211], v[108:111], v[32:35]
	v_mfma_i32_16x16x64_i8 v[188:191], v[64:67], v[112:115], v[32:35]
	v_mfma_i32_16x16x64_i8 v[32:35], v[124:127], v[120:123], v[36:39]
	v_mfma_i32_16x16x64_i8 v[176:179], v[248:251], v[132:135], v[32:35]
	v_mfma_i32_16x16x64_i8 v[32:35], v[208:211], v[120:123], v[40:43]
	v_mfma_i32_16x16x64_i8 v[172:175], v[64:67], v[132:135], v[32:35]
	v_mfma_i32_16x16x64_i8 v[32:35], v[124:127], v[140:143], v[44:47]
	v_mfma_i32_16x16x64_i8 v[156:159], v[248:251], v[152:155], v[32:35]
	v_mfma_i32_16x16x64_i8 v[32:35], v[208:211], v[140:143], v[48:51]
	v_mfma_i32_16x16x64_i8 v[152:155], v[64:67], v[152:155], v[32:35]
	v_mfma_i32_16x16x64_i8 v[32:35], v[124:127], v[68:71], v[52:55]
	v_mfma_i32_16x16x64_i8 v[76:79], v[124:127], v[108:111], v[96:99]
	v_mfma_i32_16x16x64_i8 v[140:143], v[248:251], v[72:75], v[32:35]
	v_mfma_i32_16x16x64_i8 v[32:35], v[208:211], v[68:71], v[56:59]
	v_mfma_i32_16x16x64_i8 v[192:195], v[248:251], v[112:115], v[76:79]
	v_mfma_i32_16x16x64_i8 v[136:139], v[64:67], v[72:75], v[32:35]
	s_barrier
	s_nop 3
	ds_read_b128 v[32:35], v228 offset:49152
	ds_read_b128 v[36:39], v228 offset:50176
	ds_read_b128 v[40:43], v228 offset:51200
	ds_read_b128 v[44:47], v228 offset:52224
	ds_read_b128 v[48:51], v228 offset:53248
	ds_read_b128 v[52:55], v228 offset:54272
	ds_read_b128 v[56:59], v228 offset:55296
	ds_read_b128 v[88:91], v228 offset:56320
	s_add_i32 m0, s31, 0x18000
	s_nop 0
	global_load_lds_dwordx4 v220, s[52:53]
	s_add_i32 m0, s31, 0x1a000
	s_nop 0
	global_load_lds_dwordx4 v222, s[52:53]
	s_add_u32 s44, s42, 0x40180
	s_addc_u32 s45, s43, 0
	s_add_i32 m0, s31, 0x1c000
	s_nop 0
	global_load_lds_dwordx4 v220, s[44:45]
	s_add_i32 m0, s31, 0x1e000
	s_nop 0
	global_load_lds_dwordx4 v222, s[44:45]
	s_add_i32 m0, s31, 0x8000
	s_nop 0
	global_load_lds_dwordx4 v219, s[50:51]
	s_add_i32 m0, s31, 0xa000
	s_nop 0
	global_load_lds_dwordx4 v221, s[50:51]
	s_waitcnt vmcnt(8) lgkmcnt(0)
	s_barrier
	v_mfma_i32_16x16x64_i8 v[68:71], v[4:7], v[32:35], v[128:131]
	v_mfma_i32_16x16x64_i8 v[132:135], v[12:15], v[36:39], v[68:71]
	v_mfma_i32_16x16x64_i8 v[68:71], v[104:107], v[32:35], v[168:171]
	v_mfma_i32_16x16x64_i8 v[128:131], v[116:119], v[36:39], v[68:71]
	v_mfma_i32_16x16x64_i8 v[68:71], v[4:7], v[40:43], v[204:207]
	v_mfma_i32_16x16x64_i8 v[112:115], v[12:15], v[44:47], v[68:71]
	v_mfma_i32_16x16x64_i8 v[68:71], v[104:107], v[40:43], v[214:217]
	v_mfma_i32_16x16x64_i8 v[108:111], v[116:119], v[44:47], v[68:71]
	v_mfma_i32_16x16x64_i8 v[68:71], v[4:7], v[48:51], v[232:235]
	v_mfma_i32_16x16x64_i8 v[4:7], v[4:7], v[56:59], v[24:27]
	v_mfma_i32_16x16x64_i8 v[96:99], v[12:15], v[52:55], v[68:71]
	v_mfma_i32_16x16x64_i8 v[68:71], v[104:107], v[48:51], v[236:239]
	v_mfma_i32_16x16x64_i8 v[76:79], v[12:15], v[88:91], v[4:7]
	v_mfma_i32_16x16x64_i8 v[4:7], v[104:107], v[56:59], v[16:19]
	v_mfma_i32_16x16x64_i8 v[92:95], v[116:119], v[52:55], v[68:71]
	v_mfma_i32_16x16x64_i8 v[72:75], v[116:119], v[88:91], v[4:7]
	v_mfma_i32_16x16x64_i8 v[4:7], v[124:127], v[32:35], v[20:23]
	v_mfma_i32_16x16x64_i8 v[120:123], v[248:251], v[36:39], v[4:7]
	v_mfma_i32_16x16x64_i8 v[4:7], v[208:211], v[32:35], v[28:31]
	v_mfma_i32_16x16x64_i8 v[116:119], v[64:67], v[36:39], v[4:7]
	v_mfma_i32_16x16x64_i8 v[4:7], v[124:127], v[40:43], v[60:63]
	v_mfma_i32_16x16x64_i8 v[104:107], v[248:251], v[44:47], v[4:7]
	v_mfma_i32_16x16x64_i8 v[4:7], v[208:211], v[40:43], v[100:103]
	v_mfma_i32_16x16x64_i8 v[100:103], v[64:67], v[44:47], v[4:7]
	v_mfma_i32_16x16x64_i8 v[4:7], v[124:127], v[48:51], v[240:243]
	v_mfma_i32_16x16x64_i8 v[84:87], v[248:251], v[52:55], v[4:7]
	v_mfma_i32_16x16x64_i8 v[4:7], v[208:211], v[48:51], v[244:247]
	v_mfma_i32_16x16x64_i8 v[80:83], v[64:67], v[52:55], v[4:7]
	v_mfma_i32_16x16x64_i8 v[4:7], v[124:127], v[56:59], v[8:11]
	v_mfma_i32_16x16x64_i8 v[0:3], v[208:211], v[56:59], v[0:3]
	v_mfma_i32_16x16x64_i8 v[68:71], v[248:251], v[88:91], v[4:7]
	v_mfma_i32_16x16x64_i8 v[64:67], v[64:67], v[88:91], v[0:3]
	s_barrier
	s_add_u32 s44, s27, s48
	s_addc_u32 s45, s29, s49
	s_add_u32 s79, s42, 0x200
	s_addc_u32 s80, s43, 0
	s_add_i32 s81, s54, 0
	s_add_i32 s81, s81, 0x20000

.LBB0_933:
	ds_read_b128 v[0:3], v227
	ds_read_b128 v[4:7], v227 offset:1024
	ds_read_b128 v[8:11], v227 offset:2048
	ds_read_b128 v[12:15], v227 offset:3072
	ds_read_b128 v[16:19], v226
	ds_read_b128 v[20:23], v226 offset:1024
	ds_read_b128 v[24:27], v226 offset:2048
	ds_read_b128 v[28:31], v226 offset:3072
	ds_read_b128 v[32:35], v228
	ds_read_b128 v[36:39], v228 offset:1024
	ds_read_b128 v[40:43], v228 offset:2048
	ds_read_b128 v[44:47], v228 offset:3072
	ds_read_b128 v[48:51], v228 offset:4096
	ds_read_b128 v[52:55], v228 offset:5120
	ds_read_b128 v[56:59], v228 offset:6144
	ds_read_b128 v[60:63], v228 offset:7168
	s_add_u32 s42, s46, 0x100
	s_addc_u32 s43, s47, 0
	s_and_b64 s[48:49], s[48:49], exec
	s_cselect_b32 s54, s76, s42
	s_cselect_b32 s55, s9, s43
	s_cselect_b32 s51, s35, s80
	s_cselect_b32 s50, s77, s79
	s_add_u32 s48, s54, 0x80
	s_addc_u32 s49, s55, 0
	s_add_u32 s52, s50, 0x80
	s_addc_u32 s53, s51, 0
	s_add_u32 s46, s46, 0x40080
	s_addc_u32 s47, s47, 0
	s_add_i32 m0, s31, 0xc000
	s_nop 0
	global_load_lds_dwordx4 v219, s[46:47]
	s_add_i32 m0, s31, 0xe000
	s_nop 0
	global_load_lds_dwordx4 v221, s[46:47]
	s_waitcnt vmcnt(8) lgkmcnt(0)
	s_barrier
	v_mfma_i32_16x16x64_i8 v[180:183], v[8:11], v[40:43], v[180:183]
	v_mfma_i32_16x16x64_i8 v[164:167], v[0:3], v[48:51], v[164:167]
	v_mfma_i32_16x16x64_i8 v[148:151], v[0:3], v[56:59], v[148:151]
	v_mfma_i32_16x16x64_i8 v[160:163], v[8:11], v[48:51], v[160:163]
	v_mfma_i32_16x16x64_i8 v[144:147], v[8:11], v[56:59], v[144:147]
	v_mfma_i32_16x16x64_i8 v[88:91], v[0:3], v[32:35], v[200:203]
	v_mfma_i32_16x16x64_i8 v[168:171], v[0:3], v[40:43], v[184:187]
	v_mfma_i32_16x16x64_i8 v[124:127], v[8:11], v[32:35], v[196:199]
	v_mfma_i32_16x16x64_i8 v[180:183], v[12:15], v[44:47], v[180:183]
	v_mfma_i32_16x16x64_i8 v[164:167], v[4:7], v[52:55], v[164:167]
	v_mfma_i32_16x16x64_i8 v[148:151], v[4:7], v[60:63], v[148:151]
	v_mfma_i32_16x16x64_i8 v[160:163], v[12:15], v[52:55], v[160:163]
	v_mfma_i32_16x16x64_i8 v[144:147], v[12:15], v[60:63], v[144:147]
	v_mfma_i32_16x16x64_i8 v[88:91], v[4:7], v[36:39], v[88:91]
	v_mfma_i32_16x16x64_i8 v[168:171], v[4:7], v[44:47], v[168:171]
	v_mfma_i32_16x16x64_i8 v[124:127], v[12:15], v[36:39], v[124:127]
	v_mfma_i32_16x16x64_i8 v[184:187], v[16:19], v[32:35], v[192:195]
	v_mfma_i32_16x16x64_i8 v[32:35], v[24:27], v[32:35], v[188:191]
	v_mfma_i32_16x16x64_i8 v[192:195], v[20:23], v[36:39], v[184:187]
	v_mfma_i32_16x16x64_i8 v[32:35], v[28:31], v[36:39], v[32:35]
	v_mfma_i32_16x16x64_i8 v[36:39], v[16:19], v[40:43], v[176:179]
	v_mfma_i32_16x16x64_i8 v[40:43], v[24:27], v[40:43], v[172:175]
	v_mfma_i32_16x16x64_i8 v[36:39], v[20:23], v[44:47], v[36:39]
	v_mfma_i32_16x16x64_i8 v[40:43], v[28:31], v[44:47], v[40:43]
	v_mfma_i32_16x16x64_i8 v[44:47], v[16:19], v[48:51], v[156:159]
	v_mfma_i32_16x16x64_i8 v[48:51], v[24:27], v[48:51], v[152:155]
	v_mfma_i32_16x16x64_i8 v[44:47], v[20:23], v[52:55], v[44:47]
	v_mfma_i32_16x16x64_i8 v[48:51], v[28:31], v[52:55], v[48:51]
	v_mfma_i32_16x16x64_i8 v[52:55], v[16:19], v[56:59], v[140:143]
	v_mfma_i32_16x16x64_i8 v[56:59], v[24:27], v[56:59], v[136:139]
	v_mfma_i32_16x16x64_i8 v[52:55], v[20:23], v[60:63], v[52:55]
	v_mfma_i32_16x16x64_i8 v[56:59], v[28:31], v[60:63], v[56:59]
	s_barrier
	ds_read_b128 v[60:63], v228 offset:16384
	ds_read_b128 v[136:139], v228 offset:17408
	ds_read_b128 v[140:143], v228 offset:18432
	ds_read_b128 v[152:155], v228 offset:19456
	ds_read_b128 v[156:159], v228 offset:20480
	ds_read_b128 v[172:175], v228 offset:21504
	ds_read_b128 v[176:179], v228 offset:22528
	ds_read_b128 v[184:187], v228 offset:23552
	s_add_i32 m0, s31, 0x10000
	s_nop 0
	global_load_lds_dwordx4 v220, s[50:51]
	s_add_i32 m0, s31, 0x12000
	s_nop 0
	global_load_lds_dwordx4 v222, s[50:51]
	s_add_u32 s46, s50, 0x40000
	s_addc_u32 s47, s51, 0
	s_add_i32 m0, s31, 0x14000
	s_nop 0
	global_load_lds_dwordx4 v220, s[46:47]
	s_add_i32 m0, s31, 0x16000
	s_nop 0
	global_load_lds_dwordx4 v222, s[46:47]
	s_add_i32 m0, s31, 0
	s_nop 0
	global_load_lds_dwordx4 v219, s[54:55]
	s_add_i32 m0, s31, 0x2000
	s_nop 0
	global_load_lds_dwordx4 v221, s[54:55]
	s_waitcnt vmcnt(8) lgkmcnt(0)
	s_barrier
	v_mfma_i32_16x16x64_i8 v[132:135], v[0:3], v[60:63], v[132:135]
	v_mfma_i32_16x16x64_i8 v[112:115], v[0:3], v[140:143], v[112:115]
	v_mfma_i32_16x16x64_i8 v[96:99], v[0:3], v[156:159], v[96:99]
	v_mfma_i32_16x16x64_i8 v[0:3], v[0:3], v[176:179], v[76:79]
	v_mfma_i32_16x16x64_i8 v[128:131], v[8:11], v[60:63], v[128:131]
	v_mfma_i32_16x16x64_i8 v[108:111], v[8:11], v[140:143], v[108:111]
	v_mfma_i32_16x16x64_i8 v[92:95], v[8:11], v[156:159], v[92:95]
	v_mfma_i32_16x16x64_i8 v[76:79], v[4:7], v[184:187], v[0:3]
	v_mfma_i32_16x16x64_i8 v[0:3], v[8:11], v[176:179], v[72:75]
	v_mfma_i32_16x16x64_i8 v[132:135], v[4:7], v[136:139], v[132:135]
	v_mfma_i32_16x16x64_i8 v[128:131], v[12:15], v[136:139], v[128:131]
	v_mfma_i32_16x16x64_i8 v[112:115], v[4:7], v[152:155], v[112:115]
	v_mfma_i32_16x16x64_i8 v[108:111], v[12:15], v[152:155], v[108:111]
	v_mfma_i32_16x16x64_i8 v[96:99], v[4:7], v[172:175], v[96:99]
	v_mfma_i32_16x16x64_i8 v[92:95], v[12:15], v[172:175], v[92:95]
	v_mfma_i32_16x16x64_i8 v[72:75], v[12:15], v[184:187], v[0:3]
	v_mfma_i32_16x16x64_i8 v[0:3], v[16:19], v[60:63], v[120:123]
	v_mfma_i32_16x16x64_i8 v[120:123], v[20:23], v[136:139], v[0:3]
	v_mfma_i32_16x16x64_i8 v[0:3], v[24:27], v[60:63], v[116:119]
	v_mfma_i32_16x16x64_i8 v[116:119], v[28:31], v[136:139], v[0:3]
	v_mfma_i32_16x16x64_i8 v[0:3], v[16:19], v[140:143], v[104:107]
	v_mfma_i32_16x16x64_i8 v[104:107], v[20:23], v[152:155], v[0:3]
	v_mfma_i32_16x16x64_i8 v[0:3], v[24:27], v[140:143], v[100:103]
	v_mfma_i32_16x16x64_i8 v[100:103], v[28:31], v[152:155], v[0:3]
	v_mfma_i32_16x16x64_i8 v[0:3], v[16:19], v[156:159], v[84:87]
	v_mfma_i32_16x16x64_i8 v[84:87], v[20:23], v[172:175], v[0:3]
	v_mfma_i32_16x16x64_i8 v[0:3], v[24:27], v[156:159], v[80:83]
	v_mfma_i32_16x16x64_i8 v[80:83], v[28:31], v[172:175], v[0:3]
	v_mfma_i32_16x16x64_i8 v[0:3], v[16:19], v[176:179], v[68:71]
	v_mfma_i32_16x16x64_i8 v[68:71], v[20:23], v[184:187], v[0:3]
	v_mfma_i32_16x16x64_i8 v[0:3], v[24:27], v[176:179], v[64:67]
	v_mfma_i32_16x16x64_i8 v[64:67], v[28:31], v[184:187], v[0:3]
	s_barrier
	ds_read_b128 v[16:19], v229
	ds_read_b128 v[8:11], v229 offset:1024
	ds_read_b128 v[4:7], v229 offset:2048
	s_nop 1
	ds_read_b128 v[0:3], v229 offset:3072
	ds_read_b128 v[28:31], v230
	ds_read_b128 v[24:27], v230 offset:1024
	ds_read_b128 v[20:23], v230 offset:2048
	ds_read_b128 v[12:15], v230 offset:3072
	ds_read_b128 v[60:63], v228 offset:32768
	ds_read_b128 v[136:139], v228 offset:33792
	ds_read_b128 v[140:143], v228 offset:34816
	ds_read_b128 v[152:155], v228 offset:35840
	ds_read_b128 v[204:207], v228 offset:36864
	ds_read_b128 v[208:211], v228 offset:37888
	ds_read_b128 v[214:217], v228 offset:38912
	ds_read_b128 v[232:235], v228 offset:39936
	s_add_u32 s46, s54, 0x40000
	s_addc_u32 s47, s55, 0
	s_add_i32 m0, s31, 0x4000
	s_nop 0
	global_load_lds_dwordx4 v219, s[46:47]
	s_add_i32 m0, s31, 0x6000
	s_nop 0
	global_load_lds_dwordx4 v221, s[46:47]
	s_waitcnt vmcnt(8) lgkmcnt(0)
	s_barrier
	v_mfma_i32_16x16x64_i8 v[88:91], v[16:19], v[60:63], v[88:91]
	v_mfma_i32_16x16x64_i8 v[200:203], v[8:11], v[136:139], v[88:91]
	v_mfma_i32_16x16x64_i8 v[88:91], v[4:7], v[60:63], v[124:127]
	v_mfma_i32_16x16x64_i8 v[196:199], v[0:3], v[136:139], v[88:91]
	v_mfma_i32_16x16x64_i8 v[88:91], v[16:19], v[140:143], v[168:171]
	v_mfma_i32_16x16x64_i8 v[184:187], v[8:11], v[152:155], v[88:91]
	v_mfma_i32_16x16x64_i8 v[88:91], v[4:7], v[140:143], v[180:183]
	v_mfma_i32_16x16x64_i8 v[180:183], v[0:3], v[152:155], v[88:91]
	v_mfma_i32_16x16x64_i8 v[88:91], v[16:19], v[204:207], v[164:167]
	v_mfma_i32_16x16x64_i8 v[164:167], v[8:11], v[208:211], v[88:91]
	v_mfma_i32_16x16x64_i8 v[88:91], v[4:7], v[204:207], v[160:163]
	v_mfma_i32_16x16x64_i8 v[160:163], v[0:3], v[208:211], v[88:91]
	v_mfma_i32_16x16x64_i8 v[88:91], v[16:19], v[214:217], v[148:151]
	v_mfma_i32_16x16x64_i8 v[148:151], v[8:11], v[232:235], v[88:91]
	v_mfma_i32_16x16x64_i8 v[88:91], v[4:7], v[214:217], v[144:147]
	v_mfma_i32_16x16x64_i8 v[144:147], v[0:3], v[232:235], v[88:91]
	v_mfma_i32_16x16x64_i8 v[32:35], v[20:23], v[60:63], v[32:35]
	v_mfma_i32_16x16x64_i8 v[188:191], v[12:15], v[136:139], v[32:35]
	v_mfma_i32_16x16x64_i8 v[32:35], v[28:31], v[140:143], v[36:39]
	v_mfma_i32_16x16x64_i8 v[176:179], v[24:27], v[152:155], v[32:35]
	v_mfma_i32_16x16x64_i8 v[32:35], v[20:23], v[140:143], v[40:43]
	v_mfma_i32_16x16x64_i8 v[172:175], v[12:15], v[152:155], v[32:35]
	v_mfma_i32_16x16x64_i8 v[32:35], v[28:31], v[204:207], v[44:47]
	v_mfma_i32_16x16x64_i8 v[156:159], v[24:27], v[208:211], v[32:35]
	v_mfma_i32_16x16x64_i8 v[32:35], v[20:23], v[204:207], v[48:51]
	v_mfma_i32_16x16x64_i8 v[152:155], v[12:15], v[208:211], v[32:35]
	v_mfma_i32_16x16x64_i8 v[32:35], v[28:31], v[214:217], v[52:55]
	v_mfma_i32_16x16x64_i8 v[88:91], v[28:31], v[60:63], v[192:195]
	v_mfma_i32_16x16x64_i8 v[140:143], v[24:27], v[232:235], v[32:35]
	v_mfma_i32_16x16x64_i8 v[32:35], v[20:23], v[214:217], v[56:59]
	v_mfma_i32_16x16x64_i8 v[192:195], v[24:27], v[136:139], v[88:91]
	v_mfma_i32_16x16x64_i8 v[136:139], v[12:15], v[232:235], v[32:35]
	s_barrier
	ds_read_b128 v[60:63], v228 offset:49152
	ds_read_b128 v[56:59], v228 offset:50176
	ds_read_b128 v[52:55], v228 offset:51200
	ds_read_b128 v[48:51], v228 offset:52224
	ds_read_b128 v[44:47], v228 offset:53248
	ds_read_b128 v[40:43], v228 offset:54272
	ds_read_b128 v[36:39], v228 offset:55296
	ds_read_b128 v[32:35], v228 offset:56320
	s_add_i32 m0, s31, 0x18000
	s_nop 0
	global_load_lds_dwordx4 v220, s[52:53]
	s_add_i32 m0, s31, 0x1a000
	s_nop 0
	global_load_lds_dwordx4 v222, s[52:53]
	s_add_u32 s46, s50, 0x40080
	s_addc_u32 s47, s51, 0
	s_add_i32 m0, s31, 0x1c000
	s_nop 0
	global_load_lds_dwordx4 v220, s[46:47]
	s_add_i32 m0, s31, 0x1e000
	s_nop 0
	global_load_lds_dwordx4 v222, s[46:47]
	s_add_i32 m0, s31, 0x8000
	s_nop 0
	global_load_lds_dwordx4 v219, s[48:49]
	s_add_i32 m0, s31, 0xa000
	s_nop 0
	global_load_lds_dwordx4 v221, s[48:49]
	s_waitcnt vmcnt(8) lgkmcnt(0)
	s_barrier
	v_mfma_i32_16x16x64_i8 v[88:91], v[16:19], v[60:63], v[132:135]
	v_mfma_i32_16x16x64_i8 v[132:135], v[8:11], v[56:59], v[88:91]
	v_mfma_i32_16x16x64_i8 v[88:91], v[4:7], v[60:63], v[128:131]
	v_mfma_i32_16x16x64_i8 v[128:131], v[0:3], v[56:59], v[88:91]
	v_mfma_i32_16x16x64_i8 v[88:91], v[16:19], v[52:55], v[112:115]
	v_mfma_i32_16x16x64_i8 v[112:115], v[8:11], v[48:51], v[88:91]
	v_mfma_i32_16x16x64_i8 v[88:91], v[4:7], v[52:55], v[108:111]
	v_mfma_i32_16x16x64_i8 v[108:111], v[0:3], v[48:51], v[88:91]
	v_mfma_i32_16x16x64_i8 v[88:91], v[16:19], v[44:47], v[96:99]
	v_mfma_i32_16x16x64_i8 v[96:99], v[8:11], v[40:43], v[88:91]
	v_mfma_i32_16x16x64_i8 v[88:91], v[4:7], v[44:47], v[92:95]
	v_mfma_i32_16x16x64_i8 v[76:79], v[16:19], v[36:39], v[76:79]
	v_mfma_i32_16x16x64_i8 v[72:75], v[4:7], v[36:39], v[72:75]
	v_mfma_i32_16x16x64_i8 v[92:95], v[0:3], v[40:43], v[88:91]
	v_mfma_i32_16x16x64_i8 v[76:79], v[8:11], v[32:35], v[76:79]
	v_mfma_i32_16x16x64_i8 v[72:75], v[0:3], v[32:35], v[72:75]
	v_mfma_i32_16x16x64_i8 v[88:91], v[28:31], v[60:63], v[120:123]
	v_mfma_i32_16x16x64_i8 v[120:123], v[24:27], v[56:59], v[88:91]
	v_mfma_i32_16x16x64_i8 v[88:91], v[20:23], v[60:63], v[116:119]
	v_mfma_i32_16x16x64_i8 v[116:119], v[12:15], v[56:59], v[88:91]
	v_mfma_i32_16x16x64_i8 v[88:91], v[28:31], v[52:55], v[104:107]
	v_mfma_i32_16x16x64_i8 v[104:107], v[24:27], v[48:51], v[88:91]
	v_mfma_i32_16x16x64_i8 v[88:91], v[20:23], v[52:55], v[100:103]
	v_mfma_i32_16x16x64_i8 v[84:87], v[28:31], v[44:47], v[84:87]
	v_mfma_i32_16x16x64_i8 v[80:83], v[20:23], v[44:47], v[80:83]
	v_mfma_i32_16x16x64_i8 v[68:71], v[28:31], v[36:39], v[68:71]
	v_mfma_i32_16x16x64_i8 v[64:67], v[20:23], v[36:39], v[64:67]
	v_mfma_i32_16x16x64_i8 v[100:103], v[12:15], v[48:51], v[88:91]
	v_mfma_i32_16x16x64_i8 v[84:87], v[24:27], v[40:43], v[84:87]
	v_mfma_i32_16x16x64_i8 v[80:83], v[12:15], v[40:43], v[80:83]
	v_mfma_i32_16x16x64_i8 v[68:71], v[24:27], v[32:35], v[68:71]
	v_mfma_i32_16x16x64_i8 v[64:67], v[12:15], v[32:35], v[64:67]
	s_barrier
	s_add_i32 s37, s37, 2
	s_add_u32 s79, s79, 0x100
	s_addc_u32 s80, s80, 0
	s_cmp_gt_u32 s37, 13
	s_cbranch_scc1 .LBB0_935
	s_mov_b64 s[46:47], s[42:43]
	s_branch .LBB0_931

.LBB0_1095:
	s_cmp_lt_i32 s92, 9
	s_cselect_b64 s[4:5], -1, 0
	s_cmp_gt_i32 s93, 8
	s_cselect_b64 s[6:7], -1, 0
	s_and_b64 s[4:5], s[4:5], s[6:7]
	s_andn2_b64 vcc, exec, s[4:5]
	s_cbranch_vccnz .LBB0_1170
	v_mbcnt_lo_u32_b32 v0, -1, 0
	s_and_b32 s2, s3, 0xffffffc0
	s_waitcnt vmcnt(12)
	v_mbcnt_hi_u32_b32 v138, -1, v0
	v_add_u32_e32 v0, s2, v138
	s_nop 0
	v_readfirstlane_b32 s11, v0
	s_ashr_i32 s14, s11, 6
	s_cmpk_gt_i32 s87, 0x3ff
	s_cbranch_scc1 .LBB0_1116
	v_bfe_i32 v3, v0, 27, 1
	s_waitcnt lgkmcnt(0)
	v_lshlrev_b32_e32 v1, 4, v0
	v_lshrrev_b32_e32 v3, 22, v3
	v_add_u32_e32 v3, v1, v3
	v_and_b32_e32 v3, 0xfffffc00, v3
	v_sub_u32_e32 v3, v1, v3
	v_ashrrev_i32_e32 v2, 31, v0
	v_lshrrev_b32_e32 v4, 4, v3
	v_lshrrev_b32_e32 v2, 26, v2
	v_bitop3_b32 v3, v4, v3, 32 bitop3:0x6c
	v_add_u32_e32 v2, v0, v2
	v_ashrrev_i32_e32 v5, 31, v3
	v_ashrrev_i32_e32 v2, 6, v2
	v_lshrrev_b32_e32 v5, 26, v5
	v_lshlrev_b32_e32 v4, 3, v2
	v_add_u32_e32 v5, v3, v5
	v_and_b32_e32 v4, -16, v4
	v_ashrrev_i32_e32 v6, 6, v5
	v_and_b32_e32 v5, 0xc0, v5
	v_add_u32_e32 v4, v6, v4
	v_sub_u32_e32 v3, v3, v5
	v_mov_b32_e32 v5, 1
	v_lshlrev_b32_e32 v2, 5, v2
	v_ashrrev_i16_sdwa v3, v5, sext(v3) dst_sel:DWORD dst_unused:UNUSED_PAD src0_sel:DWORD src1_sel:BYTE_0
	v_lshlrev_b32_e32 v7, 1, v4
	s_waitcnt vmcnt(3)
	v_lshrrev_b32_e32 v8, 2, v4
	v_and_b32_e32 v6, 3, v6
	s_mov_b32 s2, 0xfffe0
	v_and_b32_e32 v2, 32, v2
	v_bfe_i32 v3, v3, 0, 16
	v_and_b32_e32 v7, 24, v7
	v_and_b32_e32 v8, 4, v8
	v_and_or_b32 v6, v4, s2, v6
	v_or3_b32 v6, v6, v8, v7
	v_add_lshl_u32 v2, v2, v3, 1
	v_add_u32_e32 v1, 0x2000, v1
	v_lshl_add_u32 v139, v4, 12, v2
	v_lshl_add_u32 v140, v6, 12, v2
	v_ashrrev_i32_e32 v2, 31, v1
	v_lshrrev_b32_e32 v2, 22, v2
	v_add_u32_e32 v2, v1, v2
	v_ashrrev_i32_e32 v2, 10, v2
	v_mul_i32_i24_e32 v3, 0x400, v2
	v_sub_u32_e32 v1, v1, v3
	s_add_u32 s42, s70, 0x3a800000
	v_lshrrev_b32_e32 v3, 4, v1
	s_addc_u32 s43, s71, 0
	v_bitop3_b32 v1, v3, v1, 32 bitop3:0x6c
	s_add_u32 s44, s70, 0x8000000
	v_ashrrev_i32_e32 v4, 31, v1
	s_addc_u32 s45, s71, 0
	v_lshrrev_b32_e32 v4, 26, v4
	s_ashr_i32 s46, s87, 31
	v_lshlrev_b32_e32 v3, 3, v2
	v_add_u32_e32 v4, v1, v4
	s_lshr_b32 s4, s46, 29
	v_and_b32_e32 v3, -16, v3
	v_ashrrev_i32_e32 v6, 6, v4
	s_add_i32 s4, s87, s4
	v_add_u32_e32 v3, v6, v3
	v_and_b32_e32 v6, 3, v6
	s_and_b32 s5, s4, -8
	v_and_or_b32 v6, v3, s2, v6
	s_lshl_b32 s2, s14, 10
	s_sub_i32 s5, s87, s5
	s_ashr_i32 s15, s11, 8
	s_add_i32 s2, s2, 0
	s_lshl_b32 s7, s5, 7
	s_ashr_i32 s4, s4, 3
	s_mul_i32 s6, s5, 0x81
	s_cmp_lt_i32 s5, 0
	s_cselect_b32 s5, s6, s7
	s_add_i32 s4, s5, s4
	s_ashr_i32 s5, s4, 31
	s_lshr_b32 s5, s5, 26
	s_add_i32 s5, s4, s5
	s_ashr_i32 s6, s5, 6
	s_andn2_b32 s5, s5, 63
	s_sub_i32 s4, s4, s5
	s_bfe_i32 s5, s4, 0x80000
	s_bfe_u32 s5, s5, 0x3000c
	s_add_i32 s5, s4, s5
	s_bfe_i32 s7, s5, 0x80000
	s_and_b32 s5, s5, 0xf8
	s_sub_i32 s4, s4, s5
	s_lshl_b32 s6, s6, 3
	s_sext_i32_i8 s4, s4
	s_add_i32 s28, s6, s4
	s_sext_i32_i16 s7, s7
	s_ashr_i32 s29, s28, 31
	s_lshr_b32 s10, s7, 3
	s_lshl_b64 s[4:5], s[28:29], 20
	v_and_b32_e32 v4, 0xc0, v4
	s_add_u32 s30, s42, s4
	v_sub_u32_e32 v1, v1, v4
	s_addc_u32 s31, s43, s5
	s_bfe_i64 s[4:5], s[10:11], 0x100000
	v_lshlrev_b32_e32 v2, 5, v2
	v_ashrrev_i16_sdwa v1, v5, sext(v1) dst_sel:DWORD dst_unused:UNUSED_PAD src0_sel:DWORD src1_sel:BYTE_0
	v_lshlrev_b32_e32 v4, 1, v3
	v_lshrrev_b32_e32 v5, 2, v3
	s_lshl_b64 s[4:5], s[4:5], 20
	v_and_b32_e32 v2, 32, v2
	v_bfe_i32 v1, v1, 0, 16
	v_and_b32_e32 v4, 24, v4
	v_and_b32_e32 v5, 4, v5
	s_add_u32 s34, s44, s4
	v_or3_b32 v4, v6, v5, v4
	v_add_lshl_u32 v1, v2, v1, 1
	s_addc_u32 s35, s45, s5
	s_add_i32 m0, s2, 0x10000
	s_nop 0
	global_load_lds_dwordx4 v140, s[34:35]
	v_lshl_add_u32 v142, v4, 12, v1
	s_add_i32 m0, s2, 0x12000
	s_nop 0
	global_load_lds_dwordx4 v142, s[34:35]
	s_add_u32 s4, s34, 0x80000
	s_addc_u32 s5, s35, 0
	s_add_i32 m0, s2, 0x14000
	s_nop 0
	global_load_lds_dwordx4 v140, s[4:5]
	v_lshl_add_u32 v141, v3, 12, v1
	s_add_i32 m0, s2, 0x16000
	s_nop 0
	global_load_lds_dwordx4 v142, s[4:5]
	s_add_i32 m0, s2, 0
	s_nop 0
	global_load_lds_dwordx4 v139, s[30:31]
	s_add_i32 m0, s2, 0x2000
	s_nop 0
	global_load_lds_dwordx4 v141, s[30:31]
	s_add_u32 s6, s30, 0x80000
	s_addc_u32 s7, s31, 0
	s_add_i32 m0, s2, 0x4000
	s_nop 0
	global_load_lds_dwordx4 v139, s[6:7]
	s_add_i32 m0, s2, 0x6000
	s_nop 0
	global_load_lds_dwordx4 v141, s[6:7]
	s_cmp_eq_u32 s15, 1
	s_cselect_b64 s[6:7], -1, 0
	s_cmp_lg_u32 s15, 1
	s_mov_b64 s[8:9], 0x80000
	s_cbranch_scc1 .LBB0_1099
	s_barrier

.LBB0_1108:
	s_ashr_i32 s23, s22, 31
	s_lshl_b64 s[24:25], s[22:23], 20
	s_add_u32 s24, s42, s24
	s_addc_u32 s25, s43, s25
	s_and_b64 s[26:27], s[4:5], exec
	ds_read_b128 v[0:3], v143
	ds_read_b128 v[4:7], v143 offset:1024
	ds_read_b128 v[8:11], v143 offset:2048
	s_waitcnt vmcnt(2)
	ds_read_b128 v[12:15], v143 offset:3072
	s_waitcnt vmcnt(1)
	ds_read_b128 v[16:19], v144
	s_waitcnt vmcnt(0)
	ds_read_b128 v[20:23], v144 offset:1024
	ds_read_b128 v[24:27], v144 offset:2048
	ds_read_b128 v[28:31], v144 offset:3072
	s_cselect_b32 s23, s25, s31
	s_cselect_b32 s51, s24, s30
	s_ashr_i32 s21, s20, 31
	s_lshl_b64 s[26:27], s[20:21], 20
	s_add_u32 s26, s44, s26
	s_addc_u32 s27, s45, s27
	s_and_b64 s[36:37], s[4:5], exec
	s_cselect_b32 s21, s27, s35
	s_cselect_b32 s52, s26, s34
	s_add_u32 s40, s30, 0x100
	s_addc_u32 s41, s31, 0
	s_add_u32 s54, s34, 0x100
	s_addc_u32 s55, s35, 0
	s_add_u32 s36, s30, 0x180
	s_addc_u32 s37, s31, 0
	ds_read_b128 v[32:35], v145
	ds_read_b128 v[36:39], v145 offset:1024
	ds_read_b128 v[40:43], v145 offset:2048
	ds_read_b128 v[44:47], v145 offset:3072
	ds_read_b128 v[48:51], v145 offset:4096
	ds_read_b128 v[52:55], v145 offset:5120
	ds_read_b128 v[56:59], v145 offset:6144
	ds_read_b128 v[60:63], v145 offset:7168
	s_add_u32 s38, s34, 0x180
	s_addc_u32 s39, s35, 0
	s_add_u32 s56, s30, 0x80080
	s_addc_u32 s57, s31, 0
	s_add_i32 m0, s2, 0xc000
	s_nop 0
	global_load_lds_dwordx4 v139, s[56:57]
	s_add_i32 m0, s2, 0xe000
	s_nop 0
	global_load_lds_dwordx4 v141, s[56:57]
	s_waitcnt vmcnt(8) lgkmcnt(0)
	s_barrier
	v_mfma_f32_16x16x32_bf16 v[64:67], v[0:3], v[32:35], 0
	v_mfma_f32_16x16x32_bf16 v[68:71], v[8:11], v[32:35], 0
	v_mfma_f32_16x16x32_bf16 v[76:79], v[8:11], v[40:43], 0
	v_mfma_f32_16x16x32_bf16 v[72:75], v[0:3], v[40:43], 0
	v_mfma_f32_16x16x32_bf16 v[80:83], v[0:3], v[48:51], 0
	v_mfma_f32_16x16x32_bf16 v[84:87], v[8:11], v[48:51], 0
	v_mfma_f32_16x16x32_bf16 v[92:95], v[8:11], v[56:59], 0
	v_mfma_f32_16x16x32_bf16 v[88:91], v[0:3], v[56:59], 0
	v_mfma_f32_16x16x32_bf16 v[64:67], v[4:7], v[36:39], v[64:67]
	v_mfma_f32_16x16x32_bf16 v[68:71], v[12:15], v[36:39], v[68:71]
	v_mfma_f32_16x16x32_bf16 v[76:79], v[12:15], v[44:47], v[76:79]
	v_mfma_f32_16x16x32_bf16 v[72:75], v[4:7], v[44:47], v[72:75]
	v_mfma_f32_16x16x32_bf16 v[80:83], v[4:7], v[52:55], v[80:83]
	v_mfma_f32_16x16x32_bf16 v[84:87], v[12:15], v[52:55], v[84:87]
	v_mfma_f32_16x16x32_bf16 v[96:99], v[12:15], v[60:63], v[92:95]
	v_mfma_f32_16x16x32_bf16 v[88:91], v[4:7], v[60:63], v[88:91]
	v_mfma_f32_16x16x32_bf16 v[92:95], v[16:19], v[32:35], 0
	v_mfma_f32_16x16x32_bf16 v[32:35], v[24:27], v[32:35], 0
	v_mfma_f32_16x16x32_bf16 v[104:107], v[20:23], v[36:39], v[92:95]
	v_mfma_f32_16x16x32_bf16 v[32:35], v[28:31], v[36:39], v[32:35]
	v_mfma_f32_16x16x32_bf16 v[36:39], v[16:19], v[40:43], 0
	v_mfma_f32_16x16x32_bf16 v[40:43], v[24:27], v[40:43], 0
	v_mfma_f32_16x16x32_bf16 v[36:39], v[20:23], v[44:47], v[36:39]
	v_mfma_f32_16x16x32_bf16 v[40:43], v[28:31], v[44:47], v[40:43]
	v_mfma_f32_16x16x32_bf16 v[44:47], v[16:19], v[48:51], 0
	v_mfma_f32_16x16x32_bf16 v[48:51], v[24:27], v[48:51], 0
	v_mfma_f32_16x16x32_bf16 v[44:47], v[20:23], v[52:55], v[44:47]
	v_mfma_f32_16x16x32_bf16 v[48:51], v[28:31], v[52:55], v[48:51]
	v_mfma_f32_16x16x32_bf16 v[52:55], v[16:19], v[56:59], 0
	v_mfma_f32_16x16x32_bf16 v[56:59], v[24:27], v[56:59], 0
	v_mfma_f32_16x16x32_bf16 v[52:55], v[20:23], v[60:63], v[52:55]
	v_mfma_f32_16x16x32_bf16 v[60:63], v[28:31], v[60:63], v[56:59]
	s_barrier
	s_nop 3
	ds_read_b128 v[56:59], v145 offset:16384
	ds_read_b128 v[92:95], v145 offset:17408
	ds_read_b128 v[100:103], v145 offset:18432
	ds_read_b128 v[108:111], v145 offset:19456
	ds_read_b128 v[112:115], v145 offset:20480
	ds_read_b128 v[116:119], v145 offset:21504
	ds_read_b128 v[120:123], v145 offset:22528
	ds_read_b128 v[124:127], v145 offset:23552
	s_add_i32 m0, s2, 0x10000
	s_nop 0
	global_load_lds_dwordx4 v140, s[54:55]
	s_add_i32 m0, s2, 0x12000
	s_nop 0
	global_load_lds_dwordx4 v142, s[54:55]
	s_add_u32 s54, s34, 0x80100
	s_addc_u32 s55, s35, 0
	s_add_i32 m0, s2, 0x14000
	s_nop 0
	global_load_lds_dwordx4 v140, s[54:55]
	s_add_i32 m0, s2, 0x16000
	s_nop 0
	global_load_lds_dwordx4 v142, s[54:55]
	s_add_i32 m0, s2, 0
	s_nop 0
	global_load_lds_dwordx4 v139, s[40:41]
	s_add_i32 m0, s2, 0x2000
	s_nop 0
	global_load_lds_dwordx4 v141, s[40:41]
	s_waitcnt vmcnt(8) lgkmcnt(0)
	s_barrier
	v_mfma_f32_16x16x32_bf16 v[132:135], v[0:3], v[56:59], 0
	v_mfma_f32_16x16x32_bf16 v[152:155], v[0:3], v[100:103], 0
	v_mfma_f32_16x16x32_bf16 v[160:163], v[0:3], v[112:115], 0
	v_mfma_f32_16x16x32_bf16 v[0:3], v[0:3], v[120:123], 0
	v_mfma_f32_16x16x32_bf16 v[132:135], v[4:7], v[92:95], v[132:135]
	v_mfma_f32_16x16x32_bf16 v[152:155], v[4:7], v[108:111], v[152:155]
	v_mfma_f32_16x16x32_bf16 v[160:163], v[4:7], v[116:119], v[160:163]
	v_mfma_f32_16x16x32_bf16 v[0:3], v[4:7], v[124:127], v[0:3]
	v_mfma_f32_16x16x32_bf16 v[4:7], v[8:11], v[120:123], 0
	v_mfma_f32_16x16x32_bf16 v[148:151], v[8:11], v[56:59], 0
	v_mfma_f32_16x16x32_bf16 v[156:159], v[8:11], v[100:103], 0
	v_mfma_f32_16x16x32_bf16 v[164:167], v[8:11], v[112:115], 0
	v_mfma_f32_16x16x32_bf16 v[4:7], v[12:15], v[124:127], v[4:7]
	v_mfma_f32_16x16x32_bf16 v[148:151], v[12:15], v[92:95], v[148:151]
	v_mfma_f32_16x16x32_bf16 v[156:159], v[12:15], v[108:111], v[156:159]
	v_mfma_f32_16x16x32_bf16 v[164:167], v[12:15], v[116:119], v[164:167]
	v_mfma_f32_16x16x32_bf16 v[12:15], v[24:27], v[56:59], 0
	v_mfma_f32_16x16x32_bf16 v[168:171], v[28:31], v[92:95], v[12:15]
	v_mfma_f32_16x16x32_bf16 v[12:15], v[16:19], v[100:103], 0
	v_mfma_f32_16x16x32_bf16 v[172:175], v[20:23], v[108:111], v[12:15]
	v_mfma_f32_16x16x32_bf16 v[12:15], v[24:27], v[100:103], 0
	v_mfma_f32_16x16x32_bf16 v[176:179], v[28:31], v[108:111], v[12:15]
	v_mfma_f32_16x16x32_bf16 v[12:15], v[16:19], v[112:115], 0
	v_mfma_f32_16x16x32_bf16 v[180:183], v[20:23], v[116:119], v[12:15]
	v_mfma_f32_16x16x32_bf16 v[12:15], v[24:27], v[112:115], 0
	v_mfma_f32_16x16x32_bf16 v[8:11], v[16:19], v[56:59], 0
	v_mfma_f32_16x16x32_bf16 v[184:187], v[28:31], v[116:119], v[12:15]
	v_mfma_f32_16x16x32_bf16 v[12:15], v[16:19], v[120:123], 0
	v_mfma_f32_16x16x32_bf16 v[8:11], v[20:23], v[92:95], v[8:11]
	v_mfma_f32_16x16x32_bf16 v[188:191], v[20:23], v[124:127], v[12:15]
	v_mfma_f32_16x16x32_bf16 v[12:15], v[24:27], v[120:123], 0
	v_mfma_f32_16x16x32_bf16 v[192:195], v[28:31], v[124:127], v[12:15]
	s_barrier
	s_nop 4
	ds_read_b128 v[12:15], v146
	ds_read_b128 v[16:19], v146 offset:1024
	ds_read_b128 v[24:27], v146 offset:2048
	ds_read_b128 v[196:199], v146 offset:3072
	ds_read_b128 v[200:203], v147
	ds_read_b128 v[204:207], v147 offset:1024
	ds_read_b128 v[208:211], v147 offset:2048
	ds_read_b128 v[212:215], v147 offset:3072
	ds_read_b128 v[20:23], v145 offset:32768
	ds_read_b128 v[28:31], v145 offset:33792
	ds_read_b128 v[216:219], v145 offset:34816
	ds_read_b128 v[220:223], v145 offset:35840
	ds_read_b128 v[224:227], v145 offset:36864
	ds_read_b128 v[228:231], v145 offset:37888
	ds_read_b128 v[232:235], v145 offset:38912
	ds_read_b128 v[236:239], v145 offset:39936
	s_add_u32 s40, s30, 0x80100
	s_addc_u32 s41, s31, 0
	s_add_i32 m0, s2, 0x4000
	s_nop 0
	global_load_lds_dwordx4 v139, s[40:41]
	s_add_i32 m0, s2, 0x6000
	s_nop 0
	global_load_lds_dwordx4 v141, s[40:41]
	s_waitcnt vmcnt(8) lgkmcnt(0)
	s_barrier
	v_mfma_f32_16x16x32_bf16 v[56:59], v[12:15], v[20:23], v[64:67]
	v_mfma_f32_16x16x32_bf16 v[116:119], v[16:19], v[28:31], v[56:59]
	v_mfma_f32_16x16x32_bf16 v[56:59], v[24:27], v[20:23], v[68:71]
	v_mfma_f32_16x16x32_bf16 v[112:115], v[196:199], v[28:31], v[56:59]
	v_mfma_f32_16x16x32_bf16 v[56:59], v[12:15], v[216:219], v[72:75]
	v_mfma_f32_16x16x32_bf16 v[108:111], v[16:19], v[220:223], v[56:59]
	v_mfma_f32_16x16x32_bf16 v[56:59], v[24:27], v[216:219], v[76:79]
	v_mfma_f32_16x16x32_bf16 v[100:103], v[196:199], v[220:223], v[56:59]
	v_mfma_f32_16x16x32_bf16 v[56:59], v[12:15], v[224:227], v[80:83]
	v_mfma_f32_16x16x32_bf16 v[92:95], v[16:19], v[228:231], v[56:59]
	v_mfma_f32_16x16x32_bf16 v[56:59], v[24:27], v[224:227], v[84:87]
	v_mfma_f32_16x16x32_bf16 v[84:87], v[196:199], v[228:231], v[56:59]
	v_mfma_f32_16x16x32_bf16 v[56:59], v[12:15], v[232:235], v[88:91]
	v_mfma_f32_16x16x32_bf16 v[72:75], v[16:19], v[236:239], v[56:59]
	v_mfma_f32_16x16x32_bf16 v[56:59], v[24:27], v[232:235], v[96:99]
	v_mfma_f32_16x16x32_bf16 v[56:59], v[196:199], v[236:239], v[56:59]
	v_mfma_f32_16x16x32_bf16 v[64:67], v[200:203], v[20:23], v[104:107]
	v_mfma_f32_16x16x32_bf16 v[20:23], v[208:211], v[20:23], v[32:35]
	v_mfma_f32_16x16x32_bf16 v[120:123], v[212:215], v[28:31], v[20:23]
	v_mfma_f32_16x16x32_bf16 v[20:23], v[200:203], v[216:219], v[36:39]
	v_mfma_f32_16x16x32_bf16 v[104:107], v[204:207], v[220:223], v[20:23]
	v_mfma_f32_16x16x32_bf16 v[20:23], v[208:211], v[216:219], v[40:43]
	v_mfma_f32_16x16x32_bf16 v[96:99], v[212:215], v[220:223], v[20:23]
	v_mfma_f32_16x16x32_bf16 v[20:23], v[200:203], v[224:227], v[44:47]
	v_mfma_f32_16x16x32_bf16 v[88:91], v[204:207], v[228:231], v[20:23]
	v_mfma_f32_16x16x32_bf16 v[20:23], v[208:211], v[224:227], v[48:51]
	v_mfma_f32_16x16x32_bf16 v[80:83], v[212:215], v[228:231], v[20:23]
	v_mfma_f32_16x16x32_bf16 v[20:23], v[200:203], v[232:235], v[52:55]
	v_mfma_f32_16x16x32_bf16 v[124:127], v[204:207], v[28:31], v[64:67]
	v_mfma_f32_16x16x32_bf16 v[64:67], v[204:207], v[236:239], v[20:23]
	v_mfma_f32_16x16x32_bf16 v[20:23], v[208:211], v[232:235], v[60:63]
	v_mfma_f32_16x16x32_bf16 v[48:51], v[212:215], v[236:239], v[20:23]
	s_barrier
	ds_read_b128 v[32:35], v145 offset:49152
	ds_read_b128 v[40:43], v145 offset:50176
	ds_read_b128 v[216:219], v145 offset:51200
	ds_read_b128 v[220:223], v145 offset:52224
	ds_read_b128 v[224:227], v145 offset:53248
	ds_read_b128 v[228:231], v145 offset:54272
	ds_read_b128 v[232:235], v145 offset:55296
	ds_read_b128 v[236:239], v145 offset:56320
	s_add_i32 m0, s2, 0x18000
	s_nop 0
	global_load_lds_dwordx4 v140, s[38:39]
	s_add_i32 m0, s2, 0x1a000
	s_nop 0
	global_load_lds_dwordx4 v142, s[38:39]
	s_add_u32 s38, s34, 0x80180
	s_addc_u32 s39, s35, 0
	s_add_i32 m0, s2, 0x1c000
	s_nop 0
	global_load_lds_dwordx4 v140, s[38:39]
	s_add_i32 m0, s2, 0x1e000
	s_nop 0
	global_load_lds_dwordx4 v142, s[38:39]
	s_add_i32 m0, s2, 0x8000
	s_nop 0
	global_load_lds_dwordx4 v139, s[36:37]
	s_add_i32 m0, s2, 0xa000
	s_nop 0
	global_load_lds_dwordx4 v141, s[36:37]
	s_waitcnt vmcnt(8) lgkmcnt(0)
	s_barrier
	v_mfma_f32_16x16x32_bf16 v[20:23], v[12:15], v[32:35], v[132:135]
	v_mfma_f32_16x16x32_bf16 v[76:79], v[16:19], v[40:43], v[20:23]
	v_mfma_f32_16x16x32_bf16 v[20:23], v[24:27], v[32:35], v[148:151]
	v_mfma_f32_16x16x32_bf16 v[60:63], v[196:199], v[40:43], v[20:23]
	v_mfma_f32_16x16x32_bf16 v[20:23], v[12:15], v[216:219], v[152:155]
	v_mfma_f32_16x16x32_bf16 v[44:47], v[16:19], v[220:223], v[20:23]
	v_mfma_f32_16x16x32_bf16 v[20:23], v[24:27], v[216:219], v[156:159]
	v_mfma_f32_16x16x32_bf16 v[36:39], v[196:199], v[220:223], v[20:23]
	v_mfma_f32_16x16x32_bf16 v[20:23], v[12:15], v[224:227], v[160:163]
	v_mfma_f32_16x16x32_bf16 v[0:3], v[12:15], v[232:235], v[0:3]
	v_mfma_f32_16x16x32_bf16 v[28:31], v[16:19], v[228:231], v[20:23]
	v_mfma_f32_16x16x32_bf16 v[20:23], v[24:27], v[224:227], v[164:167]
	v_mfma_f32_16x16x32_bf16 v[12:15], v[16:19], v[236:239], v[0:3]
	v_mfma_f32_16x16x32_bf16 v[0:3], v[24:27], v[232:235], v[4:7]
	v_mfma_f32_16x16x32_bf16 v[20:23], v[196:199], v[228:231], v[20:23]
	v_mfma_f32_16x16x32_bf16 v[4:7], v[196:199], v[236:239], v[0:3]
	v_mfma_f32_16x16x32_bf16 v[0:3], v[200:203], v[32:35], v[8:11]
	v_mfma_f32_16x16x32_bf16 v[68:71], v[204:207], v[40:43], v[0:3]
	v_mfma_f32_16x16x32_bf16 v[0:3], v[208:211], v[32:35], v[168:171]
	v_mfma_f32_16x16x32_bf16 v[52:55], v[212:215], v[40:43], v[0:3]
	v_mfma_f32_16x16x32_bf16 v[0:3], v[200:203], v[216:219], v[172:175]
	v_mfma_f32_16x16x32_bf16 v[40:43], v[204:207], v[220:223], v[0:3]
	v_mfma_f32_16x16x32_bf16 v[0:3], v[208:211], v[216:219], v[176:179]
	v_mfma_f32_16x16x32_bf16 v[32:35], v[212:215], v[220:223], v[0:3]
	v_mfma_f32_16x16x32_bf16 v[0:3], v[200:203], v[224:227], v[180:183]
	v_mfma_f32_16x16x32_bf16 v[24:27], v[204:207], v[228:231], v[0:3]
	v_mfma_f32_16x16x32_bf16 v[0:3], v[208:211], v[224:227], v[184:187]
	v_mfma_f32_16x16x32_bf16 v[16:19], v[212:215], v[228:231], v[0:3]
	v_mfma_f32_16x16x32_bf16 v[0:3], v[200:203], v[232:235], v[188:191]
	v_mfma_f32_16x16x32_bf16 v[8:11], v[204:207], v[236:239], v[0:3]
	v_mfma_f32_16x16x32_bf16 v[0:3], v[208:211], v[232:235], v[192:195]
	v_mfma_f32_16x16x32_bf16 v[0:3], v[212:215], v[236:239], v[0:3]
	s_barrier
	s_add_u32 s53, s30, 0x200
	s_addc_u32 s54, s31, 0
	s_add_u32 s55, s34, 0x200
	s_addc_u32 s56, s35, 0
	s_add_u32 s30, s30, 0x80180
	s_addc_u32 s31, s31, 0
	s_mov_b32 s57, 0
.LBB0_1109:
	ds_read_b128 v[132:135], v143
	ds_read_b128 v[148:151], v143 offset:1024
	ds_read_b128 v[152:155], v143 offset:2048
	ds_read_b128 v[156:159], v143 offset:3072
	ds_read_b128 v[160:163], v144
	ds_read_b128 v[164:167], v144 offset:1024
	ds_read_b128 v[168:171], v144 offset:2048
	ds_read_b128 v[172:175], v144 offset:3072
	ds_read_b128 v[176:179], v145
	ds_read_b128 v[180:183], v145 offset:1024
	ds_read_b128 v[184:187], v145 offset:2048
	ds_read_b128 v[188:191], v145 offset:3072
	ds_read_b128 v[192:195], v145 offset:4096
	ds_read_b128 v[196:199], v145 offset:5120
	ds_read_b128 v[200:203], v145 offset:6144
	ds_read_b128 v[204:207], v145 offset:7168
	s_cmp_eq_u32 s57, 28
	s_cselect_b32 s40, s51, s53
	s_cselect_b32 s41, s23, s54
	s_cselect_b32 s36, s52, s55
	s_cselect_b32 s37, s21, s56
	s_add_u32 s34, s40, 0x80
	s_addc_u32 s35, s41, 0
	s_add_u32 s38, s36, 0x80
	s_addc_u32 s39, s37, 0
	s_add_i32 m0, s2, 0xc000
	s_nop 0
	global_load_lds_dwordx4 v139, s[30:31]
	s_add_i32 m0, s2, 0xe000
	s_nop 0
	global_load_lds_dwordx4 v141, s[30:31]
	s_waitcnt vmcnt(8) lgkmcnt(0)
	s_barrier
	v_mfma_f32_16x16x32_bf16 v[116:119], v[132:135], v[176:179], v[116:119]
	v_mfma_f32_16x16x32_bf16 v[112:115], v[152:155], v[176:179], v[112:115]
	v_mfma_f32_16x16x32_bf16 v[100:103], v[152:155], v[184:187], v[100:103]
	v_mfma_f32_16x16x32_bf16 v[108:111], v[132:135], v[184:187], v[108:111]
	v_mfma_f32_16x16x32_bf16 v[92:95], v[132:135], v[192:195], v[92:95]
	v_mfma_f32_16x16x32_bf16 v[84:87], v[152:155], v[192:195], v[84:87]
	v_mfma_f32_16x16x32_bf16 v[56:59], v[152:155], v[200:203], v[56:59]
	v_mfma_f32_16x16x32_bf16 v[72:75], v[132:135], v[200:203], v[72:75]
	v_mfma_f32_16x16x32_bf16 v[116:119], v[148:151], v[180:183], v[116:119]
	v_mfma_f32_16x16x32_bf16 v[112:115], v[156:159], v[180:183], v[112:115]
	v_mfma_f32_16x16x32_bf16 v[100:103], v[156:159], v[188:191], v[100:103]
	v_mfma_f32_16x16x32_bf16 v[108:111], v[148:151], v[188:191], v[108:111]
	v_mfma_f32_16x16x32_bf16 v[92:95], v[148:151], v[196:199], v[92:95]
	v_mfma_f32_16x16x32_bf16 v[84:87], v[156:159], v[196:199], v[84:87]
	v_mfma_f32_16x16x32_bf16 v[56:59], v[156:159], v[204:207], v[56:59]
	v_mfma_f32_16x16x32_bf16 v[72:75], v[148:151], v[204:207], v[72:75]
	v_mfma_f32_16x16x32_bf16 v[124:127], v[160:163], v[176:179], v[124:127]
	v_mfma_f32_16x16x32_bf16 v[120:123], v[168:171], v[176:179], v[120:123]
	v_mfma_f32_16x16x32_bf16 v[96:99], v[168:171], v[184:187], v[96:99]
	v_mfma_f32_16x16x32_bf16 v[104:107], v[160:163], v[184:187], v[104:107]
	v_mfma_f32_16x16x32_bf16 v[88:91], v[160:163], v[192:195], v[88:91]
	v_mfma_f32_16x16x32_bf16 v[80:83], v[168:171], v[192:195], v[80:83]
	v_mfma_f32_16x16x32_bf16 v[48:51], v[168:171], v[200:203], v[48:51]
	v_mfma_f32_16x16x32_bf16 v[64:67], v[160:163], v[200:203], v[64:67]
	v_mfma_f32_16x16x32_bf16 v[124:127], v[164:167], v[180:183], v[124:127]
	v_mfma_f32_16x16x32_bf16 v[120:123], v[172:175], v[180:183], v[120:123]
	v_mfma_f32_16x16x32_bf16 v[96:99], v[172:175], v[188:191], v[96:99]
	v_mfma_f32_16x16x32_bf16 v[104:107], v[164:167], v[188:191], v[104:107]
	v_mfma_f32_16x16x32_bf16 v[88:91], v[164:167], v[196:199], v[88:91]
	v_mfma_f32_16x16x32_bf16 v[80:83], v[172:175], v[196:199], v[80:83]
	v_mfma_f32_16x16x32_bf16 v[48:51], v[172:175], v[204:207], v[48:51]
	v_mfma_f32_16x16x32_bf16 v[64:67], v[164:167], v[204:207], v[64:67]
	s_barrier
	ds_read_b128 v[176:179], v145 offset:16384
	ds_read_b128 v[180:183], v145 offset:17408
	ds_read_b128 v[184:187], v145 offset:18432
	ds_read_b128 v[188:191], v145 offset:19456
	ds_read_b128 v[192:195], v145 offset:20480
	ds_read_b128 v[196:199], v145 offset:21504
	ds_read_b128 v[200:203], v145 offset:22528
	ds_read_b128 v[204:207], v145 offset:23552
	s_add_i32 m0, s2, 0x10000
	s_nop 0
	global_load_lds_dwordx4 v140, s[36:37]
	s_add_i32 m0, s2, 0x12000
	s_nop 0
	global_load_lds_dwordx4 v142, s[36:37]
	s_add_u32 s58, s36, 0x80000
	s_addc_u32 s59, s37, 0
	s_add_i32 m0, s2, 0x14000
	s_nop 0
	global_load_lds_dwordx4 v140, s[58:59]
	s_add_i32 m0, s2, 0x16000
	s_nop 0
	global_load_lds_dwordx4 v142, s[58:59]
	s_add_i32 m0, s2, 0
	s_nop 0
	global_load_lds_dwordx4 v139, s[40:41]
	s_add_i32 m0, s2, 0x2000
	s_nop 0
	global_load_lds_dwordx4 v141, s[40:41]
	s_waitcnt vmcnt(8) lgkmcnt(0)
	s_barrier
	v_mfma_f32_16x16x32_bf16 v[76:79], v[132:135], v[176:179], v[76:79]
	v_mfma_f32_16x16x32_bf16 v[60:63], v[152:155], v[176:179], v[60:63]
	v_mfma_f32_16x16x32_bf16 v[36:39], v[152:155], v[184:187], v[36:39]
	v_mfma_f32_16x16x32_bf16 v[44:47], v[132:135], v[184:187], v[44:47]
	v_mfma_f32_16x16x32_bf16 v[28:31], v[132:135], v[192:195], v[28:31]
	v_mfma_f32_16x16x32_bf16 v[20:23], v[152:155], v[192:195], v[20:23]
	v_mfma_f32_16x16x32_bf16 v[4:7], v[152:155], v[200:203], v[4:7]
	v_mfma_f32_16x16x32_bf16 v[12:15], v[132:135], v[200:203], v[12:15]
	v_mfma_f32_16x16x32_bf16 v[76:79], v[148:151], v[180:183], v[76:79]
	v_mfma_f32_16x16x32_bf16 v[60:63], v[156:159], v[180:183], v[60:63]
	v_mfma_f32_16x16x32_bf16 v[36:39], v[156:159], v[188:191], v[36:39]
	v_mfma_f32_16x16x32_bf16 v[44:47], v[148:151], v[188:191], v[44:47]
	v_mfma_f32_16x16x32_bf16 v[28:31], v[148:151], v[196:199], v[28:31]
	v_mfma_f32_16x16x32_bf16 v[20:23], v[156:159], v[196:199], v[20:23]
	v_mfma_f32_16x16x32_bf16 v[4:7], v[156:159], v[204:207], v[4:7]
	v_mfma_f32_16x16x32_bf16 v[12:15], v[148:151], v[204:207], v[12:15]
	v_mfma_f32_16x16x32_bf16 v[68:71], v[160:163], v[176:179], v[68:71]
	v_mfma_f32_16x16x32_bf16 v[52:55], v[168:171], v[176:179], v[52:55]
	v_mfma_f32_16x16x32_bf16 v[32:35], v[168:171], v[184:187], v[32:35]
	v_mfma_f32_16x16x32_bf16 v[40:43], v[160:163], v[184:187], v[40:43]
	v_mfma_f32_16x16x32_bf16 v[24:27], v[160:163], v[192:195], v[24:27]
	v_mfma_f32_16x16x32_bf16 v[16:19], v[168:171], v[192:195], v[16:19]
	v_mfma_f32_16x16x32_bf16 v[0:3], v[168:171], v[200:203], v[0:3]
	v_mfma_f32_16x16x32_bf16 v[8:11], v[160:163], v[200:203], v[8:11]
	v_mfma_f32_16x16x32_bf16 v[68:71], v[164:167], v[180:183], v[68:71]
	v_mfma_f32_16x16x32_bf16 v[52:55], v[172:175], v[180:183], v[52:55]
	v_mfma_f32_16x16x32_bf16 v[32:35], v[172:175], v[188:191], v[32:35]
	v_mfma_f32_16x16x32_bf16 v[40:43], v[164:167], v[188:191], v[40:43]
	v_mfma_f32_16x16x32_bf16 v[24:27], v[164:167], v[196:199], v[24:27]
	v_mfma_f32_16x16x32_bf16 v[16:19], v[172:175], v[196:199], v[16:19]
	v_mfma_f32_16x16x32_bf16 v[0:3], v[172:175], v[204:207], v[0:3]
	v_mfma_f32_16x16x32_bf16 v[8:11], v[164:167], v[204:207], v[8:11]
	s_barrier
	ds_read_b128 v[132:135], v146
	ds_read_b128 v[148:151], v146 offset:1024
	ds_read_b128 v[152:155], v146 offset:2048
	ds_read_b128 v[156:159], v146 offset:3072
	ds_read_b128 v[160:163], v147
	ds_read_b128 v[164:167], v147 offset:1024
	ds_read_b128 v[168:171], v147 offset:2048
	ds_read_b128 v[172:175], v147 offset:3072
	ds_read_b128 v[176:179], v145 offset:32768
	ds_read_b128 v[180:183], v145 offset:33792
	ds_read_b128 v[184:187], v145 offset:34816
	ds_read_b128 v[188:191], v145 offset:35840
	ds_read_b128 v[192:195], v145 offset:36864
	ds_read_b128 v[196:199], v145 offset:37888
	ds_read_b128 v[200:203], v145 offset:38912
	ds_read_b128 v[204:207], v145 offset:39936
	s_add_u32 s40, s40, 0x80000
	s_addc_u32 s41, s41, 0
	s_add_i32 m0, s2, 0x4000
	s_nop 0
	global_load_lds_dwordx4 v139, s[40:41]
	s_add_i32 m0, s2, 0x6000
	s_nop 0
	global_load_lds_dwordx4 v141, s[40:41]
	s_waitcnt vmcnt(8) lgkmcnt(0)
	s_barrier
	v_mfma_f32_16x16x32_bf16 v[116:119], v[132:135], v[176:179], v[116:119]
	v_mfma_f32_16x16x32_bf16 v[112:115], v[152:155], v[176:179], v[112:115]
	v_mfma_f32_16x16x32_bf16 v[100:103], v[152:155], v[184:187], v[100:103]
	v_mfma_f32_16x16x32_bf16 v[108:111], v[132:135], v[184:187], v[108:111]
	v_mfma_f32_16x16x32_bf16 v[92:95], v[132:135], v[192:195], v[92:95]
	v_mfma_f32_16x16x32_bf16 v[84:87], v[152:155], v[192:195], v[84:87]
	v_mfma_f32_16x16x32_bf16 v[56:59], v[152:155], v[200:203], v[56:59]
	v_mfma_f32_16x16x32_bf16 v[72:75], v[132:135], v[200:203], v[72:75]
	v_mfma_f32_16x16x32_bf16 v[116:119], v[148:151], v[180:183], v[116:119]
	v_mfma_f32_16x16x32_bf16 v[112:115], v[156:159], v[180:183], v[112:115]
	v_mfma_f32_16x16x32_bf16 v[100:103], v[156:159], v[188:191], v[100:103]
	v_mfma_f32_16x16x32_bf16 v[108:111], v[148:151], v[188:191], v[108:111]
	v_mfma_f32_16x16x32_bf16 v[92:95], v[148:151], v[196:199], v[92:95]
	v_mfma_f32_16x16x32_bf16 v[84:87], v[156:159], v[196:199], v[84:87]
	v_mfma_f32_16x16x32_bf16 v[56:59], v[156:159], v[204:207], v[56:59]
	v_mfma_f32_16x16x32_bf16 v[72:75], v[148:151], v[204:207], v[72:75]
	v_mfma_f32_16x16x32_bf16 v[124:127], v[160:163], v[176:179], v[124:127]
	v_mfma_f32_16x16x32_bf16 v[120:123], v[168:171], v[176:179], v[120:123]
	v_mfma_f32_16x16x32_bf16 v[96:99], v[168:171], v[184:187], v[96:99]
	v_mfma_f32_16x16x32_bf16 v[104:107], v[160:163], v[184:187], v[104:107]
	v_mfma_f32_16x16x32_bf16 v[88:91], v[160:163], v[192:195], v[88:91]
	v_mfma_f32_16x16x32_bf16 v[80:83], v[168:171], v[192:195], v[80:83]
	v_mfma_f32_16x16x32_bf16 v[48:51], v[168:171], v[200:203], v[48:51]
	v_mfma_f32_16x16x32_bf16 v[64:67], v[160:163], v[200:203], v[64:67]
	v_mfma_f32_16x16x32_bf16 v[124:127], v[164:167], v[180:183], v[124:127]
	v_mfma_f32_16x16x32_bf16 v[120:123], v[172:175], v[180:183], v[120:123]
	v_mfma_f32_16x16x32_bf16 v[96:99], v[172:175], v[188:191], v[96:99]
	v_mfma_f32_16x16x32_bf16 v[104:107], v[164:167], v[188:191], v[104:107]
	v_mfma_f32_16x16x32_bf16 v[88:91], v[164:167], v[196:199], v[88:91]
	v_mfma_f32_16x16x32_bf16 v[80:83], v[172:175], v[196:199], v[80:83]
	v_mfma_f32_16x16x32_bf16 v[48:51], v[172:175], v[204:207], v[48:51]
	v_mfma_f32_16x16x32_bf16 v[64:67], v[164:167], v[204:207], v[64:67]
	s_barrier
	ds_read_b128 v[176:179], v145 offset:49152
	ds_read_b128 v[180:183], v145 offset:50176
	ds_read_b128 v[184:187], v145 offset:51200
	ds_read_b128 v[188:191], v145 offset:52224
	ds_read_b128 v[192:195], v145 offset:53248
	ds_read_b128 v[196:199], v145 offset:54272
	ds_read_b128 v[200:203], v145 offset:55296
	ds_read_b128 v[204:207], v145 offset:56320
	s_add_i32 m0, s2, 0x18000
	s_nop 0
	global_load_lds_dwordx4 v140, s[38:39]
	s_add_i32 m0, s2, 0x1a000
	s_nop 0
	global_load_lds_dwordx4 v142, s[38:39]
	s_add_u32 s36, s36, 0x80080
	s_addc_u32 s37, s37, 0
	s_add_i32 m0, s2, 0x1c000
	s_nop 0
	global_load_lds_dwordx4 v140, s[36:37]
	s_add_i32 m0, s2, 0x1e000
	s_nop 0
	global_load_lds_dwordx4 v142, s[36:37]
	s_add_i32 m0, s2, 0x8000
	s_nop 0
	global_load_lds_dwordx4 v139, s[34:35]
	s_add_i32 m0, s2, 0xa000
	s_nop 0
	global_load_lds_dwordx4 v141, s[34:35]
	s_waitcnt vmcnt(8) lgkmcnt(0)
	s_barrier
	v_mfma_f32_16x16x32_bf16 v[76:79], v[132:135], v[176:179], v[76:79]
	v_mfma_f32_16x16x32_bf16 v[60:63], v[152:155], v[176:179], v[60:63]
	v_mfma_f32_16x16x32_bf16 v[36:39], v[152:155], v[184:187], v[36:39]
	v_mfma_f32_16x16x32_bf16 v[44:47], v[132:135], v[184:187], v[44:47]
	v_mfma_f32_16x16x32_bf16 v[28:31], v[132:135], v[192:195], v[28:31]
	v_mfma_f32_16x16x32_bf16 v[20:23], v[152:155], v[192:195], v[20:23]
	v_mfma_f32_16x16x32_bf16 v[4:7], v[152:155], v[200:203], v[4:7]
	v_mfma_f32_16x16x32_bf16 v[12:15], v[132:135], v[200:203], v[12:15]
	v_mfma_f32_16x16x32_bf16 v[76:79], v[148:151], v[180:183], v[76:79]
	v_mfma_f32_16x16x32_bf16 v[60:63], v[156:159], v[180:183], v[60:63]
	v_mfma_f32_16x16x32_bf16 v[36:39], v[156:159], v[188:191], v[36:39]
	v_mfma_f32_16x16x32_bf16 v[44:47], v[148:151], v[188:191], v[44:47]
	v_mfma_f32_16x16x32_bf16 v[28:31], v[148:151], v[196:199], v[28:31]
	v_mfma_f32_16x16x32_bf16 v[20:23], v[156:159], v[196:199], v[20:23]
	v_mfma_f32_16x16x32_bf16 v[4:7], v[156:159], v[204:207], v[4:7]
	v_mfma_f32_16x16x32_bf16 v[12:15], v[148:151], v[204:207], v[12:15]
	v_mfma_f32_16x16x32_bf16 v[68:71], v[160:163], v[176:179], v[68:71]
	v_mfma_f32_16x16x32_bf16 v[52:55], v[168:171], v[176:179], v[52:55]
	v_mfma_f32_16x16x32_bf16 v[32:35], v[168:171], v[184:187], v[32:35]
	v_mfma_f32_16x16x32_bf16 v[40:43], v[160:163], v[184:187], v[40:43]
	v_mfma_f32_16x16x32_bf16 v[24:27], v[160:163], v[192:195], v[24:27]
	v_mfma_f32_16x16x32_bf16 v[16:19], v[168:171], v[192:195], v[16:19]
	v_mfma_f32_16x16x32_bf16 v[0:3], v[168:171], v[200:203], v[0:3]
	v_mfma_f32_16x16x32_bf16 v[8:11], v[160:163], v[200:203], v[8:11]
	v_mfma_f32_16x16x32_bf16 v[68:71], v[164:167], v[180:183], v[68:71]
	v_mfma_f32_16x16x32_bf16 v[52:55], v[172:175], v[180:183], v[52:55]
	v_mfma_f32_16x16x32_bf16 v[32:35], v[172:175], v[188:191], v[32:35]
	v_mfma_f32_16x16x32_bf16 v[40:43], v[164:167], v[188:191], v[40:43]
	v_mfma_f32_16x16x32_bf16 v[24:27], v[164:167], v[196:199], v[24:27]
	v_mfma_f32_16x16x32_bf16 v[16:19], v[172:175], v[196:199], v[16:19]
	v_mfma_f32_16x16x32_bf16 v[0:3], v[172:175], v[204:207], v[0:3]
	v_mfma_f32_16x16x32_bf16 v[8:11], v[164:167], v[204:207], v[8:11]
	s_barrier
	s_add_i32 s57, s57, 2
	s_add_u32 s53, s53, 0x100
	s_addc_u32 s54, s54, 0
	s_add_u32 s55, s55, 0x100
	s_addc_u32 s56, s56, 0
	s_add_u32 s30, s30, 0x100
	s_addc_u32 s31, s31, 0
	s_cmp_gt_u32 s57, 29
	s_cbranch_scc0 .LBB0_1109
	s_and_b64 vcc, exec, s[10:11]
	s_cbranch_vccz .LBB0_1112
	s_barrier

.LBB0_1397:
	s_cmp_lt_i32 s92, 12
	s_cselect_b64 s[4:5], -1, 0
	s_cmp_gt_i32 s93, 11
	s_cselect_b64 s[6:7], -1, 0
	s_and_b64 s[4:5], s[4:5], s[6:7]
	s_andn2_b64 vcc, exec, s[4:5]
	s_cbranch_vccnz .LBB0_1472
	s_waitcnt vmcnt(0)
	v_mov_b32_e32 v0, 0x3ce000
	s_waitcnt lgkmcnt(0)
	global_load_dword v1, v0, s[70:71] offset:1280
	v_mbcnt_lo_u32_b32 v0, -1, 0
	s_and_b32 s2, s3, 0xffffffc0
	v_mbcnt_hi_u32_b32 v254, -1, v0
	v_add_u32_e32 v0, s2, v254
	s_waitcnt vmcnt(0)
	v_readfirstlane_b32 s38, v1
	v_readfirstlane_b32 s2, v0
	s_mul_i32 s4, s38, 56
	s_ashr_i32 s6, s2, 6
	s_cmp_ge_i32 s87, s4
	s_cbranch_scc1 .LBB0_1418
	s_add_u32 s39, s70, 0x3a800000
	s_addc_u32 s40, s71, 0
	s_add_u32 s41, s70, 0x8800000
	s_addc_u32 s42, s71, 0
	s_add_u32 s43, s70, 0x3ce000
	s_addc_u32 s44, s71, 0
	s_lshl_b32 s5, s6, 10
	s_ashr_i32 s48, s87, 31
	s_add_i32 s47, s5, 0
	s_lshr_b32 s5, s48, 29
	s_add_i32 s5, s87, s5
	s_mul_i32 s45, s38, 7
	s_ashr_i32 s8, s5, 3
	s_and_b32 s5, s5, -8
	s_add_i32 s46, s45, 1
	s_ashr_i32 s7, s2, 8
	s_sub_i32 s5, s87, s5
	s_cmp_lt_i32 s5, 0
	s_cselect_b32 s9, s46, s45
	s_mul_i32 s5, s9, s5
	s_add_i32 s5, s5, s8
	s_mul_hi_i32 s8, s5, 0x92492493
	s_add_i32 s8, s8, s5
	s_lshr_b32 s9, s8, 31
	s_ashr_i32 s8, s8, 8
	s_add_i32 s8, s8, s9
	s_lshl_b32 s9, s8, 3
	s_sub_i32 s10, s38, s9
	s_min_i32 s10, s10, 8
	s_abs_i32 s11, s10
	v_cvt_f32_u32_e32 v1, s11
	s_sub_i32 s13, 0, s11
	s_mulk_i32 s8, 0x1c0
	s_sub_i32 s5, s5, s8
	v_rcp_iflag_f32_e32 v1, v1
	s_abs_i32 s12, s5
	s_xor_b32 s8, s5, s10
	s_ashr_i32 s8, s8, 31
	v_mul_f32_e32 v1, 0x4f7ffffe, v1
	v_cvt_u32_f32_e32 v1, v1
	v_lshlrev_b32_e32 v2, 4, v0
	v_bfe_i32 v4, v0, 27, 1
	v_lshrrev_b32_e32 v4, 22, v4
	v_readfirstlane_b32 s14, v1
	s_mul_i32 s13, s13, s14
	s_mul_hi_u32 s13, s14, s13
	s_add_i32 s14, s14, s13
	s_mul_hi_u32 s13, s12, s14
	s_mul_i32 s14, s13, s11
	s_sub_i32 s12, s12, s14
	s_add_i32 s14, s13, 1
	s_sub_i32 s15, s12, s11
	s_cmp_ge_u32 s12, s11
	s_cselect_b32 s13, s14, s13
	s_cselect_b32 s12, s15, s12
	s_add_i32 s14, s13, 1
	s_cmp_ge_u32 s12, s11
	s_cselect_b32 s11, s14, s13
	s_xor_b32 s11, s11, s8
	s_sub_i32 s22, s11, s8
	s_mul_i32 s8, s22, s10
	s_sub_i32 s5, s5, s8
	s_add_i32 s24, s9, s5
	s_ashr_i32 s25, s24, 31
	s_lshl_b64 s[8:9], s[24:25], 2
	s_add_u32 s8, s43, s8
	s_addc_u32 s9, s44, s9
	v_mov_b32_e32 v1, 0
	global_load_dword v1, v1, s[8:9]
	v_add_u32_e32 v6, 0x2000, v2
	v_add_u32_e32 v4, v2, v4
	v_ashrrev_i32_e32 v7, 31, v6
	v_and_b32_e32 v4, 0xfffffc00, v4
	v_lshrrev_b32_e32 v7, 22, v7
	v_sub_u32_e32 v2, v2, v4
	v_add_u32_e32 v7, v6, v7
	v_ashrrev_i32_e32 v3, 31, v0
	v_lshrrev_b32_e32 v8, 4, v2
	v_ashrrev_i32_e32 v7, 10, v7
	v_lshrrev_b32_e32 v3, 26, v3
	v_bitop3_b32 v2, v8, v2, 32 bitop3:0x6c
	v_mul_i32_i24_e32 v8, 0x400, v7
	v_add_u32_e32 v3, v0, v3
	v_lshlrev_b32_e32 v9, 3, v7
	v_ashrrev_i32_e32 v10, 31, v2
	v_sub_u32_e32 v6, v6, v8
	v_ashrrev_i32_e32 v3, 6, v3
	v_and_b32_e32 v8, -16, v9
	v_lshrrev_b32_e32 v9, 26, v10
	v_lshrrev_b32_e32 v10, 4, v6
	v_lshlrev_b32_e32 v4, 3, v3
	v_add_u32_e32 v9, v2, v9
	v_bitop3_b32 v6, v10, v6, 32 bitop3:0x6c
	v_and_b32_e32 v4, -16, v4
	v_ashrrev_i32_e32 v10, 6, v9
	v_and_b32_e32 v9, 0xc0, v9
	v_ashrrev_i32_e32 v11, 31, v6
	v_mov_b32_e32 v5, 1
	v_add_u32_e32 v4, v10, v4
	v_sub_u32_e32 v2, v2, v9
	v_and_b32_e32 v9, 3, v10
	v_lshrrev_b32_e32 v10, 26, v11
	s_mov_b32 s5, 0x1fffe0
	v_lshlrev_b32_e32 v3, 5, v3
	v_ashrrev_i16_sdwa v2, v5, sext(v2) dst_sel:DWORD dst_unused:UNUSED_PAD src0_sel:DWORD src1_sel:BYTE_0
	v_lshlrev_b32_e32 v11, 1, v4
	v_lshrrev_b32_e32 v12, 2, v4
	v_add_u32_e32 v10, v6, v10
	v_and_b32_e32 v3, 32, v3
	v_and_or_b32 v9, v4, s5, v9
	v_bfe_i32 v2, v2, 0, 16
	v_and_b32_e32 v11, 24, v11
	v_and_b32_e32 v12, 4, v12
	v_ashrrev_i32_e32 v13, 6, v10
	v_and_b32_e32 v10, 0xc0, v10
	v_or3_b32 v9, v9, v12, v11
	v_add_lshl_u32 v2, v3, v2, 1
	v_add_u32_e32 v3, v13, v8
	v_sub_u32_e32 v6, v6, v10
	v_and_b32_e32 v8, 3, v13
	s_lshl_b64 s[8:9], s[24:25], 19
	v_lshl_add_u32 v134, v4, 11, v2
	v_lshl_add_u32 v135, v9, 11, v2
	v_ashrrev_i16_sdwa v2, v5, sext(v6) dst_sel:DWORD dst_unused:UNUSED_PAD src0_sel:DWORD src1_sel:BYTE_0
	v_and_or_b32 v6, v3, s5, v8
	s_add_u32 s28, s39, s8
	s_addc_u32 s29, s40, s9
	v_lshlrev_b32_e32 v7, 5, v7
	v_lshlrev_b32_e32 v4, 1, v3
	v_lshrrev_b32_e32 v5, 2, v3
	v_and_b32_e32 v7, 32, v7
	v_bfe_i32 v2, v2, 0, 16
	v_and_b32_e32 v4, 24, v4
	v_and_b32_e32 v5, 4, v5
	v_or3_b32 v4, v6, v5, v4
	v_add_lshl_u32 v2, v7, v2, 1
	v_lshl_add_u32 v137, v4, 11, v2
	v_lshl_add_u32 v136, v3, 11, v2
	s_waitcnt vmcnt(0)
	v_readfirstlane_b32 s5, v1
	s_mul_hi_i32 s10, s5, 0x1c00000
	s_mul_i32 s5, s5, 0x1c00000
	s_add_u32 s5, s41, s5
	s_addc_u32 s10, s42, s10
	s_ashr_i32 s23, s22, 31
	s_lshl_b64 s[8:9], s[22:23], 19
	s_add_u32 s26, s5, s8
	s_addc_u32 s27, s10, s9
	s_add_i32 m0, s47, 0x10000
	s_nop 0
	global_load_lds_dwordx4 v135, s[26:27]
	s_add_i32 m0, s47, 0x12000
	s_nop 0
	global_load_lds_dwordx4 v137, s[26:27]
	s_add_u32 s8, s26, 0x40000
	s_addc_u32 s9, s27, 0
	s_add_i32 m0, s47, 0x14000
	s_nop 0
	global_load_lds_dwordx4 v135, s[8:9]
	s_add_i32 m0, s47, 0x16000
	s_nop 0
	global_load_lds_dwordx4 v137, s[8:9]
	s_add_i32 m0, s47, 0
	s_nop 0
	global_load_lds_dwordx4 v134, s[28:29]
	s_add_i32 m0, s47, 0x2000
	s_nop 0
	global_load_lds_dwordx4 v136, s[28:29]
	s_add_u32 s8, s28, 0x40000
	s_addc_u32 s9, s29, 0
	s_add_i32 m0, s47, 0x4000
	s_nop 0
	global_load_lds_dwordx4 v134, s[8:9]
	s_add_i32 m0, s47, 0x6000
	s_nop 0
	global_load_lds_dwordx4 v136, s[8:9]
	s_cmp_eq_u32 s7, 1
	s_cselect_b64 s[8:9], -1, 0
	s_cmp_lg_u32 s7, 1
	s_cbranch_scc1 .LBB0_1401
	s_barrier

.LBB0_1410:
	ds_read_b128 v[0:3], v138
	ds_read_b128 v[4:7], v138 offset:1024
	ds_read_b128 v[8:11], v138 offset:2048
	ds_read_b128 v[12:15], v138 offset:3072
	ds_read_b128 v[16:19], v139
	ds_read_b128 v[20:23], v139 offset:1024
	ds_read_b128 v[24:27], v139 offset:2048
	ds_read_b128 v[28:31], v139 offset:3072
	ds_read_b128 v[32:35], v140
	ds_read_b128 v[36:39], v140 offset:1024
	ds_read_b128 v[40:43], v140 offset:2048
	ds_read_b128 v[44:47], v140 offset:3072
	ds_read_b128 v[48:51], v140 offset:4096
	ds_read_b128 v[52:55], v140 offset:5120
	ds_read_b128 v[56:59], v140 offset:6144
	ds_read_b128 v[60:63], v140 offset:7168
	s_lshl_b64 s[20:21], s[16:17], 19
	s_add_u32 s20, s39, s20
	s_addc_u32 s21, s40, s21
	s_and_b64 s[6:7], exec, s[6:7]
	s_cselect_b32 s2, s21, s29
	s_cselect_b32 s15, s20, s28
	s_add_u32 s6, s28, 0x100
	s_addc_u32 s7, s29, 0
	s_add_u32 s36, s26, 0x100
	s_addc_u32 s37, s27, 0
	s_add_u32 s30, s28, 0x180
	s_addc_u32 s31, s29, 0
	s_add_u32 s34, s26, 0x180
	s_addc_u32 s35, s27, 0
	s_add_u32 s54, s28, 0x40080
	s_addc_u32 s55, s29, 0
	s_add_i32 m0, s47, 0xc000
	s_nop 0
	global_load_lds_dwordx4 v134, s[54:55]
	s_add_i32 m0, s47, 0xe000
	s_nop 0
	global_load_lds_dwordx4 v136, s[54:55]
	s_waitcnt vmcnt(8) lgkmcnt(0)
	s_barrier
	v_mfma_f32_16x16x128_f8f6f4 v[64:67], v[0:7], v[32:39], 0
	v_mfma_f32_16x16x128_f8f6f4 v[68:71], v[8:15], v[32:39], 0
	v_mfma_f32_16x16x128_f8f6f4 v[76:79], v[8:15], v[40:47], 0
	v_mfma_f32_16x16x128_f8f6f4 v[72:75], v[0:7], v[40:47], 0
	v_mfma_f32_16x16x128_f8f6f4 v[80:83], v[0:7], v[48:55], 0
	v_mfma_f32_16x16x128_f8f6f4 v[88:91], v[8:15], v[48:55], 0
	v_mfma_f32_16x16x128_f8f6f4 v[104:107], v[8:15], v[56:63], 0
	v_mfma_f32_16x16x128_f8f6f4 v[92:95], v[0:7], v[56:63], 0
	v_mfma_f32_16x16x128_f8f6f4 v[108:111], v[16:23], v[32:39], 0
	v_mfma_f32_16x16x128_f8f6f4 v[124:127], v[24:31], v[32:39], 0
	v_mfma_f32_16x16x128_f8f6f4 v[166:169], v[24:31], v[40:47], 0
	v_mfma_f32_16x16x128_f8f6f4 v[162:165], v[16:23], v[40:47], 0
	v_mfma_f32_16x16x128_f8f6f4 v[170:173], v[16:23], v[48:55], 0
	v_mfma_f32_16x16x128_f8f6f4 v[174:177], v[24:31], v[48:55], 0
	v_mfma_f32_16x16x128_f8f6f4 v[182:185], v[24:31], v[56:63], 0
	v_mfma_f32_16x16x128_f8f6f4 v[178:181], v[16:23], v[56:63], 0
	s_barrier
	ds_read_b128 v[32:35], v140 offset:16384
	ds_read_b128 v[36:39], v140 offset:17408
	ds_read_b128 v[40:43], v140 offset:18432
	ds_read_b128 v[44:47], v140 offset:19456
	ds_read_b128 v[48:51], v140 offset:20480
	ds_read_b128 v[52:55], v140 offset:21504
	ds_read_b128 v[56:59], v140 offset:22528
	ds_read_b128 v[60:63], v140 offset:23552
	s_add_i32 m0, s47, 0x10000
	s_nop 0
	global_load_lds_dwordx4 v135, s[36:37]
	s_add_i32 m0, s47, 0x12000
	s_nop 0
	global_load_lds_dwordx4 v137, s[36:37]
	s_add_u32 s36, s26, 0x40100
	s_addc_u32 s37, s27, 0
	s_add_i32 m0, s47, 0x14000
	s_nop 0
	global_load_lds_dwordx4 v135, s[36:37]
	s_add_i32 m0, s47, 0x16000
	s_nop 0
	global_load_lds_dwordx4 v137, s[36:37]
	s_add_i32 m0, s47, 0
	s_nop 0
	global_load_lds_dwordx4 v134, s[6:7]
	s_add_i32 m0, s47, 0x2000
	s_nop 0
	global_load_lds_dwordx4 v136, s[6:7]
	s_waitcnt vmcnt(8) lgkmcnt(0)
	s_barrier
	v_mfma_f32_16x16x128_f8f6f4 v[186:189], v[0:7], v[32:39], 0
	v_mfma_f32_16x16x128_f8f6f4 v[190:193], v[8:15], v[32:39], 0
	v_mfma_f32_16x16x128_f8f6f4 v[198:201], v[8:15], v[40:47], 0
	v_mfma_f32_16x16x128_f8f6f4 v[194:197], v[0:7], v[40:47], 0
	v_mfma_f32_16x16x128_f8f6f4 v[202:205], v[0:7], v[48:55], 0
	v_mfma_f32_16x16x128_f8f6f4 v[206:209], v[8:15], v[48:55], 0
	v_mfma_f32_16x16x128_f8f6f4 v[214:217], v[8:15], v[56:63], 0
	v_mfma_f32_16x16x128_f8f6f4 v[210:213], v[0:7], v[56:63], 0
	v_mfma_f32_16x16x128_f8f6f4 v[218:221], v[16:23], v[32:39], 0
	v_mfma_f32_16x16x128_f8f6f4 v[222:225], v[24:31], v[32:39], 0
	v_mfma_f32_16x16x128_f8f6f4 v[230:233], v[24:31], v[40:47], 0
	v_mfma_f32_16x16x128_f8f6f4 v[226:229], v[16:23], v[40:47], 0
	v_mfma_f32_16x16x128_f8f6f4 v[234:237], v[16:23], v[48:55], 0
	v_mfma_f32_16x16x128_f8f6f4 v[238:241], v[24:31], v[48:55], 0
	v_mfma_f32_16x16x128_f8f6f4 v[246:249], v[24:31], v[56:63], 0
	v_mfma_f32_16x16x128_f8f6f4 v[242:245], v[16:23], v[56:63], 0
	s_barrier
	ds_read_b128 v[0:3], v141
	ds_read_b128 v[4:7], v141 offset:1024
	ds_read_b128 v[8:11], v141 offset:2048
	ds_read_b128 v[12:15], v141 offset:3072
	ds_read_b128 v[146:149], v142
	ds_read_b128 v[150:153], v142 offset:1024
	ds_read_b128 v[154:157], v142 offset:2048
	ds_read_b128 v[158:161], v142 offset:3072
	ds_read_b128 v[16:19], v140 offset:32768
	ds_read_b128 v[20:23], v140 offset:33792
	ds_read_b128 v[24:27], v140 offset:34816
	ds_read_b128 v[28:31], v140 offset:35840
	ds_read_b128 v[32:35], v140 offset:36864
	ds_read_b128 v[36:39], v140 offset:37888
	ds_read_b128 v[40:43], v140 offset:38912
	ds_read_b128 v[44:47], v140 offset:39936
	s_add_u32 s28, s28, 0x40100
	s_addc_u32 s29, s29, 0
	s_add_i32 m0, s47, 0x4000
	s_nop 0
	global_load_lds_dwordx4 v134, s[28:29]
	s_add_i32 m0, s47, 0x6000
	s_nop 0
	global_load_lds_dwordx4 v136, s[28:29]
	s_waitcnt vmcnt(8) lgkmcnt(0)
	s_barrier
	v_mfma_f32_16x16x128_f8f6f4 v[112:115], v[0:7], v[16:23], v[64:67]
	v_mfma_f32_16x16x128_f8f6f4 v[116:119], v[8:15], v[16:23], v[68:71]
	v_mfma_f32_16x16x128_f8f6f4 v[100:103], v[0:7], v[24:31], v[72:75]
	v_mfma_f32_16x16x128_f8f6f4 v[96:99], v[8:15], v[24:31], v[76:79]
	v_mfma_f32_16x16x128_f8f6f4 v[84:87], v[0:7], v[32:39], v[80:83]
	v_mfma_f32_16x16x128_f8f6f4 v[80:83], v[8:15], v[32:39], v[88:91]
	v_mfma_f32_16x16x128_f8f6f4 v[60:63], v[0:7], v[40:47], v[92:95]
	v_mfma_f32_16x16x128_f8f6f4 v[56:59], v[8:15], v[40:47], v[104:107]
	v_mfma_f32_16x16x128_f8f6f4 v[120:123], v[146:153], v[16:23], v[108:111]
	v_mfma_f32_16x16x128_f8f6f4 v[124:127], v[154:161], v[16:23], v[124:127]
	v_mfma_f32_16x16x128_f8f6f4 v[108:111], v[146:153], v[24:31], v[162:165]
	v_mfma_f32_16x16x128_f8f6f4 v[104:107], v[154:161], v[24:31], v[166:169]
	v_mfma_f32_16x16x128_f8f6f4 v[92:95], v[146:153], v[32:39], v[170:173]
	v_mfma_f32_16x16x128_f8f6f4 v[88:91], v[154:161], v[32:39], v[174:177]
	v_mfma_f32_16x16x128_f8f6f4 v[76:79], v[146:153], v[40:47], v[178:181]
	v_mfma_f32_16x16x128_f8f6f4 v[72:75], v[154:161], v[40:47], v[182:185]
	s_barrier
	ds_read_b128 v[24:27], v140 offset:49152
	ds_read_b128 v[28:31], v140 offset:50176
	ds_read_b128 v[162:165], v140 offset:51200
	ds_read_b128 v[166:169], v140 offset:52224
	ds_read_b128 v[170:173], v140 offset:53248
	ds_read_b128 v[174:177], v140 offset:54272
	ds_read_b128 v[178:181], v140 offset:55296
	ds_read_b128 v[182:185], v140 offset:56320
	s_add_i32 m0, s47, 0x18000
	s_nop 0
	global_load_lds_dwordx4 v135, s[34:35]
	s_add_i32 m0, s47, 0x1a000
	s_nop 0
	global_load_lds_dwordx4 v137, s[34:35]
	s_add_u32 s28, s26, 0x40180
	s_addc_u32 s29, s27, 0
	s_add_i32 m0, s47, 0x1c000
	s_nop 0
	global_load_lds_dwordx4 v135, s[28:29]
	s_add_i32 m0, s47, 0x1e000
	s_nop 0
	global_load_lds_dwordx4 v137, s[28:29]
	s_add_i32 m0, s47, 0x8000
	s_nop 0
	global_load_lds_dwordx4 v134, s[30:31]
	s_add_i32 m0, s47, 0xa000
	s_nop 0
	global_load_lds_dwordx4 v136, s[30:31]
	s_waitcnt vmcnt(8) lgkmcnt(0)
	s_barrier
	v_mfma_f32_16x16x128_f8f6f4 v[52:55], v[0:7], v[24:31], v[186:189]
	v_mfma_f32_16x16x128_f8f6f4 v[48:51], v[8:15], v[24:31], v[190:193]
	v_mfma_f32_16x16x128_f8f6f4 v[36:39], v[0:7], v[162:169], v[194:197]
	v_mfma_f32_16x16x128_f8f6f4 v[32:35], v[8:15], v[162:169], v[198:201]
	v_mfma_f32_16x16x128_f8f6f4 v[20:23], v[0:7], v[170:177], v[202:205]
	v_mfma_f32_16x16x128_f8f6f4 v[16:19], v[8:15], v[170:177], v[206:209]
	v_mfma_f32_16x16x128_f8f6f4 v[4:7], v[0:7], v[178:185], v[210:213]
	v_mfma_f32_16x16x128_f8f6f4 v[0:3], v[8:15], v[178:185], v[214:217]
	v_mfma_f32_16x16x128_f8f6f4 v[68:71], v[146:153], v[24:31], v[218:221]
	v_mfma_f32_16x16x128_f8f6f4 v[64:67], v[154:161], v[24:31], v[222:225]
	v_mfma_f32_16x16x128_f8f6f4 v[44:47], v[146:153], v[162:169], v[226:229]
	v_mfma_f32_16x16x128_f8f6f4 v[40:43], v[154:161], v[162:169], v[230:233]
	v_mfma_f32_16x16x128_f8f6f4 v[28:31], v[146:153], v[170:177], v[234:237]
	v_mfma_f32_16x16x128_f8f6f4 v[24:27], v[154:161], v[170:177], v[238:241]
	v_mfma_f32_16x16x128_f8f6f4 v[12:15], v[146:153], v[178:185], v[242:245]
	v_mfma_f32_16x16x128_f8f6f4 v[8:11], v[154:161], v[178:185], v[246:249]
	s_barrier
	s_add_u32 s17, s26, 0x200
	s_addc_u32 s54, s27, 0
	s_mov_b32 s55, 0
.LBB0_1411:
	ds_read_b128 v[146:149], v138
	ds_read_b128 v[150:153], v138 offset:1024
	ds_read_b128 v[154:157], v138 offset:2048
	ds_read_b128 v[158:161], v138 offset:3072
	ds_read_b128 v[162:165], v139
	ds_read_b128 v[166:169], v139 offset:1024
	ds_read_b128 v[170:173], v139 offset:2048
	ds_read_b128 v[174:177], v139 offset:3072
	ds_read_b128 v[178:181], v140
	ds_read_b128 v[182:185], v140 offset:1024
	ds_read_b128 v[186:189], v140 offset:2048
	ds_read_b128 v[190:193], v140 offset:3072
	ds_read_b128 v[194:197], v140 offset:4096
	ds_read_b128 v[198:201], v140 offset:5120
	ds_read_b128 v[202:205], v140 offset:6144
	ds_read_b128 v[206:209], v140 offset:7168
	s_add_u32 s26, s6, 0x100
	s_addc_u32 s27, s7, 0
	s_cmp_eq_u32 s55, 12
	s_cselect_b32 s36, s15, s26
	s_cselect_b32 s37, s2, s27
	s_cselect_b32 s30, s18, s17
	s_cselect_b32 s31, s19, s54
	s_add_u32 s28, s36, 0x80
	s_addc_u32 s29, s37, 0
	s_add_u32 s34, s30, 0x80
	s_addc_u32 s35, s31, 0
	s_add_u32 s6, s6, 0x40080
	s_addc_u32 s7, s7, 0
	s_add_i32 m0, s47, 0xc000
	s_nop 0
	global_load_lds_dwordx4 v134, s[6:7]
	s_add_i32 m0, s47, 0xe000
	s_nop 0
	global_load_lds_dwordx4 v136, s[6:7]
	s_waitcnt vmcnt(8) lgkmcnt(0)
	s_barrier
	v_mfma_f32_16x16x128_f8f6f4 v[112:115], v[146:153], v[178:185], v[112:115]
	v_mfma_f32_16x16x128_f8f6f4 v[116:119], v[154:161], v[178:185], v[116:119]
	v_mfma_f32_16x16x128_f8f6f4 v[96:99], v[154:161], v[186:193], v[96:99]
	v_mfma_f32_16x16x128_f8f6f4 v[100:103], v[146:153], v[186:193], v[100:103]
	v_mfma_f32_16x16x128_f8f6f4 v[210:213], v[146:153], v[194:201], v[84:87]
	v_mfma_f32_16x16x128_f8f6f4 v[214:217], v[154:161], v[194:201], v[80:83]
	v_mfma_f32_16x16x128_f8f6f4 v[222:225], v[154:161], v[202:209], v[56:59]
	v_mfma_f32_16x16x128_f8f6f4 v[218:221], v[146:153], v[202:209], v[60:63]
	v_mfma_f32_16x16x128_f8f6f4 v[120:123], v[162:169], v[178:185], v[120:123]
	v_mfma_f32_16x16x128_f8f6f4 v[124:127], v[170:177], v[178:185], v[124:127]
	v_mfma_f32_16x16x128_f8f6f4 v[108:111], v[162:169], v[186:193], v[108:111]
	v_mfma_f32_16x16x128_f8f6f4 v[104:107], v[170:177], v[186:193], v[104:107]
	v_mfma_f32_16x16x128_f8f6f4 v[178:181], v[162:169], v[194:201], v[92:95]
	v_mfma_f32_16x16x128_f8f6f4 v[182:185], v[170:177], v[194:201], v[88:91]
	v_mfma_f32_16x16x128_f8f6f4 v[186:189], v[162:169], v[202:209], v[76:79]
	v_mfma_f32_16x16x128_f8f6f4 v[190:193], v[170:177], v[202:209], v[72:75]
	s_barrier
	ds_read_b128 v[56:59], v140 offset:16384
	ds_read_b128 v[60:63], v140 offset:17408
	s_nop 2
	ds_read_b128 v[72:75], v140 offset:18432
	ds_read_b128 v[76:79], v140 offset:19456
	ds_read_b128 v[80:83], v140 offset:20480
	ds_read_b128 v[84:87], v140 offset:21504
	ds_read_b128 v[88:91], v140 offset:22528
	ds_read_b128 v[92:95], v140 offset:23552
	s_add_i32 m0, s47, 0x10000
	s_nop 0
	global_load_lds_dwordx4 v135, s[30:31]
	s_add_i32 m0, s47, 0x12000
	s_nop 0
	global_load_lds_dwordx4 v137, s[30:31]
	s_add_u32 s6, s30, 0x40000
	s_addc_u32 s7, s31, 0
	s_add_i32 m0, s47, 0x14000
	s_nop 0
	global_load_lds_dwordx4 v135, s[6:7]
	s_add_i32 m0, s47, 0x16000
	s_nop 0
	global_load_lds_dwordx4 v137, s[6:7]
	s_add_i32 m0, s47, 0
	s_nop 0
	global_load_lds_dwordx4 v134, s[36:37]
	s_add_i32 m0, s47, 0x2000
	s_nop 0
	global_load_lds_dwordx4 v136, s[36:37]
	s_waitcnt vmcnt(8) lgkmcnt(0)
	s_barrier
	v_mfma_f32_16x16x128_f8f6f4 v[52:55], v[146:153], v[56:63], v[52:55]
	v_mfma_f32_16x16x128_f8f6f4 v[48:51], v[154:161], v[56:63], v[48:51]
	v_mfma_f32_16x16x128_f8f6f4 v[198:201], v[154:161], v[72:79], v[32:35]
	v_mfma_f32_16x16x128_f8f6f4 v[194:197], v[146:153], v[72:79], v[36:39]
	v_mfma_f32_16x16x128_f8f6f4 v[202:205], v[146:153], v[80:87], v[20:23]
	v_mfma_f32_16x16x128_f8f6f4 v[206:209], v[154:161], v[80:87], v[16:19]
	v_mfma_f32_16x16x128_f8f6f4 v[230:233], v[154:161], v[88:95], v[0:3]
	v_mfma_f32_16x16x128_f8f6f4 v[226:229], v[146:153], v[88:95], v[4:7]
	v_mfma_f32_16x16x128_f8f6f4 v[68:71], v[162:169], v[56:63], v[68:71]
	v_mfma_f32_16x16x128_f8f6f4 v[64:67], v[170:177], v[56:63], v[64:67]
	v_mfma_f32_16x16x128_f8f6f4 v[238:241], v[170:177], v[72:79], v[40:43]
	v_mfma_f32_16x16x128_f8f6f4 v[234:237], v[162:169], v[72:79], v[44:47]
	v_mfma_f32_16x16x128_f8f6f4 v[242:245], v[162:169], v[80:87], v[28:31]
	v_mfma_f32_16x16x128_f8f6f4 v[246:249], v[170:177], v[80:87], v[24:27]
	v_mfma_f32_16x16x128_f8f6f4 v[130:133], v[170:177], v[88:95], v[8:11]
	v_mfma_f32_16x16x128_f8f6f4 v[250:253], v[162:169], v[88:95], v[12:15]
	s_barrier
	ds_read_b128 v[0:3], v141
	ds_read_b128 v[4:7], v141 offset:1024
	s_nop 2
	ds_read_b128 v[8:11], v141 offset:2048
	ds_read_b128 v[12:15], v141 offset:3072
	ds_read_b128 v[146:149], v142
	ds_read_b128 v[150:153], v142 offset:1024
	ds_read_b128 v[154:157], v142 offset:2048
	ds_read_b128 v[158:161], v142 offset:3072
	ds_read_b128 v[16:19], v140 offset:32768
	ds_read_b128 v[20:23], v140 offset:33792
	ds_read_b128 v[24:27], v140 offset:34816
	ds_read_b128 v[28:31], v140 offset:35840
	ds_read_b128 v[32:35], v140 offset:36864
	ds_read_b128 v[36:39], v140 offset:37888
	ds_read_b128 v[40:43], v140 offset:38912
	ds_read_b128 v[44:47], v140 offset:39936
	s_add_u32 s6, s36, 0x40000
	s_addc_u32 s7, s37, 0
	s_add_i32 m0, s47, 0x4000
	s_nop 0
	global_load_lds_dwordx4 v134, s[6:7]
	s_add_i32 m0, s47, 0x6000
	s_nop 0
	global_load_lds_dwordx4 v136, s[6:7]
	s_waitcnt vmcnt(8) lgkmcnt(0)
	s_barrier
	v_mfma_f32_16x16x128_f8f6f4 v[112:115], v[0:7], v[16:23], v[112:115]
	v_mfma_f32_16x16x128_f8f6f4 v[116:119], v[8:15], v[16:23], v[116:119]
	v_mfma_f32_16x16x128_f8f6f4 v[96:99], v[8:15], v[24:31], v[96:99]
	v_mfma_f32_16x16x128_f8f6f4 v[100:103], v[0:7], v[24:31], v[100:103]
	v_mfma_f32_16x16x128_f8f6f4 v[84:87], v[0:7], v[32:39], v[210:213]
	v_mfma_f32_16x16x128_f8f6f4 v[80:83], v[8:15], v[32:39], v[214:217]
	v_mfma_f32_16x16x128_f8f6f4 v[56:59], v[8:15], v[40:47], v[222:225]
	v_mfma_f32_16x16x128_f8f6f4 v[60:63], v[0:7], v[40:47], v[218:221]
	v_mfma_f32_16x16x128_f8f6f4 v[120:123], v[146:153], v[16:23], v[120:123]
	v_mfma_f32_16x16x128_f8f6f4 v[124:127], v[154:161], v[16:23], v[124:127]
	v_mfma_f32_16x16x128_f8f6f4 v[104:107], v[154:161], v[24:31], v[104:107]
	v_mfma_f32_16x16x128_f8f6f4 v[108:111], v[146:153], v[24:31], v[108:111]
	v_mfma_f32_16x16x128_f8f6f4 v[92:95], v[146:153], v[32:39], v[178:181]
	v_mfma_f32_16x16x128_f8f6f4 v[88:91], v[154:161], v[32:39], v[182:185]
	v_mfma_f32_16x16x128_f8f6f4 v[72:75], v[154:161], v[40:47], v[190:193]
	v_mfma_f32_16x16x128_f8f6f4 v[76:79], v[146:153], v[40:47], v[186:189]
	s_barrier
	ds_read_b128 v[24:27], v140 offset:49152
	ds_read_b128 v[28:31], v140 offset:50176
	ds_read_b128 v[162:165], v140 offset:51200
	ds_read_b128 v[166:169], v140 offset:52224
	ds_read_b128 v[170:173], v140 offset:53248
	ds_read_b128 v[174:177], v140 offset:54272
	ds_read_b128 v[178:181], v140 offset:55296
	ds_read_b128 v[182:185], v140 offset:56320
	s_add_i32 m0, s47, 0x18000
	s_nop 0
	global_load_lds_dwordx4 v135, s[34:35]
	s_add_i32 m0, s47, 0x1a000
	s_nop 0
	global_load_lds_dwordx4 v137, s[34:35]
	s_add_u32 s6, s30, 0x40080
	s_addc_u32 s7, s31, 0
	s_add_i32 m0, s47, 0x1c000
	s_nop 0
	global_load_lds_dwordx4 v135, s[6:7]
	s_add_i32 m0, s47, 0x1e000
	s_nop 0
	global_load_lds_dwordx4 v137, s[6:7]
	s_add_i32 m0, s47, 0x8000
	s_nop 0
	global_load_lds_dwordx4 v134, s[28:29]
	s_add_i32 m0, s47, 0xa000
	s_nop 0
	global_load_lds_dwordx4 v136, s[28:29]
	s_waitcnt vmcnt(8) lgkmcnt(0)
	s_barrier
	v_mfma_f32_16x16x128_f8f6f4 v[52:55], v[0:7], v[24:31], v[52:55]
	v_mfma_f32_16x16x128_f8f6f4 v[48:51], v[8:15], v[24:31], v[48:51]
	v_mfma_f32_16x16x128_f8f6f4 v[36:39], v[0:7], v[162:169], v[194:197]
	v_mfma_f32_16x16x128_f8f6f4 v[32:35], v[8:15], v[162:169], v[198:201]
	v_mfma_f32_16x16x128_f8f6f4 v[20:23], v[0:7], v[170:177], v[202:205]
	v_mfma_f32_16x16x128_f8f6f4 v[16:19], v[8:15], v[170:177], v[206:209]
	v_mfma_f32_16x16x128_f8f6f4 v[4:7], v[0:7], v[178:185], v[226:229]
	v_mfma_f32_16x16x128_f8f6f4 v[0:3], v[8:15], v[178:185], v[230:233]
	v_mfma_f32_16x16x128_f8f6f4 v[68:71], v[146:153], v[24:31], v[68:71]
	v_mfma_f32_16x16x128_f8f6f4 v[64:67], v[154:161], v[24:31], v[64:67]
	v_mfma_f32_16x16x128_f8f6f4 v[44:47], v[146:153], v[162:169], v[234:237]
	v_mfma_f32_16x16x128_f8f6f4 v[40:43], v[154:161], v[162:169], v[238:241]
	v_mfma_f32_16x16x128_f8f6f4 v[28:31], v[146:153], v[170:177], v[242:245]
	v_mfma_f32_16x16x128_f8f6f4 v[24:27], v[154:161], v[170:177], v[246:249]
	v_mfma_f32_16x16x128_f8f6f4 v[12:15], v[146:153], v[178:185], v[250:253]
	v_mfma_f32_16x16x128_f8f6f4 v[8:11], v[154:161], v[178:185], v[130:133]
	s_barrier
	s_add_i32 s55, s55, 2
	s_add_u32 s17, s17, 0x100
	s_addc_u32 s54, s54, 0
	s_cmp_gt_u32 s55, 13
	s_mov_b64 s[6:7], s[26:27]
	s_cbranch_scc0 .LBB0_1411
	s_and_b64 vcc, exec, s[12:13]
	s_cbranch_vccz .LBB0_1414
	s_barrier

.LBB0_1476:
	v_bfe_i32 v3, v0, 27, 1
	v_lshlrev_b32_e32 v1, 4, v0
	v_lshrrev_b32_e32 v3, 22, v3
	v_add_u32_e32 v3, v1, v3
	v_and_b32_e32 v3, 0xfffffc00, v3
	v_sub_u32_e32 v3, v1, v3
	v_lshrrev_b32_e32 v4, 4, v3
	v_ashrrev_i32_e32 v2, 31, v0
	v_bitop3_b32 v3, v4, v3, 32 bitop3:0x6c
	v_lshrrev_b32_e32 v2, 26, v2
	v_ashrrev_i32_e32 v5, 31, v3
	v_add_u32_e32 v2, v0, v2
	v_lshrrev_b32_e32 v5, 26, v5
	v_ashrrev_i32_e32 v2, 6, v2
	v_add_u32_e32 v5, v3, v5
	v_lshlrev_b32_e32 v4, 3, v2
	v_ashrrev_i32_e32 v6, 6, v5
	v_and_b32_e32 v5, 0xc0, v5
	v_and_b32_e32 v4, -16, v4
	v_lshlrev_b32_e32 v2, 5, v2
	v_sub_u32_e32 v3, v3, v5
	v_mov_b32_e32 v5, 1
	v_add_u32_e32 v4, v6, v4
	v_and_b32_e32 v2, 32, v2
	v_ashrrev_i16_sdwa v3, v5, sext(v3) dst_sel:DWORD dst_unused:UNUSED_PAD src0_sel:DWORD src1_sel:BYTE_0
	v_add_u32_sdwa v2, v2, sext(v3) dst_sel:DWORD dst_unused:UNUSED_PAD src0_sel:DWORD src1_sel:WORD_0
	v_lshlrev_b32_e32 v3, 1, v4
	v_lshrrev_b32_e32 v7, 2, v4
	v_and_b32_e32 v6, 3, v6
	s_mov_b32 s5, 0x7fffe0
	v_and_b32_e32 v3, 24, v3
	v_and_b32_e32 v7, 4, v7
	v_and_or_b32 v6, v4, s5, v6
	v_or3_b32 v3, v6, v7, v3
	s_movk_i32 s8, 0xe00
	v_mul_lo_u32 v4, v4, s8
	v_mul_u32_u24_e32 v3, 0xe00, v3
	v_add_u32_e32 v1, 0x2000, v1
	v_add_lshl_u32 v149, v2, v4, 1
	v_add_lshl_u32 v150, v3, v2, 1
	v_ashrrev_i32_e32 v2, 31, v1
	v_lshrrev_b32_e32 v2, 22, v2
	v_add_u32_e32 v2, v1, v2
	v_ashrrev_i32_e32 v2, 10, v2
	v_mul_i32_i24_e32 v3, 0x400, v2
	v_sub_u32_e32 v1, v1, v3
	v_lshrrev_b32_e32 v3, 4, v1
	v_bitop3_b32 v1, v3, v1, 32 bitop3:0x6c
	v_ashrrev_i32_e32 v4, 31, v1
	v_lshrrev_b32_e32 v4, 26, v4
	v_add_u32_e32 v4, v1, v4
	s_add_u32 s40, s70, 0x4b800000
	v_lshlrev_b32_e32 v3, 3, v2
	v_ashrrev_i32_e32 v6, 6, v4
	v_and_b32_e32 v4, 0xc0, v4
	s_addc_u32 s41, s71, 0
	v_and_b32_e32 v3, -16, v3
	v_sub_u32_e32 v1, v1, v4
	s_add_u32 s42, s70, 0x24800000
	v_add_u32_e32 v3, v6, v3
	v_lshlrev_b32_e32 v2, 5, v2
	v_ashrrev_i16_sdwa v1, v5, sext(v1) dst_sel:DWORD dst_unused:UNUSED_PAD src0_sel:DWORD src1_sel:BYTE_0
	v_and_b32_e32 v5, 3, v6
	s_addc_u32 s43, s71, 0
	v_and_b32_e32 v2, 32, v2
	v_and_or_b32 v5, v3, s5, v5
	s_lshl_b32 s5, s17, 10
	s_ashr_i32 s18, s16, 8
	v_add_u32_sdwa v1, v2, sext(v1) dst_sel:DWORD dst_unused:UNUSED_PAD src0_sel:DWORD src1_sel:WORD_0
	v_lshlrev_b32_e32 v2, 1, v3
	v_lshrrev_b32_e32 v4, 2, v3
	v_mul_lo_u32 v3, v3, s8
	s_add_i32 s44, s5, 0
	s_mul_i32 s8, s22, 0x1c0000
	s_mul_hi_i32 s5, s22, 0x1c0000
	s_add_u32 s28, s40, s8
	s_addc_u32 s29, s41, s5
	s_add_u32 s5, s42, s6
	v_and_b32_e32 v2, 24, v2
	v_and_b32_e32 v4, 4, v4
	s_addc_u32 s6, s43, s7
	s_mul_i32 s8, s2, 0x1c0000
	v_or3_b32 v2, v5, v4, v2
	s_mul_hi_i32 s7, s2, 0x1c0000
	s_add_u32 s24, s5, s8
	v_mul_u32_u24_e32 v2, 0xe00, v2
	s_addc_u32 s25, s6, s7
	s_add_i32 m0, s44, 0x10000
	s_nop 0
	global_load_lds_dwordx4 v150, s[24:25]
	v_add_lshl_u32 v152, v2, v1, 1
	s_add_i32 m0, s44, 0x12000
	s_nop 0
	global_load_lds_dwordx4 v152, s[24:25]
	s_add_u32 s6, s24, 0xe0000
	s_addc_u32 s7, s25, 0
	s_add_i32 m0, s44, 0x14000
	s_nop 0
	global_load_lds_dwordx4 v150, s[6:7]
	v_add_lshl_u32 v151, v1, v3, 1
	s_add_i32 m0, s44, 0x16000
	s_nop 0
	global_load_lds_dwordx4 v152, s[6:7]
	s_mov_b32 s45, 0
	s_add_i32 m0, s44, 0
	s_nop 0
	global_load_lds_dwordx4 v149, s[28:29]
	s_add_i32 m0, s44, 0x2000
	s_nop 0
	global_load_lds_dwordx4 v151, s[28:29]
	s_add_u32 s6, s28, 0xe0000
	s_addc_u32 s7, s29, 0
	s_add_i32 m0, s44, 0x4000
	s_nop 0
	global_load_lds_dwordx4 v149, s[6:7]
	s_add_i32 m0, s44, 0x6000
	s_nop 0
	global_load_lds_dwordx4 v151, s[6:7]
	s_cmp_eq_u32 s18, 1
	s_cselect_b64 s[8:9], -1, 0
	s_cmp_lg_u32 s18, 1
	s_cbranch_scc1 .LBB0_1478
	s_barrier

.LBB0_1487:
	ds_read_b128 v[0:3], v153
	ds_read_b128 v[4:7], v153 offset:1024
	ds_read_b128 v[8:11], v153 offset:2048
	ds_read_b128 v[12:15], v153 offset:3072
	ds_read_b128 v[16:19], v154
	ds_read_b128 v[20:23], v154 offset:1024
	ds_read_b128 v[24:27], v154 offset:2048
	ds_read_b128 v[28:31], v154 offset:3072
	ds_read_b128 v[32:35], v155
	ds_read_b128 v[36:39], v155 offset:1024
	ds_read_b128 v[40:43], v155 offset:2048
	ds_read_b128 v[44:47], v155 offset:3072
	ds_read_b128 v[48:51], v155 offset:4096
	ds_read_b128 v[52:55], v155 offset:5120
	ds_read_b128 v[56:59], v155 offset:6144
	ds_read_b128 v[60:63], v155 offset:7168
	s_add_u32 s26, s28, 0x100
	s_addc_u32 s27, s29, 0
	s_add_u32 s36, s24, 0x100
	s_addc_u32 s37, s25, 0
	s_add_u32 s30, s28, 0x180
	s_addc_u32 s31, s29, 0
	s_add_u32 s34, s24, 0x180
	s_addc_u32 s35, s25, 0
	s_add_u32 s52, s28, 0xe0080
	s_addc_u32 s53, s29, 0
	s_add_i32 m0, s44, 0xc000
	s_nop 0
	global_load_lds_dwordx4 v149, s[52:53]
	s_add_i32 m0, s44, 0xe000
	s_nop 0
	global_load_lds_dwordx4 v151, s[52:53]
	s_waitcnt vmcnt(8) lgkmcnt(0)
	s_barrier
	v_mfma_f32_16x16x128_f8f6f4 v[64:67], v[0:7], v[32:39], 0
	v_mfma_f32_16x16x128_f8f6f4 v[68:71], v[8:15], v[32:39], 0
	v_mfma_f32_16x16x128_f8f6f4 v[76:79], v[8:15], v[40:47], 0
	v_mfma_f32_16x16x128_f8f6f4 v[72:75], v[0:7], v[40:47], 0
	v_mfma_f32_16x16x128_f8f6f4 v[80:83], v[0:7], v[48:55], 0
	v_mfma_f32_16x16x128_f8f6f4 v[88:91], v[8:15], v[48:55], 0
	v_mfma_f32_16x16x128_f8f6f4 v[104:107], v[8:15], v[56:63], 0
	v_mfma_f32_16x16x128_f8f6f4 v[92:95], v[0:7], v[56:63], 0
	v_mfma_f32_16x16x128_f8f6f4 v[108:111], v[16:23], v[32:39], 0
	v_mfma_f32_16x16x128_f8f6f4 v[124:127], v[24:31], v[32:39], 0
	v_mfma_f32_16x16x128_f8f6f4 v[162:165], v[24:31], v[40:47], 0
	v_mfma_f32_16x16x128_f8f6f4 v[158:161], v[16:23], v[40:47], 0
	v_mfma_f32_16x16x128_f8f6f4 v[166:169], v[16:23], v[48:55], 0
	v_mfma_f32_16x16x128_f8f6f4 v[170:173], v[24:31], v[48:55], 0
	v_mfma_f32_16x16x128_f8f6f4 v[178:181], v[24:31], v[56:63], 0
	v_mfma_f32_16x16x128_f8f6f4 v[174:177], v[16:23], v[56:63], 0
	s_barrier
	ds_read_b128 v[32:35], v155 offset:16384
	ds_read_b128 v[36:39], v155 offset:17408
	ds_read_b128 v[40:43], v155 offset:18432
	ds_read_b128 v[44:47], v155 offset:19456
	ds_read_b128 v[48:51], v155 offset:20480
	ds_read_b128 v[52:55], v155 offset:21504
	ds_read_b128 v[56:59], v155 offset:22528
	ds_read_b128 v[60:63], v155 offset:23552
	s_add_i32 m0, s44, 0x10000
	s_nop 0
	global_load_lds_dwordx4 v150, s[36:37]
	s_add_i32 m0, s44, 0x12000
	s_nop 0
	global_load_lds_dwordx4 v152, s[36:37]
	s_add_u32 s36, s24, 0xe0100
	s_addc_u32 s37, s25, 0
	s_add_i32 m0, s44, 0x14000
	s_nop 0
	global_load_lds_dwordx4 v150, s[36:37]
	s_add_i32 m0, s44, 0x16000
	s_nop 0
	global_load_lds_dwordx4 v152, s[36:37]
	s_add_i32 m0, s44, 0
	s_nop 0
	global_load_lds_dwordx4 v149, s[26:27]
	s_add_i32 m0, s44, 0x2000
	s_nop 0
	global_load_lds_dwordx4 v151, s[26:27]
	s_waitcnt vmcnt(8) lgkmcnt(0)
	s_barrier
	v_mfma_f32_16x16x128_f8f6f4 v[190:193], v[0:7], v[32:39], 0
	v_mfma_f32_16x16x128_f8f6f4 v[194:197], v[8:15], v[32:39], 0
	v_mfma_f32_16x16x128_f8f6f4 v[202:205], v[8:15], v[40:47], 0
	v_mfma_f32_16x16x128_f8f6f4 v[198:201], v[0:7], v[40:47], 0
	v_mfma_f32_16x16x128_f8f6f4 v[206:209], v[0:7], v[48:55], 0
	v_mfma_f32_16x16x128_f8f6f4 v[210:213], v[8:15], v[48:55], 0
	v_mfma_f32_16x16x128_f8f6f4 v[218:221], v[8:15], v[56:63], 0
	v_mfma_f32_16x16x128_f8f6f4 v[214:217], v[0:7], v[56:63], 0
	v_mfma_f32_16x16x128_f8f6f4 v[222:225], v[16:23], v[32:39], 0
	v_mfma_f32_16x16x128_f8f6f4 v[226:229], v[24:31], v[32:39], 0
	v_mfma_f32_16x16x128_f8f6f4 v[234:237], v[24:31], v[40:47], 0
	v_mfma_f32_16x16x128_f8f6f4 v[230:233], v[16:23], v[40:47], 0
	v_mfma_f32_16x16x128_f8f6f4 v[238:241], v[16:23], v[48:55], 0
	v_mfma_f32_16x16x128_f8f6f4 v[242:245], v[24:31], v[48:55], 0
	v_mfma_f32_16x16x128_f8f6f4 v[250:253], v[24:31], v[56:63], 0
	v_mfma_f32_16x16x128_f8f6f4 v[246:249], v[16:23], v[56:63], 0
	s_barrier
	ds_read_b128 v[0:3], v156
	ds_read_b128 v[4:7], v156 offset:1024
	ds_read_b128 v[16:19], v156 offset:2048
	ds_read_b128 v[20:23], v156 offset:3072
	ds_read_b128 v[132:135], v157
	ds_read_b128 v[136:139], v157 offset:1024
	ds_read_b128 v[140:143], v157 offset:2048
	ds_read_b128 v[144:147], v157 offset:3072
	ds_read_b128 v[8:11], v155 offset:32768
	ds_read_b128 v[12:15], v155 offset:33792
	ds_read_b128 v[24:27], v155 offset:34816
	ds_read_b128 v[28:31], v155 offset:35840
	ds_read_b128 v[32:35], v155 offset:36864
	ds_read_b128 v[36:39], v155 offset:37888
	ds_read_b128 v[40:43], v155 offset:38912
	ds_read_b128 v[44:47], v155 offset:39936
	s_add_u32 s28, s28, 0xe0100
	s_addc_u32 s29, s29, 0
	s_add_i32 m0, s44, 0x4000
	s_nop 0
	global_load_lds_dwordx4 v149, s[28:29]
	s_add_i32 m0, s44, 0x6000
	s_nop 0
	global_load_lds_dwordx4 v151, s[28:29]
	s_waitcnt vmcnt(8) lgkmcnt(0)
	s_barrier
	v_mfma_f32_16x16x128_f8f6f4 v[112:115], v[0:7], v[8:15], v[64:67]
	v_mfma_f32_16x16x128_f8f6f4 v[116:119], v[16:23], v[8:15], v[68:71]
	v_mfma_f32_16x16x128_f8f6f4 v[100:103], v[0:7], v[24:31], v[72:75]
	v_mfma_f32_16x16x128_f8f6f4 v[96:99], v[16:23], v[24:31], v[76:79]
	v_mfma_f32_16x16x128_f8f6f4 v[84:87], v[0:7], v[32:39], v[80:83]
	v_mfma_f32_16x16x128_f8f6f4 v[80:83], v[16:23], v[32:39], v[88:91]
	v_mfma_f32_16x16x128_f8f6f4 v[60:63], v[0:7], v[40:47], v[92:95]
	v_mfma_f32_16x16x128_f8f6f4 v[52:55], v[16:23], v[40:47], v[104:107]
	v_mfma_f32_16x16x128_f8f6f4 v[120:123], v[132:139], v[8:15], v[108:111]
	v_mfma_f32_16x16x128_f8f6f4 v[124:127], v[140:147], v[8:15], v[124:127]
	v_mfma_f32_16x16x128_f8f6f4 v[108:111], v[132:139], v[24:31], v[158:161]
	v_mfma_f32_16x16x128_f8f6f4 v[104:107], v[140:147], v[24:31], v[162:165]
	v_mfma_f32_16x16x128_f8f6f4 v[92:95], v[132:139], v[32:39], v[166:169]
	v_mfma_f32_16x16x128_f8f6f4 v[88:91], v[140:147], v[32:39], v[170:173]
	v_mfma_f32_16x16x128_f8f6f4 v[56:59], v[132:139], v[40:47], v[174:177]
	v_mfma_f32_16x16x128_f8f6f4 v[48:51], v[140:147], v[40:47], v[178:181]
	s_barrier
	ds_read_b128 v[158:161], v155 offset:49152
	ds_read_b128 v[162:165], v155 offset:50176
	ds_read_b128 v[166:169], v155 offset:51200
	ds_read_b128 v[170:173], v155 offset:52224
	ds_read_b128 v[174:177], v155 offset:53248
	ds_read_b128 v[178:181], v155 offset:54272
	ds_read_b128 v[182:185], v155 offset:55296
	ds_read_b128 v[186:189], v155 offset:56320
	s_add_i32 m0, s44, 0x18000
	s_nop 0
	global_load_lds_dwordx4 v150, s[34:35]
	s_add_i32 m0, s44, 0x1a000
	s_nop 0
	global_load_lds_dwordx4 v152, s[34:35]
	s_add_u32 s28, s24, 0xe0180
	s_addc_u32 s29, s25, 0
	s_add_i32 m0, s44, 0x1c000
	s_nop 0
	global_load_lds_dwordx4 v150, s[28:29]
	s_add_i32 m0, s44, 0x1e000
	s_nop 0
	global_load_lds_dwordx4 v152, s[28:29]
	s_add_i32 m0, s44, 0x8000
	s_nop 0
	global_load_lds_dwordx4 v149, s[30:31]
	s_add_i32 m0, s44, 0xa000
	s_nop 0
	global_load_lds_dwordx4 v151, s[30:31]
	s_waitcnt vmcnt(8) lgkmcnt(0)
	s_barrier
	v_mfma_f32_16x16x128_f8f6f4 v[68:71], v[0:7], v[158:165], v[190:193]
	v_mfma_f32_16x16x128_f8f6f4 v[64:67], v[16:23], v[158:165], v[194:197]
	v_mfma_f32_16x16x128_f8f6f4 v[36:39], v[16:23], v[166:173], v[202:205]
	v_mfma_f32_16x16x128_f8f6f4 v[44:47], v[0:7], v[166:173], v[198:201]
	v_mfma_f32_16x16x128_f8f6f4 v[28:31], v[0:7], v[174:181], v[206:209]
	v_mfma_f32_16x16x128_f8f6f4 v[24:27], v[16:23], v[174:181], v[210:213]
	v_mfma_f32_16x16x128_f8f6f4 v[8:11], v[16:23], v[182:189], v[218:221]
	v_mfma_f32_16x16x128_f8f6f4 v[12:15], v[0:7], v[182:189], v[214:217]
	v_mfma_f32_16x16x128_f8f6f4 v[76:79], v[132:139], v[158:165], v[222:225]
	v_mfma_f32_16x16x128_f8f6f4 v[72:75], v[140:147], v[158:165], v[226:229]
	v_mfma_f32_16x16x128_f8f6f4 v[32:35], v[140:147], v[166:173], v[234:237]
	v_mfma_f32_16x16x128_f8f6f4 v[40:43], v[132:139], v[166:173], v[230:233]
	v_mfma_f32_16x16x128_f8f6f4 v[20:23], v[132:139], v[174:181], v[238:241]
	v_mfma_f32_16x16x128_f8f6f4 v[16:19], v[140:147], v[174:181], v[242:245]
	v_mfma_f32_16x16x128_f8f6f4 v[0:3], v[140:147], v[182:189], v[250:253]
	v_mfma_f32_16x16x128_f8f6f4 v[4:7], v[132:139], v[182:189], v[246:249]
	s_barrier
	s_add_u32 s23, s24, 0x200
	s_addc_u32 s51, s25, 0
	s_mov_b32 s52, 0
.LBB0_1488:
	ds_read_b128 v[132:135], v153
	ds_read_b128 v[136:139], v153 offset:1024
	ds_read_b128 v[140:143], v153 offset:2048
	ds_read_b128 v[144:147], v153 offset:3072
	ds_read_b128 v[158:161], v154
	ds_read_b128 v[162:165], v154 offset:1024
	ds_read_b128 v[166:169], v154 offset:2048
	ds_read_b128 v[170:173], v154 offset:3072
	ds_read_b128 v[174:177], v155
	ds_read_b128 v[178:181], v155 offset:1024
	ds_read_b128 v[182:185], v155 offset:2048
	ds_read_b128 v[186:189], v155 offset:3072
	ds_read_b128 v[190:193], v155 offset:4096
	ds_read_b128 v[194:197], v155 offset:5120
	ds_read_b128 v[198:201], v155 offset:6144
	ds_read_b128 v[202:205], v155 offset:7168
	s_add_u32 s24, s26, 0x100
	s_addc_u32 s25, s27, 0
	s_cmp_eq_u32 s52, 52
	s_cselect_b32 s36, s6, s24
	s_cselect_b32 s37, s7, s25
	s_cselect_b32 s30, s20, s23
	s_cselect_b32 s31, s21, s51
	s_add_u32 s28, s36, 0x80
	s_addc_u32 s29, s37, 0
	s_add_u32 s34, s30, 0x80
	s_addc_u32 s35, s31, 0
	s_add_u32 s26, s26, 0xe0080
	s_addc_u32 s27, s27, 0
	s_add_i32 m0, s44, 0xc000
	s_nop 0
	global_load_lds_dwordx4 v149, s[26:27]
	s_add_i32 m0, s44, 0xe000
	s_nop 0
	global_load_lds_dwordx4 v151, s[26:27]
	s_waitcnt vmcnt(8) lgkmcnt(0)
	s_barrier
	v_mfma_f32_16x16x128_f8f6f4 v[112:115], v[132:139], v[174:181], v[112:115]
	v_mfma_f32_16x16x128_f8f6f4 v[116:119], v[140:147], v[174:181], v[116:119]
	v_mfma_f32_16x16x128_f8f6f4 v[96:99], v[140:147], v[182:189], v[96:99]
	v_mfma_f32_16x16x128_f8f6f4 v[100:103], v[132:139], v[182:189], v[100:103]
	v_mfma_f32_16x16x128_f8f6f4 v[206:209], v[132:139], v[190:197], v[84:87]
	v_mfma_f32_16x16x128_f8f6f4 v[210:213], v[140:147], v[190:197], v[80:83]
	v_mfma_f32_16x16x128_f8f6f4 v[218:221], v[140:147], v[198:205], v[52:55]
	v_mfma_f32_16x16x128_f8f6f4 v[214:217], v[132:139], v[198:205], v[60:63]
	v_mfma_f32_16x16x128_f8f6f4 v[120:123], v[158:165], v[174:181], v[120:123]
	v_mfma_f32_16x16x128_f8f6f4 v[124:127], v[166:173], v[174:181], v[124:127]
	v_mfma_f32_16x16x128_f8f6f4 v[108:111], v[158:165], v[182:189], v[108:111]
	v_mfma_f32_16x16x128_f8f6f4 v[104:107], v[166:173], v[182:189], v[104:107]
	v_mfma_f32_16x16x128_f8f6f4 v[174:177], v[158:165], v[190:197], v[92:95]
	v_mfma_f32_16x16x128_f8f6f4 v[178:181], v[166:173], v[190:197], v[88:91]
	v_mfma_f32_16x16x128_f8f6f4 v[182:185], v[158:165], v[198:205], v[56:59]
	v_mfma_f32_16x16x128_f8f6f4 v[186:189], v[166:173], v[198:205], v[48:51]
	s_barrier
	s_nop 4
	ds_read_b128 v[48:51], v155 offset:16384
	ds_read_b128 v[52:55], v155 offset:17408
	ds_read_b128 v[56:59], v155 offset:18432
	ds_read_b128 v[60:63], v155 offset:19456
	ds_read_b128 v[80:83], v155 offset:20480
	ds_read_b128 v[84:87], v155 offset:21504
	ds_read_b128 v[88:91], v155 offset:22528
	ds_read_b128 v[92:95], v155 offset:23552
	s_add_i32 m0, s44, 0x10000
	s_nop 0
	global_load_lds_dwordx4 v150, s[30:31]
	s_add_i32 m0, s44, 0x12000
	s_nop 0
	global_load_lds_dwordx4 v152, s[30:31]
	s_add_u32 s26, s30, 0xe0000
	s_addc_u32 s27, s31, 0
	s_add_i32 m0, s44, 0x14000
	s_nop 0
	global_load_lds_dwordx4 v150, s[26:27]
	s_add_i32 m0, s44, 0x16000
	s_nop 0
	global_load_lds_dwordx4 v152, s[26:27]
	s_add_i32 m0, s44, 0
	s_nop 0
	global_load_lds_dwordx4 v149, s[36:37]
	s_add_i32 m0, s44, 0x2000
	s_nop 0
	global_load_lds_dwordx4 v151, s[36:37]
	s_waitcnt vmcnt(8) lgkmcnt(0)
	s_barrier
	v_mfma_f32_16x16x128_f8f6f4 v[68:71], v[132:139], v[48:55], v[68:71]
	v_mfma_f32_16x16x128_f8f6f4 v[64:67], v[140:147], v[48:55], v[64:67]
	v_mfma_f32_16x16x128_f8f6f4 v[194:197], v[140:147], v[56:63], v[36:39]
	v_mfma_f32_16x16x128_f8f6f4 v[190:193], v[132:139], v[56:63], v[44:47]
	v_mfma_f32_16x16x128_f8f6f4 v[198:201], v[132:139], v[80:87], v[28:31]
	v_mfma_f32_16x16x128_f8f6f4 v[202:205], v[140:147], v[80:87], v[24:27]
	v_mfma_f32_16x16x128_f8f6f4 v[226:229], v[140:147], v[88:95], v[8:11]
	v_mfma_f32_16x16x128_f8f6f4 v[222:225], v[132:139], v[88:95], v[12:15]
	v_mfma_f32_16x16x128_f8f6f4 v[76:79], v[158:165], v[48:55], v[76:79]
	v_mfma_f32_16x16x128_f8f6f4 v[72:75], v[166:173], v[48:55], v[72:75]
	v_mfma_f32_16x16x128_f8f6f4 v[234:237], v[166:173], v[56:63], v[32:35]
	v_mfma_f32_16x16x128_f8f6f4 v[230:233], v[158:165], v[56:63], v[40:43]
	v_mfma_f32_16x16x128_f8f6f4 v[238:241], v[158:165], v[80:87], v[20:23]
	v_mfma_f32_16x16x128_f8f6f4 v[242:245], v[166:173], v[80:87], v[16:19]
	v_mfma_f32_16x16x128_f8f6f4 v[250:253], v[166:173], v[88:95], v[0:3]
	v_mfma_f32_16x16x128_f8f6f4 v[246:249], v[158:165], v[88:95], v[4:7]
	s_barrier
	s_nop 4
	ds_read_b128 v[0:3], v156
	ds_read_b128 v[4:7], v156 offset:1024
	ds_read_b128 v[16:19], v156 offset:2048
	ds_read_b128 v[20:23], v156 offset:3072
	ds_read_b128 v[132:135], v157
	ds_read_b128 v[136:139], v157 offset:1024
	ds_read_b128 v[140:143], v157 offset:2048
	ds_read_b128 v[144:147], v157 offset:3072
	ds_read_b128 v[8:11], v155 offset:32768
	ds_read_b128 v[12:15], v155 offset:33792
	ds_read_b128 v[24:27], v155 offset:34816
	ds_read_b128 v[28:31], v155 offset:35840
	ds_read_b128 v[32:35], v155 offset:36864
	ds_read_b128 v[36:39], v155 offset:37888
	ds_read_b128 v[40:43], v155 offset:38912
	ds_read_b128 v[44:47], v155 offset:39936
	s_add_u32 s26, s36, 0xe0000
	s_addc_u32 s27, s37, 0
	s_add_i32 m0, s44, 0x4000
	s_nop 0
	global_load_lds_dwordx4 v149, s[26:27]
	s_add_i32 m0, s44, 0x6000
	s_nop 0
	global_load_lds_dwordx4 v151, s[26:27]
	s_waitcnt vmcnt(8) lgkmcnt(0)
	s_barrier
	v_mfma_f32_16x16x128_f8f6f4 v[112:115], v[0:7], v[8:15], v[112:115]
	v_mfma_f32_16x16x128_f8f6f4 v[116:119], v[16:23], v[8:15], v[116:119]
	v_mfma_f32_16x16x128_f8f6f4 v[96:99], v[16:23], v[24:31], v[96:99]
	v_mfma_f32_16x16x128_f8f6f4 v[100:103], v[0:7], v[24:31], v[100:103]
	v_mfma_f32_16x16x128_f8f6f4 v[84:87], v[0:7], v[32:39], v[206:209]
	v_mfma_f32_16x16x128_f8f6f4 v[80:83], v[16:23], v[32:39], v[210:213]
	v_mfma_f32_16x16x128_f8f6f4 v[52:55], v[16:23], v[40:47], v[218:221]
	v_mfma_f32_16x16x128_f8f6f4 v[60:63], v[0:7], v[40:47], v[214:217]
	v_mfma_f32_16x16x128_f8f6f4 v[120:123], v[132:139], v[8:15], v[120:123]
	v_mfma_f32_16x16x128_f8f6f4 v[124:127], v[140:147], v[8:15], v[124:127]
	v_mfma_f32_16x16x128_f8f6f4 v[104:107], v[140:147], v[24:31], v[104:107]
	v_mfma_f32_16x16x128_f8f6f4 v[108:111], v[132:139], v[24:31], v[108:111]
	v_mfma_f32_16x16x128_f8f6f4 v[92:95], v[132:139], v[32:39], v[174:177]
	v_mfma_f32_16x16x128_f8f6f4 v[88:91], v[140:147], v[32:39], v[178:181]
	v_mfma_f32_16x16x128_f8f6f4 v[48:51], v[140:147], v[40:47], v[186:189]
	v_mfma_f32_16x16x128_f8f6f4 v[56:59], v[132:139], v[40:47], v[182:185]
	s_barrier
	ds_read_b128 v[158:161], v155 offset:49152
	ds_read_b128 v[162:165], v155 offset:50176
	ds_read_b128 v[166:169], v155 offset:51200
	ds_read_b128 v[170:173], v155 offset:52224
	ds_read_b128 v[174:177], v155 offset:53248
	ds_read_b128 v[178:181], v155 offset:54272
	ds_read_b128 v[182:185], v155 offset:55296
	ds_read_b128 v[186:189], v155 offset:56320
	s_add_i32 m0, s44, 0x18000
	s_nop 0
	global_load_lds_dwordx4 v150, s[34:35]
	s_add_i32 m0, s44, 0x1a000
	s_nop 0
	global_load_lds_dwordx4 v152, s[34:35]
	s_add_u32 s26, s30, 0xe0080
	s_addc_u32 s27, s31, 0
	s_add_i32 m0, s44, 0x1c000
	s_nop 0
	global_load_lds_dwordx4 v150, s[26:27]
	s_add_i32 m0, s44, 0x1e000
	s_nop 0
	global_load_lds_dwordx4 v152, s[26:27]
	s_add_i32 m0, s44, 0x8000
	s_nop 0
	global_load_lds_dwordx4 v149, s[28:29]
	s_add_i32 m0, s44, 0xa000
	s_nop 0
	global_load_lds_dwordx4 v151, s[28:29]
	s_waitcnt vmcnt(8) lgkmcnt(0)
	s_barrier
	v_mfma_f32_16x16x128_f8f6f4 v[68:71], v[0:7], v[158:165], v[68:71]
	v_mfma_f32_16x16x128_f8f6f4 v[64:67], v[16:23], v[158:165], v[64:67]
	v_mfma_f32_16x16x128_f8f6f4 v[36:39], v[16:23], v[166:173], v[194:197]
	v_mfma_f32_16x16x128_f8f6f4 v[44:47], v[0:7], v[166:173], v[190:193]
	v_mfma_f32_16x16x128_f8f6f4 v[28:31], v[0:7], v[174:181], v[198:201]
	v_mfma_f32_16x16x128_f8f6f4 v[24:27], v[16:23], v[174:181], v[202:205]
	v_mfma_f32_16x16x128_f8f6f4 v[8:11], v[16:23], v[182:189], v[226:229]
	v_mfma_f32_16x16x128_f8f6f4 v[12:15], v[0:7], v[182:189], v[222:225]
	v_mfma_f32_16x16x128_f8f6f4 v[76:79], v[132:139], v[158:165], v[76:79]
	v_mfma_f32_16x16x128_f8f6f4 v[72:75], v[140:147], v[158:165], v[72:75]
	v_mfma_f32_16x16x128_f8f6f4 v[32:35], v[140:147], v[166:173], v[234:237]
	v_mfma_f32_16x16x128_f8f6f4 v[40:43], v[132:139], v[166:173], v[230:233]
	v_mfma_f32_16x16x128_f8f6f4 v[20:23], v[132:139], v[174:181], v[238:241]
	v_mfma_f32_16x16x128_f8f6f4 v[16:19], v[140:147], v[174:181], v[242:245]
	v_mfma_f32_16x16x128_f8f6f4 v[0:3], v[140:147], v[182:189], v[250:253]
	v_mfma_f32_16x16x128_f8f6f4 v[4:7], v[132:139], v[182:189], v[246:249]
	s_barrier
	s_add_i32 s52, s52, 2
	s_add_u32 s23, s23, 0x100
	s_addc_u32 s51, s51, 0
	s_cmp_gt_u32 s52, 53
	s_mov_b64 s[26:27], s[24:25]
	s_cbranch_scc0 .LBB0_1488
	s_and_b64 vcc, exec, s[16:17]
	s_cbranch_vccz .LBB0_1491
	s_barrier
